# speedup vs baseline: 1.0208x; 1.0208x over previous
.LBB0_4:
	s_load_dwordx8 s[4:11], s[0:1], 0x20
	v_lshrrev_b32_e32 v1, 5, v0
	v_lshlrev_b32_e32 v0, 2, v0
	s_lshl_b32 s0, s2, 3
	v_and_b32_e32 v50, 0xfc, v0
	s_addk_i32 s0, 0xf280
	v_lshlrev_b32_e32 v24, 2, v50
	v_mov_b32_e32 v25, 0
	v_and_or_b32 v45, v1, 6, s0
	s_waitcnt lgkmcnt(0)
	v_lshl_add_u64 v[4:5], s[4:5], 0, v[24:25]
	s_movk_i32 s2, 0xc00
	v_mad_i64_i32 v[6:7], s[0:1], v45, s2, v[4:5]
	global_load_dwordx4 v[16:19], v[6:7], off nt
	global_load_dwordx4 v[20:23], v[6:7], off offset:1024 nt
	global_load_dwordx4 v[0:3], v[6:7], off offset:2048 nt
	v_mbcnt_lo_u32_b32 v6, -1, 0
	v_mbcnt_hi_u32_b32 v30, -1, v6
	v_and_b32_e32 v6, 64, v30
	v_mov_b32_e32 v8, v25
	v_xor_b32_e32 v7, 32, v30
	v_add_u32_e32 v33, 64, v6
	v_cmp_lt_i32_e32 vcc, v7, v33
	v_or_b32_e32 v52, 1, v45
	v_xor_b32_e32 v31, 16, v30
	v_cndmask_b32_e32 v6, v30, v7, vcc
	v_lshlrev_b32_e32 v53, 2, v6
	v_mad_i64_i32 v[10:11], s[0:1], v52, s2, v[4:5]
	v_xor_b32_e32 v32, 8, v30
	global_load_dwordx4 v[4:7], v[10:11], off nt
	v_cmp_lt_i32_e32 vcc, v31, v33
	v_mov_b32_e32 v59, 0x3727c5ac
	s_mov_b32 s2, 0xf800000
	v_mov_b32_e32 v60, 0x260
	s_movk_i32 s3, 0x600
	s_waitcnt vmcnt(3)
	v_mov_b32_e32 v12, v17
	v_mov_b32_e32 v13, v18
	v_mov_b32_e32 v14, v16
	v_mov_b32_e32 v15, v19
	v_pk_add_f32 v[12:13], v[12:13], v[14:15]
	s_waitcnt vmcnt(2)
	v_add_f32_e32 v26, v20, v21
	v_pk_add_f32 v[12:13], v[12:13], v[12:13] op_sel:[0,1] op_sel_hi:[1,0]
	v_add_f32_e32 v28, v22, v23
	s_waitcnt vmcnt(1)
	v_mov_b32_e32 v9, v1
	v_mov_b32_e32 v27, v2
	v_mov_b32_e32 v29, v3
	v_mov_b32_e32 v13, v0
	v_pk_add_f32 v[14:15], v[26:27], v[28:29]
	v_pk_add_f32 v[8:9], v[12:13], v[8:9]
	v_cndmask_b32_e32 v12, v30, v31, vcc
	v_pk_add_f32 v[8:9], v[8:9], v[14:15]
	v_cmp_lt_i32_e32 vcc, v32, v33
	v_add_f32_e32 v8, v8, v9
	ds_bpermute_b32 v9, v53, v8
	v_lshlrev_b32_e32 v54, 2, v12
	global_load_dwordx4 v[12:15], v[10:11], off offset:1024 nt
	v_xor_b32_e32 v28, 4, v30
	s_waitcnt lgkmcnt(0)
	v_add_f32_e32 v26, v8, v9
	v_cndmask_b32_e32 v8, v30, v32, vcc
	v_lshlrev_b32_e32 v55, 2, v8
	global_load_dwordx4 v[8:11], v[10:11], off offset:2048 nt
	ds_bpermute_b32 v27, v54, v26
	v_cmp_lt_i32_e32 vcc, v28, v33
	s_waitcnt lgkmcnt(0)
	v_add_f32_e32 v26, v26, v27
	ds_bpermute_b32 v27, v55, v26
	v_cndmask_b32_e32 v28, v30, v28, vcc
	v_lshlrev_b32_e32 v56, 2, v28
	v_xor_b32_e32 v28, 2, v30
	v_cmp_lt_i32_e32 vcc, v28, v33
	s_waitcnt lgkmcnt(0)
	v_add_f32_e32 v26, v26, v27
	ds_bpermute_b32 v27, v56, v26
	v_cndmask_b32_e32 v28, v30, v28, vcc
	v_lshlrev_b32_e32 v57, 2, v28
	v_xor_b32_e32 v28, 1, v30
	v_cmp_lt_i32_e32 vcc, v28, v33
	s_waitcnt lgkmcnt(0)
	v_add_f32_e32 v26, v26, v27
	ds_bpermute_b32 v27, v57, v26
	v_cndmask_b32_e32 v28, v30, v28, vcc
	v_lshlrev_b32_e32 v58, 2, v28
	s_waitcnt lgkmcnt(0)
	v_add_f32_e32 v26, v26, v27
	ds_bpermute_b32 v27, v58, v26
	s_waitcnt lgkmcnt(0)
	v_add_f32_e32 v26, v26, v27
	v_fmamk_f32 v34, v26, 0xbaaaaaab, v16
	v_fmac_f32_e32 v18, 0xbaaaaaab, v26
	v_fmamk_f32 v36, v26, 0xbaaaaaab, v20
	v_fmac_f32_e32 v22, 0xbaaaaaab, v26
	v_fmamk_f32 v35, v26, 0xbaaaaaab, v17
	v_fmamk_f32 v19, v26, 0xbaaaaaab, v19
	v_fmamk_f32 v37, v26, 0xbaaaaaab, v21
	v_fmamk_f32 v23, v26, 0xbaaaaaab, v23
	v_fmamk_f32 v3, v26, 0xbaaaaaab, v3
	v_fmamk_f32 v2, v26, 0xbaaaaaab, v2
	v_fmamk_f32 v1, v26, 0xbaaaaaab, v1
	v_fmac_f32_e32 v0, 0xbaaaaaab, v26
	v_mul_f32_e32 v16, v34, v34
	v_mul_f32_e32 v20, v18, v18
	v_mul_f32_e32 v26, v36, v36
	v_mul_f32_e32 v28, v22, v22
	v_pk_fma_f32 v[16:17], v[34:35], v[34:35], v[16:17] op_sel_hi:[1,1,0]
	v_pk_fma_f32 v[20:21], v[18:19], v[18:19], v[20:21] op_sel_hi:[1,1,0]
	v_pk_fma_f32 v[26:27], v[36:37], v[36:37], v[26:27] op_sel_hi:[1,1,0]
	v_pk_fma_f32 v[28:29], v[22:23], v[22:23], v[28:29] op_sel_hi:[1,1,0]
	v_mul_f32_e32 v16, v0, v0
	v_mul_f32_e32 v20, v1, v1
	v_mul_f32_e32 v26, v2, v2
	v_mul_f32_e32 v28, v3, v3
	v_pk_add_f32 v[16:17], v[16:17], v[20:21]
	v_pk_add_f32 v[20:21], v[26:27], v[28:29]
	s_waitcnt vmcnt(2)
	v_mov_b32_e32 v26, v4
	v_pk_add_f32 v[16:17], v[16:17], v[20:21]
	v_mov_b32_e32 v20, v5
	v_add_f32_e32 v16, v16, v17
	ds_bpermute_b32 v17, v53, v16
	v_mov_b32_e32 v27, v7
	s_waitcnt lgkmcnt(0)
	v_add_f32_e32 v16, v16, v17
	ds_bpermute_b32 v17, v54, v16
	s_waitcnt lgkmcnt(0)
	v_add_f32_e32 v17, v16, v17
	ds_bpermute_b32 v21, v55, v17
	v_mov_b32_e32 v16, v25
	s_waitcnt vmcnt(1)
	v_add_f32_e32 v28, v12, v13
	v_add_f32_e32 v30, v14, v15
	s_waitcnt lgkmcnt(0)
	v_add_f32_e32 v17, v17, v21
	ds_bpermute_b32 v29, v56, v17
	v_mov_b32_e32 v21, v6
	v_pk_add_f32 v[20:21], v[20:21], v[26:27]
	s_waitcnt vmcnt(0)
	v_mov_b32_e32 v31, v11
	v_pk_add_f32 v[20:21], v[20:21], v[20:21] op_sel:[0,1] op_sel_hi:[1,0]
	s_waitcnt lgkmcnt(0)
	v_add_f32_e32 v17, v17, v29
	ds_bpermute_b32 v32, v57, v17
	v_mov_b32_e32 v21, v8
	v_mov_b32_e32 v29, v10
	v_pk_add_f32 v[38:39], v[28:29], v[30:31]
	s_waitcnt lgkmcnt(0)
	v_add_f32_e32 v40, v17, v32
	ds_bpermute_b32 v41, v58, v40
	v_mov_b32_e32 v17, v9
	v_pk_add_f32 v[16:17], v[20:21], v[16:17]
	global_load_dwordx4 v[26:29], v24, s[6:7]
	global_load_dwordx4 v[30:33], v24, s[8:9]
	s_waitcnt lgkmcnt(0)
	v_add_f32_e32 v40, v40, v41
	v_fmamk_f32 v40, v40, 0x3aaaaaab, v59
	v_mul_f32_e32 v41, 0x4f800000, v40
	v_cmp_gt_f32_e32 vcc, s2, v40
	s_nop 1
	v_cndmask_b32_e32 v40, v40, v41, vcc
	v_sqrt_f32_e32 v41, v40
	s_nop 0
	v_add_u32_e32 v20, -1, v41
	v_add_u32_e32 v21, 1, v41
	v_fma_f32 v42, -v20, v41, v40
	v_cmp_ge_f32_e64 s[0:1], 0, v42
	v_fma_f32 v42, -v21, v41, v40
	s_nop 0
	v_cndmask_b32_e64 v20, v41, v20, s[0:1]
	v_cmp_lt_f32_e64 s[0:1], 0, v42
	v_pk_add_f32 v[42:43], v[16:17], v[38:39]
	s_nop 0
	v_cndmask_b32_e64 v20, v20, v21, s[0:1]
	v_mul_f32_e32 v21, 0x37800000, v20
	v_cndmask_b32_e32 v20, v20, v21, vcc
	v_cmp_class_f32_e32 vcc, v40, v60
	v_add_f32_e32 v42, v42, v43
	ds_bpermute_b32 v43, v53, v42
	v_cndmask_b32_e32 v20, v20, v40, vcc
	v_div_scale_f32 v21, s[0:1], v20, v20, 1.0
	v_rcp_f32_e32 v40, v21
	v_div_scale_f32 v16, vcc, 1.0, v20, 1.0
	s_waitcnt lgkmcnt(0)
	v_add_f32_e32 v42, v42, v43
	v_fma_f32 v17, -v21, v40, 1.0
	v_fmac_f32_e32 v40, v17, v40
	v_mul_f32_e32 v17, v16, v40
	v_fma_f32 v38, -v21, v17, v16
	v_fmac_f32_e32 v17, v38, v40
	v_fma_f32 v16, -v21, v17, v16
	v_div_fmas_f32 v16, v16, v40, v17
	v_div_fixup_f32 v44, v16, v20, 1.0
	v_pk_mul_f32 v[38:39], v[18:19], v[44:45] op_sel_hi:[1,0]
	v_pk_mul_f32 v[40:41], v[22:23], v[44:45] op_sel_hi:[1,0]
	global_load_dwordx4 v[16:19], v24, s[6:7] offset:1024
	global_load_dwordx4 v[20:23], v24, s[8:9] offset:1024
	ds_bpermute_b32 v43, v54, v42
	v_pk_mul_f32 v[34:35], v[34:35], v[44:45] op_sel_hi:[1,0]
	v_pk_mul_f32 v[36:37], v[36:37], v[44:45] op_sel_hi:[1,0]
	s_waitcnt lgkmcnt(0)
	v_add_f32_e32 v42, v42, v43
	ds_bpermute_b32 v43, v55, v42
	s_waitcnt lgkmcnt(0)
	v_add_f32_e32 v42, v42, v43
	ds_bpermute_b32 v43, v56, v42
	s_waitcnt lgkmcnt(0)
	v_add_f32_e32 v42, v42, v43
	ds_bpermute_b32 v43, v57, v42
	s_waitcnt lgkmcnt(0)
	v_add_f32_e32 v42, v42, v43
	ds_bpermute_b32 v43, v58, v42
	s_waitcnt vmcnt(2)
	v_pk_fma_f32 v[38:39], v[28:29], v[38:39], v[32:33]
	v_pk_fma_f32 v[34:35], v[26:27], v[34:35], v[30:31]
	v_cvt_pk_f16_f32 v47, v38, v39
	v_cvt_pk_f16_f32 v46, v34, v35
	s_waitcnt vmcnt(0)
	v_pk_fma_f32 v[40:41], v[18:19], v[40:41], v[22:23]
	v_pk_fma_f32 v[36:37], v[16:17], v[36:37], v[20:21]
	v_cvt_pk_f16_f32 v49, v40, v41
	v_cvt_pk_f16_f32 v48, v36, v37
	global_load_dwordx4 v[34:37], v24, s[6:7] offset:2048
	global_load_dwordx4 v[38:41], v24, s[8:9] offset:2048
	v_lshlrev_b32_e32 v24, 1, v50
	v_lshl_add_u64 v[24:25], s[10:11], 0, v[24:25]
	v_mad_i64_i32 v[50:51], s[0:1], v45, s3, v[24:25]
	s_waitcnt lgkmcnt(0)
	v_add_f32_e32 v45, v42, v43
	v_fmamk_f32 v4, v45, 0xbaaaaaab, v4
	v_fmamk_f32 v5, v45, 0xbaaaaaab, v5
	v_mul_f32_e32 v42, v4, v4
	v_fmac_f32_e32 v6, 0xbaaaaaab, v45
	v_pk_fma_f32 v[42:43], v[4:5], v[4:5], v[42:43] op_sel_hi:[1,1,0]
	v_fmamk_f32 v7, v45, 0xbaaaaaab, v7
	v_mul_f32_e32 v42, v6, v6
	global_store_dwordx2 v[50:51], v[46:47], off
	v_pk_fma_f32 v[46:47], v[6:7], v[6:7], v[42:43] op_sel_hi:[1,1,0]
	v_fmamk_f32 v9, v45, 0xbaaaaaab, v9
	v_fmac_f32_e32 v8, 0xbaaaaaab, v45
	v_mul_f32_e32 v42, v8, v8
	v_mul_f32_e32 v46, v9, v9
	v_fmamk_f32 v12, v45, 0xbaaaaaab, v12
	v_pk_add_f32 v[42:43], v[42:43], v[46:47]
	v_fmamk_f32 v13, v45, 0xbaaaaaab, v13
	v_mul_f32_e32 v46, v12, v12
	v_fmac_f32_e32 v14, 0xbaaaaaab, v45
	v_pk_fma_f32 v[46:47], v[12:13], v[12:13], v[46:47] op_sel_hi:[1,1,0]
	v_fmamk_f32 v15, v45, 0xbaaaaaab, v15
	v_mul_f32_e32 v46, v14, v14
	global_store_dwordx2 v[50:51], v[48:49], off offset:512
	v_fmamk_f32 v11, v45, 0xbaaaaaab, v11
	v_fmamk_f32 v10, v45, 0xbaaaaaab, v10
	v_pk_fma_f32 v[48:49], v[14:15], v[14:15], v[46:47] op_sel_hi:[1,1,0]
	v_mul_f32_e32 v46, v10, v10
	v_mul_f32_e32 v48, v11, v11
	v_pk_add_f32 v[46:47], v[46:47], v[48:49]
	v_pk_mul_f32 v[0:1], v[0:1], v[44:45] op_sel_hi:[1,0]
	v_pk_add_f32 v[42:43], v[42:43], v[46:47]
	v_pk_mul_f32 v[2:3], v[2:3], v[44:45] op_sel_hi:[1,0]
	v_add_f32_e32 v42, v42, v43
	ds_bpermute_b32 v43, v53, v42
	s_waitcnt lgkmcnt(0)
	v_add_f32_e32 v42, v42, v43
	ds_bpermute_b32 v43, v54, v42
	s_waitcnt lgkmcnt(0)
	v_add_f32_e32 v42, v42, v43
	ds_bpermute_b32 v43, v55, v42
	s_waitcnt lgkmcnt(0)
	v_add_f32_e32 v42, v42, v43
	ds_bpermute_b32 v43, v56, v42
	s_waitcnt lgkmcnt(0)
	v_add_f32_e32 v42, v42, v43
	ds_bpermute_b32 v43, v57, v42
	s_waitcnt lgkmcnt(0)
	v_add_f32_e32 v42, v42, v43
	ds_bpermute_b32 v43, v58, v42
	s_waitcnt lgkmcnt(0)
	v_add_f32_e32 v42, v42, v43
	v_fmac_f32_e32 v59, 0x3aaaaaab, v42
	v_mul_f32_e32 v42, 0x4f800000, v59
	v_cmp_gt_f32_e32 vcc, s2, v59
	s_waitcnt vmcnt(2)
	v_pk_fma_f32 v[2:3], v[36:37], v[2:3], v[40:41]
	v_cndmask_b32_e32 v42, v59, v42, vcc
	v_sqrt_f32_e32 v43, v42
	v_pk_fma_f32 v[0:1], v[34:35], v[0:1], v[38:39]
	v_add_u32_e32 v44, -1, v43
	v_fma_f32 v45, -v44, v43, v42
	v_cmp_ge_f32_e64 s[0:1], 0, v45
	v_add_u32_e32 v45, 1, v43
	v_cvt_pk_f16_f32 v0, v0, v1
	v_cndmask_b32_e64 v44, v43, v44, s[0:1]
	v_fma_f32 v43, -v45, v43, v42
	v_cmp_lt_f32_e64 s[0:1], 0, v43
	v_cvt_pk_f16_f32 v1, v2, v3
	global_store_dwordx2 v[50:51], v[0:1], off offset:1024
	v_cndmask_b32_e64 v43, v44, v45, s[0:1]
	v_mul_f32_e32 v44, 0x37800000, v43
	v_cndmask_b32_e32 v43, v43, v44, vcc
	v_cmp_class_f32_e32 vcc, v42, v60
	s_nop 1
	v_cndmask_b32_e32 v42, v43, v42, vcc
	v_div_scale_f32 v43, s[0:1], v42, v42, 1.0
	v_rcp_f32_e32 v44, v43
	s_nop 0
	v_fma_f32 v0, -v43, v44, 1.0
	v_fmac_f32_e32 v44, v0, v44
	v_div_scale_f32 v0, vcc, 1.0, v42, 1.0
	v_mul_f32_e32 v1, v0, v44
	v_fma_f32 v2, -v43, v1, v0
	v_fmac_f32_e32 v1, v2, v44
	v_fma_f32 v0, -v43, v1, v0
	v_div_fmas_f32 v0, v0, v44, v1
	v_div_fixup_f32 v0, v0, v42, 1.0
	v_pk_mul_f32 v[4:5], v[4:5], v[0:1] op_sel_hi:[1,0]
	v_pk_mul_f32 v[6:7], v[6:7], v[0:1] op_sel_hi:[1,0]
	v_pk_fma_f32 v[4:5], v[26:27], v[4:5], v[30:31]
	v_pk_fma_f32 v[6:7], v[28:29], v[6:7], v[32:33]
	v_mad_i64_i32 v[2:3], s[0:1], v52, s3, v[24:25]
	v_cvt_pk_f16_f32 v4, v4, v5
	v_cvt_pk_f16_f32 v5, v6, v7
	global_store_dwordx2 v[2:3], v[4:5], off
	v_pk_mul_f32 v[4:5], v[12:13], v[0:1] op_sel_hi:[1,0]
	v_pk_mul_f32 v[6:7], v[14:15], v[0:1] op_sel_hi:[1,0]
	v_pk_fma_f32 v[4:5], v[16:17], v[4:5], v[20:21]
	v_pk_fma_f32 v[6:7], v[18:19], v[6:7], v[22:23]
	v_cvt_pk_f16_f32 v4, v4, v5
	v_cvt_pk_f16_f32 v5, v6, v7
	global_store_dwordx2 v[2:3], v[4:5], off offset:512
	v_pk_mul_f32 v[4:5], v[8:9], v[0:1] op_sel_hi:[1,0]
	v_pk_mul_f32 v[0:1], v[10:11], v[0:1] op_sel_hi:[1,0]
	v_pk_fma_f32 v[4:5], v[34:35], v[4:5], v[38:39]
	v_pk_fma_f32 v[0:1], v[36:37], v[0:1], v[40:41]
	v_cvt_pk_f16_f32 v4, v4, v5
	v_cvt_pk_f16_f32 v5, v0, v1
	global_store_dwordx2 v[2:3], v[4:5], off offset:1024
	s_endpgm
	.p2align	8

.LBB1_6:
	v_add_u32_e32 v50, s35, v216
	ds_read_b64_tr_b16 v[190:191], v50 offset:24576
	ds_read_b64_tr_b16 v[192:193], v50 offset:25088
	s_waitcnt lgkmcnt(9)
	v_mfma_f32_32x32x16_f16 v[130:145], v[118:121], v[174:177], v[34:49]
	v_add_f32_e32 v51, v98, v99
	v_add_f32_e32 v51, v100, v51
	v_add_f32_e32 v51, v101, v51
	v_add_f32_e32 v51, v102, v51
	v_add_f32_e32 v51, v103, v51
	v_cvt_pkrtz_f16_f32 v158, v98, v99
	v_cvt_pkrtz_f16_f32 v159, v100, v101
	ds_read_b64_tr_b16 v[182:183], v50 offset:28672
	ds_read_b64_tr_b16 v[184:185], v50 offset:29184
	s_waitcnt lgkmcnt(10)
	v_mfma_f32_32x32x16_f16 v[114:129], v[178:181], v[174:177], v[34:49]
	v_add_f32_e32 v51, v104, v51
	v_add_f32_e32 v51, v105, v51
	v_add_f32_e32 v51, v106, v51
	v_add_f32_e32 v51, v107, v51
	v_cvt_pkrtz_f16_f32 v160, v102, v103
	v_cvt_pkrtz_f16_f32 v161, v104, v105
	ds_read_b64_tr_b16 v[178:179], v50 offset:25600
	ds_read_b64_tr_b16 v[180:181], v50 offset:26112
	s_waitcnt lgkmcnt(11)
	v_mfma_f32_32x32x16_f16 v[130:145], v[186:189], v[170:173], v[130:145]
	v_add_f32_e32 v51, v108, v51
	v_add_f32_e32 v51, v109, v51
	v_add_f32_e32 v51, v110, v51
	v_add_f32_e32 v51, v111, v51
	v_cvt_pkrtz_f16_f32 v154, v106, v107
	v_cvt_pkrtz_f16_f32 v155, v108, v109
	ds_read_b64_tr_b16 v[186:187], v50 offset:29696
	ds_read_b64_tr_b16 v[188:189], v50 offset:30208
	s_waitcnt lgkmcnt(12)
	v_mfma_f32_32x32x16_f16 v[114:129], v[78:81], v[170:173], v[114:129]
	v_add_f32_e32 v51, v112, v51
	v_add_f32_e32 v51, v113, v51
	v_add_f32_e32 v51, v82, v51
	v_add_f32_e32 v51, v83, v51
	v_cvt_pkrtz_f16_f32 v156, v110, v111
	v_cvt_pkrtz_f16_f32 v157, v112, v113
	ds_read_b64_tr_b16 v[110:111], v50 offset:26624
	ds_read_b64_tr_b16 v[112:113], v50 offset:27136
	s_waitcnt lgkmcnt(13)
	v_mfma_f32_32x32x16_f16 v[130:145], v[74:77], v[166:169], v[130:145]
	v_add_f32_e32 v51, v84, v51
	v_add_f32_e32 v51, v85, v51
	v_add_f32_e32 v51, v86, v51
	v_add_f32_e32 v51, v87, v51
	v_cvt_pkrtz_f16_f32 v150, v82, v83
	v_cvt_pkrtz_f16_f32 v151, v84, v85
	ds_read_b64_tr_b16 v[106:107], v50 offset:30720
	ds_read_b64_tr_b16 v[108:109], v50 offset:31232
	s_waitcnt lgkmcnt(14)
	v_mfma_f32_32x32x16_f16 v[114:129], v[62:65], v[166:169], v[114:129]
	v_add_f32_e32 v51, v88, v51
	v_add_f32_e32 v51, v89, v51
	v_add_f32_e32 v51, v90, v51
	v_add_f32_e32 v51, v91, v51
	v_cvt_pkrtz_f16_f32 v152, v86, v87
	v_cvt_pkrtz_f16_f32 v153, v88, v89
	ds_read_b64_tr_b16 v[102:103], v50 offset:27648
	ds_read_b64_tr_b16 v[104:105], v50 offset:28160
	s_waitcnt lgkmcnt(14)
	v_mfma_f32_32x32x16_f16 v[130:145], v[70:73], v[162:165], v[130:145]
	v_add_f32_e32 v51, v92, v51
	v_add_f32_e32 v51, v93, v51
	v_add_f32_e32 v51, v94, v51
	v_add_f32_e32 v51, v95, v51
	v_cvt_pkrtz_f16_f32 v146, v90, v91
	v_cvt_pkrtz_f16_f32 v147, v92, v93
	ds_read_b64_tr_b16 v[98:99], v50 offset:31744
	ds_read_b64_tr_b16 v[100:101], v50 offset:32256
	v_mfma_f32_32x32x16_f16 v[114:129], v[58:61], v[162:165], v[114:129]
	v_add_f32_e32 v50, v96, v51
	v_add_f32_e32 v50, v97, v50
	v_add_f32_e32 v50, 0, v50
	v_cvt_pkrtz_f16_f32 v148, v94, v95
	v_cvt_pkrtz_f16_f32 v149, v96, v97
	s_nop 0
	v_add_f32_e32 v51, v201, v50
	v_max_f32_e32 v50, v131, v131
	v_max_f32_e32 v52, v130, v130
	v_max_f32_e32 v50, v52, v50
	s_nop 1
	v_max3_f32 v52, v132, v133, v115
	v_max3_f32 v50, v50, v114, v116
	v_max3_f32 v50, v50, v117, v134
	v_max3_f32 v52, v52, v136, v137
	v_max3_f32 v50, v50, v135, v118
	v_max3_f32 v52, v52, v120, v121
	v_max3_f32 v50, v50, v119, v138
	v_max3_f32 v52, v52, v140, v141
	v_max3_f32 v50, v50, v139, v122
	v_max3_f32 v52, v52, v124, v125
	v_max3_f32 v50, v50, v123, v142
	v_max3_f32 v52, v52, v144, v145
	v_max3_f32 v50, v50, v143, v126
	v_max3_f32 v52, v52, v128, v129
	v_max3_f32 v50, v50, v127, v52
	v_mov_b32_e32 v52, v50
	s_nop 1
	v_permlane32_swap_b32_e32 v50, v52
	v_max_f32_e32 v52, v52, v52
	v_max_f32_e32 v50, v50, v50
	v_max_f32_e32 v50, v50, v52
	v_cmp_lt_f32_e32 vcc, s34, v50
	s_cmp_lg_u64 vcc, 0
	s_cselect_b64 s[20:21], -1, 0
	s_cbranch_vccnz .LBB1_17
	v_mov_b32_e32 v201, v51
	v_mov_b32_e32 v219, v220
.LBB1_10:
	s_add_i32 s22, s33, 0x2000
	s_cmpk_lg_i32 s33, 0x4000
	s_cselect_b32 s35, s22, 0
	s_waitcnt lgkmcnt(14)
	v_mfma_f32_32x32x16_f16 v[2:17], v[158:161], v[190:193], v[2:17]
	v_exp_f32_e32 v66, v130
	v_exp_f32_e32 v67, v131
	v_exp_f32_e32 v68, v132
	v_exp_f32_e32 v69, v133
	v_lshl_add_u64 v[50:51], v[204:205], 0, s[18:19]
	s_add_i32 s22, s33, s29
	s_mov_b32 s23, m0
	s_mov_b32 m0, s22
	s_nop 0
	global_load_lds_dwordx4 v[50:51], off
	s_mov_b32 m0, s23
	s_waitcnt lgkmcnt(12)
	v_mfma_f32_32x32x16_f16 v[18:33], v[158:161], v[182:185], v[18:33]
	v_exp_f32_e32 v78, v142
	v_exp_f32_e32 v79, v143
	v_exp_f32_e32 v80, v144
	v_exp_f32_e32 v81, v145
	v_lshl_add_u64 v[50:51], v[206:207], 0, s[18:19]
	s_add_i32 s22, s33, s28
	s_mov_b32 s23, m0
	s_mov_b32 m0, s22
	s_nop 0
	global_load_lds_dwordx4 v[50:51], off
	s_mov_b32 m0, s23
	v_add_u32_e32 v86, s35, v218
	ds_read_b128 v[82:85], v86
	ds_read_b128 v[182:185], v86 offset:512
	s_waitcnt lgkmcnt(12)
	v_mfma_f32_32x32x16_f16 v[2:17], v[154:157], v[178:181], v[2:17]
	v_exp_f32_e32 v74, v138
	v_exp_f32_e32 v75, v139
	v_exp_f32_e32 v76, v140
	v_exp_f32_e32 v77, v141
	v_lshl_add_u64 v[50:51], v[208:209], 0, s[8:9]
	s_add_i32 s22, s35, s26
	s_mov_b32 s23, m0
	s_mov_b32 m0, s22
	s_nop 0
	global_load_lds_dwordx4 v[50:51], off
	s_mov_b32 m0, s23
	ds_read_b128 v[178:181], v86 offset:2048
	ds_read_b128 v[142:145], v86 offset:2560
	s_waitcnt lgkmcnt(12)
	v_mfma_f32_32x32x16_f16 v[18:33], v[154:157], v[186:189], v[18:33]
	v_exp_f32_e32 v70, v134
	v_exp_f32_e32 v71, v135
	v_exp_f32_e32 v72, v136
	v_exp_f32_e32 v73, v137
	v_lshl_add_u64 v[50:51], v[210:211], 0, s[8:9]
	s_add_i32 s22, s35, s25
	s_mov_b32 s23, m0
	s_mov_b32 m0, s22
	s_nop 0
	global_load_lds_dwordx4 v[50:51], off
	s_mov_b32 m0, s23
	ds_read_b128 v[138:141], v86 offset:4096
	ds_read_b128 v[134:137], v86 offset:4608
	s_waitcnt lgkmcnt(12)
	v_mfma_f32_32x32x16_f16 v[2:17], v[150:153], v[110:113], v[2:17]
	v_exp_f32_e32 v62, v126
	v_exp_f32_e32 v63, v127
	v_exp_f32_e32 v64, v128
	v_exp_f32_e32 v65, v129
	ds_read_b128 v[130:133], v86 offset:6144
	ds_read_b128 v[126:129], v86 offset:6656
	s_waitcnt lgkmcnt(12)
	v_mfma_f32_32x32x16_f16 v[18:33], v[150:153], v[106:109], v[18:33]
	v_exp_f32_e32 v50, v114
	v_exp_f32_e32 v51, v115
	v_exp_f32_e32 v52, v116
	v_exp_f32_e32 v53, v117
	s_waitcnt lgkmcnt(10)
	v_mfma_f32_32x32x16_f16 v[2:17], v[146:149], v[102:105], v[2:17]
	v_exp_f32_e32 v54, v118
	v_exp_f32_e32 v55, v119
	v_exp_f32_e32 v56, v120
	v_exp_f32_e32 v57, v121
	s_waitcnt lgkmcnt(8)
	v_mfma_f32_32x32x16_f16 v[18:33], v[146:149], v[98:101], v[18:33]
	v_exp_f32_e32 v58, v122
	v_exp_f32_e32 v59, v123
	v_exp_f32_e32 v60, v124
	v_exp_f32_e32 v61, v125
	s_waitcnt vmcnt(4) lgkmcnt(0)
	s_barrier
	s_andn2_b64 vcc, exec, s[20:21]
	s_cbranch_vccnz .LBB1_12
	v_add_u32_e32 v98, s30, v200
	ds_read_b128 v[86:89], v98 offset:49248
	ds_read_b128 v[90:93], v98 offset:49216
	ds_read_b128 v[94:97], v98 offset:49152
	ds_read_b128 v[98:101], v98 offset:49184
	s_waitcnt lgkmcnt(3)
	v_pk_mul_f32 v[16:17], v[16:17], v[88:89]
	v_pk_mul_f32 v[14:15], v[14:15], v[86:87]
	s_waitcnt lgkmcnt(2)
	v_pk_mul_f32 v[12:13], v[12:13], v[92:93]
	v_pk_mul_f32 v[10:11], v[10:11], v[90:91]
	s_waitcnt lgkmcnt(0)
	v_pk_mul_f32 v[8:9], v[8:9], v[100:101]
	v_pk_mul_f32 v[6:7], v[6:7], v[98:99]
	v_pk_mul_f32 v[4:5], v[4:5], v[96:97]
	v_pk_mul_f32 v[2:3], v[2:3], v[94:95]
	v_pk_mul_f32 v[32:33], v[32:33], v[88:89]
	v_pk_mul_f32 v[30:31], v[30:31], v[86:87]
	v_pk_mul_f32 v[28:29], v[28:29], v[92:93]
	v_pk_mul_f32 v[26:27], v[26:27], v[90:91]
	v_pk_mul_f32 v[24:25], v[24:25], v[100:101]
	v_pk_mul_f32 v[22:23], v[22:23], v[98:99]
	v_pk_mul_f32 v[20:21], v[20:21], v[96:97]
	v_pk_mul_f32 v[18:19], v[18:19], v[94:95]

.LBB1_17:
	v_max_f32_e32 v35, v50, v50
	v_max_f32_e32 v52, 0, v35
	v_exp_f32_e64 v35, -v52
	s_and_saveexec_b64 s[22:23], s[4:5]
	ds_write_b32 v217, v35 offset:49152
	s_or_b64 exec, exec, s[22:23]
	v_add_f32_e32 v219, v220, v52
	v_xor_b32_e32 v50, 0x80000000, v219
	v_mul_f32_e32 v201, v51, v35
	v_pk_add_f32 v[114:115], v[114:115], v[52:53] op_sel_hi:[1,0] neg_lo:[0,1] neg_hi:[0,1]
	v_pk_add_f32 v[116:117], v[116:117], v[52:53] op_sel_hi:[1,0] neg_lo:[0,1] neg_hi:[0,1]
	v_pk_add_f32 v[118:119], v[118:119], v[52:53] op_sel_hi:[1,0] neg_lo:[0,1] neg_hi:[0,1]
	v_pk_add_f32 v[120:121], v[120:121], v[52:53] op_sel_hi:[1,0] neg_lo:[0,1] neg_hi:[0,1]
	v_pk_add_f32 v[122:123], v[122:123], v[52:53] op_sel_hi:[1,0] neg_lo:[0,1] neg_hi:[0,1]
	v_pk_add_f32 v[124:125], v[124:125], v[52:53] op_sel_hi:[1,0] neg_lo:[0,1] neg_hi:[0,1]
	v_pk_add_f32 v[126:127], v[126:127], v[52:53] op_sel_hi:[1,0] neg_lo:[0,1] neg_hi:[0,1]
	v_pk_add_f32 v[128:129], v[128:129], v[52:53] op_sel_hi:[1,0] neg_lo:[0,1] neg_hi:[0,1]
	v_pk_add_f32 v[130:131], v[130:131], v[52:53] op_sel_hi:[1,0] neg_lo:[0,1] neg_hi:[0,1]
	v_pk_add_f32 v[132:133], v[132:133], v[52:53] op_sel_hi:[1,0] neg_lo:[0,1] neg_hi:[0,1]
	v_pk_add_f32 v[134:135], v[134:135], v[52:53] op_sel_hi:[1,0] neg_lo:[0,1] neg_hi:[0,1]
	v_pk_add_f32 v[136:137], v[136:137], v[52:53] op_sel_hi:[1,0] neg_lo:[0,1] neg_hi:[0,1]
	v_pk_add_f32 v[138:139], v[138:139], v[52:53] op_sel_hi:[1,0] neg_lo:[0,1] neg_hi:[0,1]
	v_pk_add_f32 v[140:141], v[140:141], v[52:53] op_sel_hi:[1,0] neg_lo:[0,1] neg_hi:[0,1]
	v_pk_add_f32 v[142:143], v[142:143], v[52:53] op_sel_hi:[1,0] neg_lo:[0,1] neg_hi:[0,1]
	v_pk_add_f32 v[144:145], v[144:145], v[52:53] op_sel_hi:[1,0] neg_lo:[0,1] neg_hi:[0,1]
	v_mov_b32_e32 v34, v50
	v_mov_b32_e32 v35, v50
	v_mov_b32_e32 v36, v50
	v_mov_b32_e32 v37, v50
	v_mov_b32_e32 v38, v50
	v_mov_b32_e32 v39, v50
	v_mov_b32_e32 v40, v50
	v_mov_b32_e32 v41, v50
	v_mov_b32_e32 v42, v50
	v_mov_b32_e32 v43, v50
	v_mov_b32_e32 v44, v50
	v_mov_b32_e32 v45, v50
	v_mov_b32_e32 v46, v50
	v_mov_b32_e32 v47, v50
	v_mov_b32_e32 v48, v50
	v_mov_b32_e32 v49, v50
	s_branch .LBB1_10

.LBB2_10:
	s_or_b64 exec, exec, s[14:15]
	v_lshrrev_b32_e32 v45, 2, v44
	s_lshl_b64 s[0:1], s[2:3], 2
	v_and_or_b32 v45, v45, 12, s18
	s_waitcnt lgkmcnt(0)
	s_add_u32 s18, s8, s0
	s_addc_u32 s19, s9, s1
	s_waitcnt lgkmcnt(0)
	s_barrier
	v_lshlrev_b32_e32 v124, 2, v45
	s_add_u32 s20, s10, s0
	global_load_dwordx4 v[116:119], v124, s[18:19]
	s_addc_u32 s21, s11, s1
	global_load_dwordx4 v[112:115], v124, s[20:21]
	v_and_or_b32 v44, v44, 15, s16
	s_movk_i32 s7, 0x190
	v_lshl_add_u32 v46, v44, 3, 0
	v_mul_lo_u32 v104, v44, s7
	v_add_u32_e32 v44, 0xc800, v46
	v_lshlrev_b32_e32 v105, 1, v45
	ds_read2_b64 v[60:63], v44 offset1:16
	ds_read2_b64 v[44:47], v44 offset0:32 offset1:48
	v_add3_u32 v121, 0, v105, v104
	global_load_dwordx4 v[108:111], v124, s[18:19] offset:64
	global_load_dwordx4 v[104:107], v124, s[20:21] offset:64
	s_mov_b32 s8, 0x3e6d3388
	s_mov_b32 s22, 0xbf3a00e3
	s_mov_b32 s0, 0x3f07dc22
	s_mov_b32 s16, 0xbf38aa3b
	v_mov_b64_e32 v[122:123], s[22:23]
	s_mov_b32 s14, 0x3f35f0e3
	s_mov_b32 s6, 0xbe11a98e
	s_mov_b32 s10, 0x3e027906
	s_waitcnt vmcnt(3) lgkmcnt(1)
	v_pk_fma_f32 v[100:101], v[116:117], v[60:61], v[100:101] op_sel_hi:[1,0,1] neg_lo:[1,0,0] neg_hi:[1,0,0]
	v_xor_b32_e32 v119, 0x80000000, v119
	v_xor_b32_e32 v118, 0x80000000, v118
	v_pk_fma_f32 v[102:103], v[118:119], v[60:61], v[102:103] op_sel_hi:[1,0,1]
	s_waitcnt vmcnt(2)
	v_pk_fma_f32 v[100:101], v[60:61], v[100:101], v[112:113] op_sel:[1,0,0]
	v_pk_fma_f32 v[102:103], v[60:61], v[102:103], v[114:115] op_sel:[1,0,0]
	v_and_b32_e32 v127, 0x7fffffff, v101
	v_and_b32_e32 v126, 0x7fffffff, v100
	v_and_b32_e32 v133, 0x7fffffff, v103
	v_and_b32_e32 v132, 0x7fffffff, v102
	v_pk_fma_f32 v[126:127], v[126:127], s[8:9], 1.0 op_sel_hi:[1,0,0]
	v_pk_fma_f32 v[96:97], v[116:117], v[62:63], v[96:97] op_sel_hi:[1,0,1] neg_lo:[1,0,0] neg_hi:[1,0,0]
	v_pk_fma_f32 v[132:133], v[132:133], s[8:9], 1.0 op_sel_hi:[1,0,0]
	v_rcp_f32_e32 v126, v126
	v_rcp_f32_e32 v127, v127
	v_pk_fma_f32 v[96:97], v[62:63], v[96:97], v[112:113] op_sel:[1,0,0]
	v_rcp_f32_e32 v132, v132
	v_rcp_f32_e32 v133, v133
	v_and_b32_e32 v135, 0x7fffffff, v97
	v_and_b32_e32 v134, 0x7fffffff, v96
	v_pk_mul_f32 v[130:131], v[100:101], v[100:101]
	v_pk_fma_f32 v[134:135], v[134:135], s[8:9], 1.0 op_sel_hi:[1,0,0]
	v_pk_mul_f32 v[128:129], v[102:103], v[102:103]
	v_pk_mul_f32 v[130:131], v[130:131], s[16:17] op_sel_hi:[1,0]
	v_rcp_f32_e32 v134, v134
	v_rcp_f32_e32 v135, v135
	v_pk_fma_f32 v[140:141], v[126:127], s[0:1], v[122:123] op_sel_hi:[1,0,0]
	v_pk_mul_f32 v[128:129], v[128:129], s[16:17] op_sel_hi:[1,0]
	v_exp_f32_e32 v130, v130
	v_exp_f32_e32 v131, v131
	v_pk_fma_f32 v[142:143], v[132:133], s[0:1], v[122:123] op_sel_hi:[1,0,0]
	v_pk_fma_f32 v[140:141], v[126:127], v[140:141], s[14:15] op_sel_hi:[1,1,0]
	v_exp_f32_e32 v128, v128
	v_exp_f32_e32 v129, v129
	v_pk_fma_f32 v[142:143], v[132:133], v[142:143], s[14:15] op_sel_hi:[1,1,0]
	v_pk_fma_f32 v[140:141], v[126:127], v[140:141], s[6:7] op_sel_hi:[1,1,0]
	v_pk_mul_f32 v[138:139], v[96:97], v[96:97]
	v_pk_fma_f32 v[142:143], v[132:133], v[142:143], s[6:7] op_sel_hi:[1,1,0]
	v_pk_fma_f32 v[140:141], v[126:127], v[140:141], s[10:11] op_sel_hi:[1,1,0]
	v_pk_mul_f32 v[138:139], v[138:139], s[16:17] op_sel_hi:[1,0]
	v_pk_fma_f32 v[144:145], v[134:135], s[0:1], v[122:123] op_sel_hi:[1,0,0]
	v_pk_fma_f32 v[142:143], v[132:133], v[142:143], s[10:11] op_sel_hi:[1,1,0]
	v_pk_mul_f32 v[126:127], v[126:127], v[140:141]
	v_exp_f32_e32 v138, v138
	v_exp_f32_e32 v139, v139
	v_pk_fma_f32 v[144:145], v[134:135], v[144:145], s[14:15] op_sel_hi:[1,1,0]
	v_pk_mul_f32 v[132:133], v[132:133], v[142:143]
	v_pk_mul_f32 v[126:127], v[130:131], v[126:127]
	v_pk_fma_f32 v[98:99], v[118:119], v[62:63], v[98:99] op_sel_hi:[1,0,1]
	v_pk_fma_f32 v[144:145], v[134:135], v[144:145], s[6:7] op_sel_hi:[1,1,0]
	v_pk_mul_f32 v[128:129], v[128:129], v[132:133]
	v_pk_mul_f32 v[132:133], v[100:101], v[126:127]
	v_pk_fma_f32 v[126:127], v[100:101], v[126:127], v[100:101] neg_lo:[1,0,0] neg_hi:[1,0,0]
	v_cmp_gt_f32_e32 vcc, 0, v100
	v_pk_fma_f32 v[98:99], v[62:63], v[98:99], v[114:115] op_sel:[1,0,0]
	v_pk_fma_f32 v[144:145], v[134:135], v[144:145], s[10:11] op_sel_hi:[1,1,0]
	v_cndmask_b32_e32 v100, v126, v132, vcc
	v_cmp_gt_f32_e32 vcc, 0, v101
	v_pk_mul_f32 v[134:135], v[134:135], v[144:145]
	v_and_b32_e32 v126, 0x7fffffff, v98
	v_cndmask_b32_e32 v101, v127, v133, vcc
	v_and_b32_e32 v127, 0x7fffffff, v99
	v_pk_mul_f32 v[130:131], v[138:139], v[134:135]
	v_pk_mul_f32 v[134:135], v[102:103], v[128:129]
	v_pk_fma_f32 v[128:129], v[102:103], v[128:129], v[102:103] neg_lo:[1,0,0] neg_hi:[1,0,0]
	v_cmp_gt_f32_e32 vcc, 0, v102
	v_pk_fma_f32 v[126:127], v[126:127], s[8:9], 1.0 op_sel_hi:[1,0,0]
	v_pk_mul_f32 v[138:139], v[96:97], v[130:131]
	v_cndmask_b32_e32 v102, v128, v134, vcc
	v_cmp_gt_f32_e32 vcc, 0, v103
	v_rcp_f32_e32 v126, v126
	v_rcp_f32_e32 v127, v127
	v_cndmask_b32_e32 v103, v129, v135, vcc
	v_cvt_pk_f16_f32 v100, v100, v101
	v_cvt_pk_f16_f32 v101, v102, v103
	v_pk_fma_f32 v[102:103], v[96:97], v[130:131], v[96:97] neg_lo:[1,0,0] neg_hi:[1,0,0]
	v_cmp_gt_f32_e32 vcc, 0, v96
	v_pk_mul_f32 v[136:137], v[98:99], v[98:99]
	s_waitcnt lgkmcnt(0)
	v_pk_fma_f32 v[92:93], v[116:117], v[44:45], v[92:93] op_sel_hi:[1,0,1] neg_lo:[1,0,0] neg_hi:[1,0,0]
	v_cndmask_b32_e32 v125, v102, v138, vcc
	v_cmp_gt_f32_e32 vcc, 0, v97
	v_pk_fma_f32 v[96:97], v[126:127], s[0:1], v[122:123] op_sel_hi:[1,0,0]
	v_pk_fma_f32 v[92:93], v[44:45], v[92:93], v[112:113] op_sel:[1,0,0]
	v_cndmask_b32_e32 v128, v103, v139, vcc
	v_pk_mul_f32 v[102:103], v[136:137], s[16:17] op_sel_hi:[1,0]
	v_pk_fma_f32 v[96:97], v[126:127], v[96:97], s[14:15] op_sel_hi:[1,1,0]
	v_exp_f32_e32 v102, v102
	v_exp_f32_e32 v103, v103
	v_pk_fma_f32 v[96:97], v[126:127], v[96:97], s[6:7] op_sel_hi:[1,1,0]
	v_cmp_gt_f32_e32 vcc, 0, v98
	v_pk_fma_f32 v[96:97], v[126:127], v[96:97], s[10:11] op_sel_hi:[1,1,0]
	v_pk_fma_f32 v[94:95], v[118:119], v[44:45], v[94:95] op_sel_hi:[1,0,1]
	v_pk_mul_f32 v[96:97], v[126:127], v[96:97]
	v_pk_mul_f32 v[126:127], v[92:93], v[92:93]
	v_pk_mul_f32 v[96:97], v[102:103], v[96:97]
	v_pk_mul_f32 v[126:127], v[126:127], s[16:17] op_sel_hi:[1,0]
	v_pk_mul_f32 v[102:103], v[98:99], v[96:97]
	v_pk_fma_f32 v[96:97], v[98:99], v[96:97], v[98:99] neg_lo:[1,0,0] neg_hi:[1,0,0]
	v_and_b32_e32 v98, 0x7fffffff, v92
	v_cndmask_b32_e32 v102, v96, v102, vcc
	v_cmp_gt_f32_e32 vcc, 0, v99
	v_and_b32_e32 v99, 0x7fffffff, v93
	v_pk_fma_f32 v[98:99], v[98:99], s[8:9], 1.0 op_sel_hi:[1,0,0]
	v_cndmask_b32_e32 v97, v97, v103, vcc
	v_rcp_f32_e32 v98, v98
	v_rcp_f32_e32 v99, v99
	v_cvt_pk_f16_f32 v97, v102, v97
	v_pk_fma_f32 v[94:95], v[44:45], v[94:95], v[114:115] op_sel:[1,0,0]
	v_exp_f32_e32 v126, v126
	v_pk_fma_f32 v[102:103], v[98:99], s[0:1], v[122:123] op_sel_hi:[1,0,0]
	v_exp_f32_e32 v127, v127
	v_pk_fma_f32 v[102:103], v[98:99], v[102:103], s[14:15] op_sel_hi:[1,1,0]
	v_cvt_pk_f16_f32 v96, v125, v128
	v_pk_fma_f32 v[102:103], v[98:99], v[102:103], s[6:7] op_sel_hi:[1,1,0]
	v_and_b32_e32 v129, 0x7fffffff, v95
	v_and_b32_e32 v128, 0x7fffffff, v94
	v_pk_fma_f32 v[102:103], v[98:99], v[102:103], s[10:11] op_sel_hi:[1,1,0]
	v_pk_fma_f32 v[128:129], v[128:129], s[8:9], 1.0 op_sel_hi:[1,0,0]
	v_pk_mul_f32 v[98:99], v[98:99], v[102:103]
	v_rcp_f32_e32 v128, v128
	v_rcp_f32_e32 v129, v129
	v_pk_mul_f32 v[98:99], v[126:127], v[98:99]
	v_cmp_gt_f32_e32 vcc, 0, v92
	v_pk_mul_f32 v[126:127], v[92:93], v[98:99]
	v_pk_fma_f32 v[98:99], v[92:93], v[98:99], v[92:93] neg_lo:[1,0,0] neg_hi:[1,0,0]
	v_pk_mul_f32 v[102:103], v[94:95], v[94:95]
	v_cndmask_b32_e32 v125, v98, v126, vcc
	v_cmp_gt_f32_e32 vcc, 0, v93
	v_pk_fma_f32 v[92:93], v[128:129], s[0:1], v[122:123] op_sel_hi:[1,0,0]
	v_pk_fma_f32 v[88:89], v[116:117], v[46:47], v[88:89] op_sel_hi:[1,0,1] neg_lo:[1,0,0] neg_hi:[1,0,0]
	v_cndmask_b32_e32 v126, v99, v127, vcc
	v_pk_mul_f32 v[98:99], v[102:103], s[16:17] op_sel_hi:[1,0]
	v_pk_fma_f32 v[92:93], v[128:129], v[92:93], s[14:15] op_sel_hi:[1,1,0]
	v_exp_f32_e32 v98, v98
	v_exp_f32_e32 v99, v99
	v_pk_fma_f32 v[92:93], v[128:129], v[92:93], s[6:7] op_sel_hi:[1,1,0]
	v_cmp_gt_f32_e32 vcc, 0, v94
	v_pk_fma_f32 v[92:93], v[128:129], v[92:93], s[10:11] op_sel_hi:[1,1,0]
	v_pk_fma_f32 v[88:89], v[46:47], v[88:89], v[112:113] op_sel:[1,0,0]
	v_pk_mul_f32 v[92:93], v[128:129], v[92:93]
	v_pk_mul_f32 v[102:103], v[88:89], v[88:89]
	v_pk_mul_f32 v[92:93], v[98:99], v[92:93]
	v_pk_fma_f32 v[90:91], v[118:119], v[46:47], v[90:91] op_sel_hi:[1,0,1]
	v_pk_mul_f32 v[98:99], v[94:95], v[92:93]
	v_pk_fma_f32 v[92:93], v[94:95], v[92:93], v[94:95] neg_lo:[1,0,0] neg_hi:[1,0,0]
	v_and_b32_e32 v94, 0x7fffffff, v88
	v_cndmask_b32_e32 v98, v92, v98, vcc
	v_cmp_gt_f32_e32 vcc, 0, v95
	v_and_b32_e32 v95, 0x7fffffff, v89
	v_pk_fma_f32 v[94:95], v[94:95], s[8:9], 1.0 op_sel_hi:[1,0,0]
	v_cndmask_b32_e32 v93, v93, v99, vcc
	v_rcp_f32_e32 v94, v94
	v_rcp_f32_e32 v95, v95
	v_cvt_pk_f16_f32 v93, v98, v93
	v_pk_mul_f32 v[102:103], v[102:103], s[16:17] op_sel_hi:[1,0]
	v_pk_fma_f32 v[90:91], v[46:47], v[90:91], v[114:115] op_sel:[1,0,0]
	v_pk_fma_f32 v[98:99], v[94:95], s[0:1], v[122:123] op_sel_hi:[1,0,0]
	v_exp_f32_e32 v102, v102
	v_pk_fma_f32 v[98:99], v[94:95], v[98:99], s[14:15] op_sel_hi:[1,1,0]
	v_exp_f32_e32 v103, v103
	v_pk_fma_f32 v[98:99], v[94:95], v[98:99], s[6:7] op_sel_hi:[1,1,0]
	v_and_b32_e32 v113, 0x7fffffff, v91
	v_and_b32_e32 v112, 0x7fffffff, v90
	v_pk_fma_f32 v[98:99], v[94:95], v[98:99], s[10:11] op_sel_hi:[1,1,0]
	v_pk_fma_f32 v[112:113], v[112:113], s[8:9], 1.0 op_sel_hi:[1,0,0]
	v_pk_mul_f32 v[94:95], v[94:95], v[98:99]
	v_rcp_f32_e32 v112, v112
	v_rcp_f32_e32 v113, v113
	v_pk_mul_f32 v[94:95], v[102:103], v[94:95]
	v_cmp_gt_f32_e32 vcc, 0, v88
	v_pk_mul_f32 v[102:103], v[88:89], v[94:95]
	v_pk_fma_f32 v[94:95], v[88:89], v[94:95], v[88:89] neg_lo:[1,0,0] neg_hi:[1,0,0]
	v_pk_mul_f32 v[98:99], v[90:91], v[90:91]
	v_cndmask_b32_e32 v102, v94, v102, vcc
	v_cmp_gt_f32_e32 vcc, 0, v89
	v_pk_fma_f32 v[88:89], v[112:113], s[0:1], v[122:123] op_sel_hi:[1,0,0]
	s_waitcnt vmcnt(1)
	v_pk_fma_f32 v[84:85], v[108:109], v[60:61], v[84:85] op_sel_hi:[1,0,1] neg_lo:[1,0,0] neg_hi:[1,0,0]
	v_cndmask_b32_e32 v103, v95, v103, vcc
	v_pk_mul_f32 v[94:95], v[98:99], s[16:17] op_sel_hi:[1,0]
	v_pk_fma_f32 v[88:89], v[112:113], v[88:89], s[14:15] op_sel_hi:[1,1,0]
	v_exp_f32_e32 v94, v94
	v_exp_f32_e32 v95, v95
	v_pk_fma_f32 v[88:89], v[112:113], v[88:89], s[6:7] op_sel_hi:[1,1,0]
	v_cmp_gt_f32_e32 vcc, 0, v90
	v_pk_fma_f32 v[88:89], v[112:113], v[88:89], s[10:11] op_sel_hi:[1,1,0]
	s_waitcnt vmcnt(0)
	v_pk_fma_f32 v[84:85], v[60:61], v[84:85], v[104:105] op_sel:[1,0,0]
	v_pk_mul_f32 v[88:89], v[112:113], v[88:89]
	v_pk_fma_f32 v[80:81], v[108:109], v[62:63], v[80:81] op_sel_hi:[1,0,1] neg_lo:[1,0,0] neg_hi:[1,0,0]
	v_pk_mul_f32 v[88:89], v[94:95], v[88:89]
	v_pk_fma_f32 v[80:81], v[62:63], v[80:81], v[104:105] op_sel:[1,0,0]
	v_pk_mul_f32 v[94:95], v[90:91], v[88:89]
	v_pk_fma_f32 v[88:89], v[90:91], v[88:89], v[90:91] neg_lo:[1,0,0] neg_hi:[1,0,0]
	v_pk_fma_f32 v[76:77], v[108:109], v[44:45], v[76:77] op_sel_hi:[1,0,1] neg_lo:[1,0,0] neg_hi:[1,0,0]
	v_cndmask_b32_e32 v90, v88, v94, vcc
	v_cmp_gt_f32_e32 vcc, 0, v91
	v_and_b32_e32 v94, 0x7fffffff, v84
	v_cvt_pk_f16_f32 v88, v102, v103
	v_cndmask_b32_e32 v89, v89, v95, vcc
	v_and_b32_e32 v95, 0x7fffffff, v85
	v_pk_fma_f32 v[94:95], v[94:95], s[8:9], 1.0 op_sel_hi:[1,0,0]
	v_cvt_pk_f16_f32 v89, v90, v89
	v_rcp_f32_e32 v94, v94
	v_rcp_f32_e32 v95, v95
	v_xor_b32_e32 v91, 0x80000000, v111
	v_xor_b32_e32 v90, 0x80000000, v110
	v_pk_mul_f32 v[102:103], v[84:85], v[84:85]
	v_pk_fma_f32 v[86:87], v[90:91], v[60:61], v[86:87] op_sel_hi:[1,0,1]
	v_pk_fma_f32 v[98:99], v[94:95], s[0:1], v[122:123] op_sel_hi:[1,0,0]
	v_pk_mul_f32 v[102:103], v[102:103], s[16:17] op_sel_hi:[1,0]
	v_pk_fma_f32 v[86:87], v[60:61], v[86:87], v[106:107] op_sel:[1,0,0]
	v_pk_fma_f32 v[98:99], v[94:95], v[98:99], s[14:15] op_sel_hi:[1,1,0]
	v_exp_f32_e32 v102, v102
	v_exp_f32_e32 v103, v103
	v_pk_fma_f32 v[98:99], v[94:95], v[98:99], s[6:7] op_sel_hi:[1,1,0]
	v_and_b32_e32 v111, 0x7fffffff, v87
	v_and_b32_e32 v110, 0x7fffffff, v86
	v_pk_fma_f32 v[98:99], v[94:95], v[98:99], s[10:11] op_sel_hi:[1,1,0]
	v_pk_fma_f32 v[110:111], v[110:111], s[8:9], 1.0 op_sel_hi:[1,0,0]
	v_pk_mul_f32 v[94:95], v[94:95], v[98:99]
	v_rcp_f32_e32 v110, v110
	v_rcp_f32_e32 v111, v111
	v_pk_mul_f32 v[94:95], v[102:103], v[94:95]
	v_cmp_gt_f32_e32 vcc, 0, v84
	v_pk_mul_f32 v[102:103], v[84:85], v[94:95]
	v_pk_fma_f32 v[94:95], v[84:85], v[94:95], v[84:85] neg_lo:[1,0,0] neg_hi:[1,0,0]
	v_pk_mul_f32 v[98:99], v[86:87], v[86:87]
	v_cndmask_b32_e32 v102, v94, v102, vcc
	v_cmp_gt_f32_e32 vcc, 0, v85
	v_pk_fma_f32 v[84:85], v[110:111], s[0:1], v[122:123] op_sel_hi:[1,0,0]
	v_pk_fma_f32 v[82:83], v[90:91], v[62:63], v[82:83] op_sel_hi:[1,0,1]
	v_cndmask_b32_e32 v103, v95, v103, vcc
	v_pk_mul_f32 v[94:95], v[98:99], s[16:17] op_sel_hi:[1,0]
	v_pk_fma_f32 v[84:85], v[110:111], v[84:85], s[14:15] op_sel_hi:[1,1,0]
	v_exp_f32_e32 v94, v94
	v_exp_f32_e32 v95, v95
	v_pk_fma_f32 v[84:85], v[110:111], v[84:85], s[6:7] op_sel_hi:[1,1,0]
	v_cmp_gt_f32_e32 vcc, 0, v86
	v_pk_fma_f32 v[84:85], v[110:111], v[84:85], s[10:11] op_sel_hi:[1,1,0]
	v_pk_fma_f32 v[82:83], v[62:63], v[82:83], v[106:107] op_sel:[1,0,0]
	v_pk_mul_f32 v[84:85], v[110:111], v[84:85]
	v_and_b32_e32 v99, 0x7fffffff, v83
	v_pk_mul_f32 v[84:85], v[94:95], v[84:85]
	v_and_b32_e32 v98, 0x7fffffff, v82
	v_pk_mul_f32 v[94:95], v[86:87], v[84:85]
	v_pk_fma_f32 v[84:85], v[86:87], v[84:85], v[86:87] neg_lo:[1,0,0] neg_hi:[1,0,0]
	v_pk_fma_f32 v[98:99], v[98:99], s[8:9], 1.0 op_sel_hi:[1,0,0]
	v_cndmask_b32_e32 v86, v84, v94, vcc
	v_cmp_gt_f32_e32 vcc, 0, v87
	v_and_b32_e32 v87, 0x7fffffff, v81
	v_cvt_pk_f16_f32 v84, v102, v103
	v_cndmask_b32_e32 v85, v85, v95, vcc
	v_cvt_pk_f16_f32 v85, v86, v85
	v_and_b32_e32 v86, 0x7fffffff, v80
	v_pk_fma_f32 v[86:87], v[86:87], s[8:9], 1.0 op_sel_hi:[1,0,0]
	v_pk_mul_f32 v[94:95], v[80:81], v[80:81]
	v_rcp_f32_e32 v86, v86
	v_rcp_f32_e32 v87, v87
	ds_write2_b64 v121, v[100:101], v[84:85] offset1:4
	v_pk_mul_f32 v[94:95], v[94:95], s[16:17] op_sel_hi:[1,0]
	v_rcp_f32_e32 v98, v98
	v_pk_fma_f32 v[84:85], v[86:87], s[0:1], v[122:123] op_sel_hi:[1,0,0]
	v_exp_f32_e32 v94, v94
	v_pk_fma_f32 v[84:85], v[86:87], v[84:85], s[14:15] op_sel_hi:[1,1,0]
	v_exp_f32_e32 v95, v95
	v_pk_fma_f32 v[84:85], v[86:87], v[84:85], s[6:7] op_sel_hi:[1,1,0]
	v_rcp_f32_e32 v99, v99
	v_pk_fma_f32 v[84:85], v[86:87], v[84:85], s[10:11] op_sel_hi:[1,1,0]
	v_cmp_gt_f32_e32 vcc, 0, v80
	v_pk_mul_f32 v[84:85], v[86:87], v[84:85]
	v_pk_mul_f32 v[86:87], v[82:83], v[82:83]
	v_pk_mul_f32 v[84:85], v[94:95], v[84:85]
	v_pk_fma_f32 v[76:77], v[44:45], v[76:77], v[104:105] op_sel:[1,0,0]
	v_pk_mul_f32 v[94:95], v[80:81], v[84:85]
	v_pk_fma_f32 v[84:85], v[80:81], v[84:85], v[80:81] neg_lo:[1,0,0] neg_hi:[1,0,0]
	v_pk_fma_f32 v[78:79], v[90:91], v[44:45], v[78:79] op_sel_hi:[1,0,1]
	v_cndmask_b32_e32 v94, v84, v94, vcc
	v_cmp_gt_f32_e32 vcc, 0, v81
	v_pk_fma_f32 v[80:81], v[98:99], s[0:1], v[122:123] op_sel_hi:[1,0,0]
	v_pk_fma_f32 v[78:79], v[44:45], v[78:79], v[106:107] op_sel:[1,0,0]
	v_cndmask_b32_e32 v95, v85, v95, vcc
	v_pk_mul_f32 v[84:85], v[86:87], s[16:17] op_sel_hi:[1,0]
	v_pk_fma_f32 v[80:81], v[98:99], v[80:81], s[14:15] op_sel_hi:[1,1,0]
	v_exp_f32_e32 v84, v84
	v_exp_f32_e32 v85, v85
	v_pk_fma_f32 v[80:81], v[98:99], v[80:81], s[6:7] op_sel_hi:[1,1,0]
	v_cmp_gt_f32_e32 vcc, 0, v82
	v_pk_fma_f32 v[80:81], v[98:99], v[80:81], s[10:11] op_sel_hi:[1,1,0]
	v_pk_fma_f32 v[72:73], v[108:109], v[46:47], v[72:73] op_sel_hi:[1,0,1] neg_lo:[1,0,0] neg_hi:[1,0,0]
	v_pk_mul_f32 v[80:81], v[98:99], v[80:81]
	v_pk_fma_f32 v[72:73], v[46:47], v[72:73], v[104:105] op_sel:[1,0,0]
	v_pk_mul_f32 v[80:81], v[84:85], v[80:81]
	v_cvt_pk_f16_f32 v92, v125, v126
	v_pk_mul_f32 v[84:85], v[82:83], v[80:81]
	v_pk_fma_f32 v[80:81], v[82:83], v[80:81], v[82:83] neg_lo:[1,0,0] neg_hi:[1,0,0]
	v_pk_fma_f32 v[74:75], v[90:91], v[46:47], v[74:75] op_sel_hi:[1,0,1]
	v_cndmask_b32_e32 v82, v80, v84, vcc
	v_cmp_gt_f32_e32 vcc, 0, v83
	v_and_b32_e32 v83, 0x7fffffff, v77
	v_cvt_pk_f16_f32 v80, v94, v95
	v_cndmask_b32_e32 v81, v81, v85, vcc
	v_cvt_pk_f16_f32 v81, v82, v81
	v_and_b32_e32 v82, 0x7fffffff, v76
	v_pk_fma_f32 v[82:83], v[82:83], s[8:9], 1.0 op_sel_hi:[1,0,0]
	v_add_u32_e32 v94, 0x1800, v121
	v_rcp_f32_e32 v82, v82
	v_rcp_f32_e32 v83, v83
	v_pk_mul_f32 v[84:85], v[76:77], v[76:77]
	ds_write2_b64 v94, v[96:97], v[80:81] offset0:32 offset1:36
	v_pk_mul_f32 v[84:85], v[84:85], s[16:17] op_sel_hi:[1,0]
	v_pk_fma_f32 v[80:81], v[82:83], s[0:1], v[122:123] op_sel_hi:[1,0,0]
	v_exp_f32_e32 v84, v84
	v_pk_fma_f32 v[80:81], v[82:83], v[80:81], s[14:15] op_sel_hi:[1,1,0]
	v_exp_f32_e32 v85, v85
	v_pk_fma_f32 v[80:81], v[82:83], v[80:81], s[6:7] op_sel_hi:[1,1,0]
	v_pk_mul_f32 v[96:97], v[78:79], v[78:79]
	v_pk_fma_f32 v[80:81], v[82:83], v[80:81], s[10:11] op_sel_hi:[1,1,0]
	v_cmp_gt_f32_e32 vcc, 0, v76
	v_pk_mul_f32 v[80:81], v[82:83], v[80:81]
	v_pk_mul_f32 v[96:97], v[96:97], s[16:17] op_sel_hi:[1,0]
	v_pk_mul_f32 v[80:81], v[84:85], v[80:81]
	global_load_dwordx4 v[84:87], v124, s[18:19] offset:128
	v_pk_mul_f32 v[98:99], v[76:77], v[80:81]
	v_pk_fma_f32 v[100:101], v[76:77], v[80:81], v[76:77] neg_lo:[1,0,0] neg_hi:[1,0,0]
	v_and_b32_e32 v81, 0x7fffffff, v79
	v_and_b32_e32 v80, 0x7fffffff, v78
	v_pk_fma_f32 v[102:103], v[80:81], s[8:9], 1.0 op_sel_hi:[1,0,0]
	global_load_dwordx4 v[80:83], v124, s[20:21] offset:128
	v_rcp_f32_e32 v102, v102
	v_rcp_f32_e32 v103, v103
	v_cndmask_b32_e32 v95, v100, v98, vcc
	v_cmp_gt_f32_e32 vcc, 0, v77
	v_exp_f32_e32 v96, v96
	v_pk_fma_f32 v[76:77], v[102:103], s[0:1], v[122:123] op_sel_hi:[1,0,0]
	v_exp_f32_e32 v97, v97
	v_pk_fma_f32 v[76:77], v[102:103], v[76:77], s[14:15] op_sel_hi:[1,1,0]
	v_cndmask_b32_e32 v98, v101, v99, vcc
	v_pk_fma_f32 v[76:77], v[102:103], v[76:77], s[6:7] op_sel_hi:[1,1,0]
	v_cmp_gt_f32_e32 vcc, 0, v78
	v_pk_fma_f32 v[76:77], v[102:103], v[76:77], s[10:11] op_sel_hi:[1,1,0]
	v_pk_mul_f32 v[90:91], v[72:73], v[72:73]
	v_pk_mul_f32 v[76:77], v[102:103], v[76:77]
	v_pk_mul_f32 v[90:91], v[90:91], s[16:17] op_sel_hi:[1,0]
	v_pk_mul_f32 v[76:77], v[96:97], v[76:77]
	v_pk_fma_f32 v[74:75], v[46:47], v[74:75], v[106:107] op_sel:[1,0,0]
	v_pk_mul_f32 v[96:97], v[78:79], v[76:77]
	v_pk_fma_f32 v[76:77], v[78:79], v[76:77], v[78:79] neg_lo:[1,0,0] neg_hi:[1,0,0]
	v_exp_f32_e32 v90, v90
	v_cndmask_b32_e32 v78, v76, v96, vcc
	v_cmp_gt_f32_e32 vcc, 0, v79
	v_and_b32_e32 v79, 0x7fffffff, v73
	v_cvt_pk_f16_f32 v76, v95, v98
	v_cndmask_b32_e32 v77, v77, v97, vcc
	v_cvt_pk_f16_f32 v77, v78, v77
	v_and_b32_e32 v78, 0x7fffffff, v72
	v_pk_fma_f32 v[78:79], v[78:79], s[8:9], 1.0 op_sel_hi:[1,0,0]
	v_add_u32_e32 v95, 0x3000, v121
	v_rcp_f32_e32 v78, v78
	v_rcp_f32_e32 v79, v79
	ds_write2_b64 v95, v[92:93], v[76:77] offset0:64 offset1:68
	v_exp_f32_e32 v91, v91
	v_and_b32_e32 v93, 0x7fffffff, v75
	v_pk_fma_f32 v[76:77], v[78:79], s[0:1], v[122:123] op_sel_hi:[1,0,0]
	v_and_b32_e32 v92, 0x7fffffff, v74
	v_pk_fma_f32 v[76:77], v[78:79], v[76:77], s[14:15] op_sel_hi:[1,1,0]
	v_pk_fma_f32 v[92:93], v[92:93], s[8:9], 1.0 op_sel_hi:[1,0,0]
	v_pk_fma_f32 v[76:77], v[78:79], v[76:77], s[6:7] op_sel_hi:[1,1,0]
	v_rcp_f32_e32 v92, v92
	v_pk_fma_f32 v[76:77], v[78:79], v[76:77], s[10:11] op_sel_hi:[1,1,0]
	v_rcp_f32_e32 v93, v93
	v_pk_mul_f32 v[76:77], v[78:79], v[76:77]
	v_cmp_gt_f32_e32 vcc, 0, v72
	v_pk_mul_f32 v[76:77], v[90:91], v[76:77]
	v_pk_mul_f32 v[78:79], v[74:75], v[74:75]
	v_pk_mul_f32 v[90:91], v[72:73], v[76:77]
	v_pk_fma_f32 v[76:77], v[72:73], v[76:77], v[72:73] neg_lo:[1,0,0] neg_hi:[1,0,0]
	s_nop 0
	v_cndmask_b32_e32 v90, v76, v90, vcc
	v_cmp_gt_f32_e32 vcc, 0, v73
	v_pk_fma_f32 v[72:73], v[92:93], s[0:1], v[122:123] op_sel_hi:[1,0,0]
	s_nop 0
	v_cndmask_b32_e32 v91, v77, v91, vcc
	v_pk_mul_f32 v[76:77], v[78:79], s[16:17] op_sel_hi:[1,0]
	v_pk_fma_f32 v[72:73], v[92:93], v[72:73], s[14:15] op_sel_hi:[1,1,0]
	v_exp_f32_e32 v76, v76
	v_exp_f32_e32 v77, v77
	v_pk_fma_f32 v[72:73], v[92:93], v[72:73], s[6:7] op_sel_hi:[1,1,0]
	v_cmp_gt_f32_e32 vcc, 0, v74
	v_pk_fma_f32 v[72:73], v[92:93], v[72:73], s[10:11] op_sel_hi:[1,1,0]
	s_nop 0
	v_pk_mul_f32 v[72:73], v[92:93], v[72:73]
	s_nop 0
	v_pk_mul_f32 v[72:73], v[76:77], v[72:73]
	s_nop 0
	v_pk_mul_f32 v[76:77], v[74:75], v[72:73]
	v_pk_fma_f32 v[72:73], v[74:75], v[72:73], v[74:75] neg_lo:[1,0,0] neg_hi:[1,0,0]
	s_nop 0
	v_cndmask_b32_e32 v74, v72, v76, vcc
	v_cmp_gt_f32_e32 vcc, 0, v75
	v_cvt_pk_f16_f32 v72, v90, v91
	v_add_u32_e32 v90, 0x4800, v121
	v_cndmask_b32_e32 v73, v73, v77, vcc
	v_cvt_pk_f16_f32 v73, v74, v73
	global_load_dwordx4 v[76:79], v124, s[18:19] offset:192
	s_waitcnt vmcnt(2)
	v_pk_fma_f32 v[68:69], v[84:85], v[60:61], v[68:69] op_sel_hi:[1,0,1] neg_lo:[1,0,0] neg_hi:[1,0,0]
	ds_write2_b64 v90, v[88:89], v[72:73] offset0:96 offset1:100
	global_load_dwordx4 v[72:75], v124, s[20:21] offset:192
	s_waitcnt vmcnt(2)
	v_pk_fma_f32 v[68:69], v[60:61], v[68:69], v[80:81] op_sel:[1,0,0]
	v_xor_b32_e32 v87, 0x80000000, v87
	v_and_b32_e32 v89, 0x7fffffff, v69
	v_and_b32_e32 v88, 0x7fffffff, v68
	v_pk_fma_f32 v[88:89], v[88:89], s[8:9], 1.0 op_sel_hi:[1,0,0]
	v_xor_b32_e32 v86, 0x80000000, v86
	v_rcp_f32_e32 v88, v88
	v_rcp_f32_e32 v89, v89
	v_pk_mul_f32 v[96:97], v[68:69], v[68:69]
	v_pk_fma_f32 v[70:71], v[86:87], v[60:61], v[70:71] op_sel_hi:[1,0,1]
	v_pk_mul_f32 v[96:97], v[96:97], s[16:17] op_sel_hi:[1,0]
	v_pk_fma_f32 v[92:93], v[88:89], s[0:1], v[122:123] op_sel_hi:[1,0,0]
	v_pk_fma_f32 v[70:71], v[60:61], v[70:71], v[82:83] op_sel:[1,0,0]
	v_pk_fma_f32 v[92:93], v[88:89], v[92:93], s[14:15] op_sel_hi:[1,1,0]
	v_exp_f32_e32 v96, v96
	v_exp_f32_e32 v97, v97
	v_pk_fma_f32 v[92:93], v[88:89], v[92:93], s[6:7] op_sel_hi:[1,1,0]
	v_and_b32_e32 v99, 0x7fffffff, v71
	v_and_b32_e32 v98, 0x7fffffff, v70
	v_pk_fma_f32 v[92:93], v[88:89], v[92:93], s[10:11] op_sel_hi:[1,1,0]
	v_pk_fma_f32 v[98:99], v[98:99], s[8:9], 1.0 op_sel_hi:[1,0,0]
	v_pk_mul_f32 v[88:89], v[88:89], v[92:93]
	v_rcp_f32_e32 v98, v98
	v_rcp_f32_e32 v99, v99
	v_pk_mul_f32 v[88:89], v[96:97], v[88:89]
	v_cmp_gt_f32_e32 vcc, 0, v68
	v_pk_mul_f32 v[96:97], v[68:69], v[88:89]
	v_pk_fma_f32 v[88:89], v[68:69], v[88:89], v[68:69] neg_lo:[1,0,0] neg_hi:[1,0,0]
	v_pk_mul_f32 v[92:93], v[70:71], v[70:71]
	v_cndmask_b32_e32 v91, v88, v96, vcc
	v_cmp_gt_f32_e32 vcc, 0, v69
	v_pk_fma_f32 v[68:69], v[98:99], s[0:1], v[122:123] op_sel_hi:[1,0,0]
	v_pk_fma_f32 v[64:65], v[84:85], v[62:63], v[64:65] op_sel_hi:[1,0,1] neg_lo:[1,0,0] neg_hi:[1,0,0]
	v_cndmask_b32_e32 v96, v89, v97, vcc
	v_pk_mul_f32 v[88:89], v[92:93], s[16:17] op_sel_hi:[1,0]
	v_pk_fma_f32 v[68:69], v[98:99], v[68:69], s[14:15] op_sel_hi:[1,1,0]
	v_exp_f32_e32 v88, v88
	v_exp_f32_e32 v89, v89
	v_pk_fma_f32 v[68:69], v[98:99], v[68:69], s[6:7] op_sel_hi:[1,1,0]
	v_cmp_gt_f32_e32 vcc, 0, v70
	v_pk_fma_f32 v[68:69], v[98:99], v[68:69], s[10:11] op_sel_hi:[1,1,0]
	v_pk_fma_f32 v[64:65], v[62:63], v[64:65], v[80:81] op_sel:[1,0,0]
	v_pk_mul_f32 v[68:69], v[98:99], v[68:69]
	v_pk_mul_f32 v[92:93], v[64:65], v[64:65]
	v_pk_mul_f32 v[68:69], v[88:89], v[68:69]
	v_pk_fma_f32 v[66:67], v[86:87], v[62:63], v[66:67] op_sel_hi:[1,0,1]
	v_pk_mul_f32 v[88:89], v[70:71], v[68:69]
	v_pk_fma_f32 v[68:69], v[70:71], v[68:69], v[70:71] neg_lo:[1,0,0] neg_hi:[1,0,0]
	v_and_b32_e32 v70, 0x7fffffff, v64
	v_cndmask_b32_e32 v88, v68, v88, vcc
	v_cmp_gt_f32_e32 vcc, 0, v71
	v_and_b32_e32 v71, 0x7fffffff, v65
	v_pk_fma_f32 v[70:71], v[70:71], s[8:9], 1.0 op_sel_hi:[1,0,0]
	v_cndmask_b32_e32 v69, v69, v89, vcc
	v_rcp_f32_e32 v70, v70
	v_rcp_f32_e32 v71, v71
	v_cvt_pk_f16_f32 v69, v88, v69
	v_pk_mul_f32 v[92:93], v[92:93], s[16:17] op_sel_hi:[1,0]
	v_pk_fma_f32 v[66:67], v[62:63], v[66:67], v[82:83] op_sel:[1,0,0]
	v_pk_fma_f32 v[88:89], v[70:71], s[0:1], v[122:123] op_sel_hi:[1,0,0]
	v_exp_f32_e32 v92, v92
	v_pk_fma_f32 v[88:89], v[70:71], v[88:89], s[14:15] op_sel_hi:[1,1,0]
	v_exp_f32_e32 v93, v93
	v_cvt_pk_f16_f32 v68, v91, v96
	v_pk_fma_f32 v[88:89], v[70:71], v[88:89], s[6:7] op_sel_hi:[1,1,0]
	v_and_b32_e32 v97, 0x7fffffff, v67
	v_and_b32_e32 v96, 0x7fffffff, v66
	v_pk_fma_f32 v[88:89], v[70:71], v[88:89], s[10:11] op_sel_hi:[1,1,0]
	v_pk_fma_f32 v[96:97], v[96:97], s[8:9], 1.0 op_sel_hi:[1,0,0]
	v_pk_mul_f32 v[70:71], v[70:71], v[88:89]
	v_rcp_f32_e32 v96, v96
	v_rcp_f32_e32 v97, v97
	v_pk_mul_f32 v[70:71], v[92:93], v[70:71]
	v_cmp_gt_f32_e32 vcc, 0, v64
	v_pk_mul_f32 v[92:93], v[64:65], v[70:71]
	v_pk_fma_f32 v[70:71], v[64:65], v[70:71], v[64:65] neg_lo:[1,0,0] neg_hi:[1,0,0]
	v_pk_mul_f32 v[88:89], v[66:67], v[66:67]
	v_cndmask_b32_e32 v91, v70, v92, vcc
	v_cmp_gt_f32_e32 vcc, 0, v65
	v_pk_fma_f32 v[64:65], v[96:97], s[0:1], v[122:123] op_sel_hi:[1,0,0]
	v_pk_fma_f32 v[56:57], v[84:85], v[44:45], v[56:57] op_sel_hi:[1,0,1] neg_lo:[1,0,0] neg_hi:[1,0,0]
	v_cndmask_b32_e32 v92, v71, v93, vcc
	v_pk_mul_f32 v[70:71], v[88:89], s[16:17] op_sel_hi:[1,0]
	v_pk_fma_f32 v[64:65], v[96:97], v[64:65], s[14:15] op_sel_hi:[1,1,0]
	v_exp_f32_e32 v70, v70
	v_exp_f32_e32 v71, v71
	v_pk_fma_f32 v[64:65], v[96:97], v[64:65], s[6:7] op_sel_hi:[1,1,0]
	v_cmp_gt_f32_e32 vcc, 0, v66
	v_pk_fma_f32 v[64:65], v[96:97], v[64:65], s[10:11] op_sel_hi:[1,1,0]
	v_pk_fma_f32 v[56:57], v[44:45], v[56:57], v[80:81] op_sel:[1,0,0]
	v_pk_mul_f32 v[64:65], v[96:97], v[64:65]
	v_pk_mul_f32 v[88:89], v[56:57], v[56:57]
	v_pk_mul_f32 v[64:65], v[70:71], v[64:65]
	v_pk_fma_f32 v[58:59], v[86:87], v[44:45], v[58:59] op_sel_hi:[1,0,1]
	v_pk_mul_f32 v[70:71], v[66:67], v[64:65]
	v_pk_fma_f32 v[64:65], v[66:67], v[64:65], v[66:67] neg_lo:[1,0,0] neg_hi:[1,0,0]
	v_and_b32_e32 v66, 0x7fffffff, v56
	v_cndmask_b32_e32 v70, v64, v70, vcc
	v_cmp_gt_f32_e32 vcc, 0, v67
	v_and_b32_e32 v67, 0x7fffffff, v57
	v_pk_fma_f32 v[66:67], v[66:67], s[8:9], 1.0 op_sel_hi:[1,0,0]
	v_cndmask_b32_e32 v65, v65, v71, vcc
	v_rcp_f32_e32 v66, v66
	v_rcp_f32_e32 v67, v67
	v_cvt_pk_f16_f32 v65, v70, v65
	v_pk_mul_f32 v[88:89], v[88:89], s[16:17] op_sel_hi:[1,0]
	v_pk_fma_f32 v[58:59], v[44:45], v[58:59], v[82:83] op_sel:[1,0,0]
	v_pk_fma_f32 v[70:71], v[66:67], s[0:1], v[122:123] op_sel_hi:[1,0,0]
	v_exp_f32_e32 v88, v88
	v_pk_fma_f32 v[70:71], v[66:67], v[70:71], s[14:15] op_sel_hi:[1,1,0]
	v_exp_f32_e32 v89, v89
	v_cvt_pk_f16_f32 v64, v91, v92
	v_pk_fma_f32 v[70:71], v[66:67], v[70:71], s[6:7] op_sel_hi:[1,1,0]
	v_and_b32_e32 v93, 0x7fffffff, v59
	v_and_b32_e32 v92, 0x7fffffff, v58
	v_pk_fma_f32 v[70:71], v[66:67], v[70:71], s[10:11] op_sel_hi:[1,1,0]
	v_pk_fma_f32 v[92:93], v[92:93], s[8:9], 1.0 op_sel_hi:[1,0,0]
	v_pk_mul_f32 v[66:67], v[66:67], v[70:71]
	v_rcp_f32_e32 v92, v92
	v_rcp_f32_e32 v93, v93
	v_pk_mul_f32 v[66:67], v[88:89], v[66:67]
	v_cmp_gt_f32_e32 vcc, 0, v56
	v_pk_mul_f32 v[88:89], v[56:57], v[66:67]
	v_pk_fma_f32 v[66:67], v[56:57], v[66:67], v[56:57] neg_lo:[1,0,0] neg_hi:[1,0,0]
	v_pk_mul_f32 v[70:71], v[58:59], v[58:59]
	v_cndmask_b32_e32 v88, v66, v88, vcc
	v_cmp_gt_f32_e32 vcc, 0, v57
	v_pk_fma_f32 v[56:57], v[92:93], s[0:1], v[122:123] op_sel_hi:[1,0,0]
	v_pk_fma_f32 v[52:53], v[84:85], v[46:47], v[52:53] op_sel_hi:[1,0,1] neg_lo:[1,0,0] neg_hi:[1,0,0]
	v_cndmask_b32_e32 v89, v67, v89, vcc
	v_pk_mul_f32 v[66:67], v[70:71], s[16:17] op_sel_hi:[1,0]
	v_pk_fma_f32 v[56:57], v[92:93], v[56:57], s[14:15] op_sel_hi:[1,1,0]
	v_exp_f32_e32 v66, v66
	v_exp_f32_e32 v67, v67
	v_pk_fma_f32 v[56:57], v[92:93], v[56:57], s[6:7] op_sel_hi:[1,1,0]
	v_cmp_gt_f32_e32 vcc, 0, v58
	v_pk_fma_f32 v[56:57], v[92:93], v[56:57], s[10:11] op_sel_hi:[1,1,0]
	v_pk_fma_f32 v[52:53], v[46:47], v[52:53], v[80:81] op_sel:[1,0,0]
	v_pk_mul_f32 v[56:57], v[92:93], v[56:57]
	v_pk_mul_f32 v[70:71], v[52:53], v[52:53]
	v_pk_mul_f32 v[56:57], v[66:67], v[56:57]
	v_pk_fma_f32 v[54:55], v[86:87], v[46:47], v[54:55] op_sel_hi:[1,0,1]
	v_pk_mul_f32 v[66:67], v[58:59], v[56:57]
	v_pk_fma_f32 v[56:57], v[58:59], v[56:57], v[58:59] neg_lo:[1,0,0] neg_hi:[1,0,0]
	v_and_b32_e32 v58, 0x7fffffff, v52
	v_cndmask_b32_e32 v66, v56, v66, vcc
	v_cmp_gt_f32_e32 vcc, 0, v59
	v_and_b32_e32 v59, 0x7fffffff, v53
	v_pk_fma_f32 v[58:59], v[58:59], s[8:9], 1.0 op_sel_hi:[1,0,0]
	v_cndmask_b32_e32 v57, v57, v67, vcc
	v_rcp_f32_e32 v58, v58
	v_rcp_f32_e32 v59, v59
	v_cvt_pk_f16_f32 v57, v66, v57
	v_pk_mul_f32 v[70:71], v[70:71], s[16:17] op_sel_hi:[1,0]
	v_pk_fma_f32 v[54:55], v[46:47], v[54:55], v[82:83] op_sel:[1,0,0]
	v_pk_fma_f32 v[66:67], v[58:59], s[0:1], v[122:123] op_sel_hi:[1,0,0]
	v_exp_f32_e32 v70, v70
	v_pk_fma_f32 v[66:67], v[58:59], v[66:67], s[14:15] op_sel_hi:[1,1,0]
	v_exp_f32_e32 v71, v71
	v_pk_fma_f32 v[66:67], v[58:59], v[66:67], s[6:7] op_sel_hi:[1,1,0]
	v_and_b32_e32 v81, 0x7fffffff, v55
	v_and_b32_e32 v80, 0x7fffffff, v54
	v_pk_fma_f32 v[66:67], v[58:59], v[66:67], s[10:11] op_sel_hi:[1,1,0]
	v_pk_fma_f32 v[80:81], v[80:81], s[8:9], 1.0 op_sel_hi:[1,0,0]
	v_pk_mul_f32 v[58:59], v[58:59], v[66:67]
	v_rcp_f32_e32 v80, v80
	v_rcp_f32_e32 v81, v81
	v_pk_mul_f32 v[58:59], v[70:71], v[58:59]
	v_cmp_gt_f32_e32 vcc, 0, v52
	v_pk_mul_f32 v[70:71], v[52:53], v[58:59]
	v_pk_fma_f32 v[58:59], v[52:53], v[58:59], v[52:53] neg_lo:[1,0,0] neg_hi:[1,0,0]
	v_pk_mul_f32 v[66:67], v[54:55], v[54:55]
	v_cndmask_b32_e32 v70, v58, v70, vcc
	v_cmp_gt_f32_e32 vcc, 0, v53
	v_pk_fma_f32 v[52:53], v[80:81], s[0:1], v[122:123] op_sel_hi:[1,0,0]
	s_waitcnt vmcnt(1)
	v_pk_fma_f32 v[40:41], v[76:77], v[62:63], v[40:41] op_sel_hi:[1,0,1] neg_lo:[1,0,0] neg_hi:[1,0,0]
	v_cndmask_b32_e32 v71, v59, v71, vcc
	v_pk_mul_f32 v[58:59], v[66:67], s[16:17] op_sel_hi:[1,0]
	v_pk_fma_f32 v[52:53], v[80:81], v[52:53], s[14:15] op_sel_hi:[1,1,0]
	v_exp_f32_e32 v58, v58
	v_exp_f32_e32 v59, v59
	v_pk_fma_f32 v[52:53], v[80:81], v[52:53], s[6:7] op_sel_hi:[1,1,0]
	v_cmp_gt_f32_e32 vcc, 0, v54
	v_pk_fma_f32 v[52:53], v[80:81], v[52:53], s[10:11] op_sel_hi:[1,1,0]
	s_waitcnt vmcnt(0)
	v_pk_fma_f32 v[40:41], v[62:63], v[40:41], v[72:73] op_sel:[1,0,0]
	v_pk_mul_f32 v[52:53], v[80:81], v[52:53]
	v_pk_fma_f32 v[36:37], v[76:77], v[44:45], v[36:37] op_sel_hi:[1,0,1] neg_lo:[1,0,0] neg_hi:[1,0,0]
	v_pk_mul_f32 v[52:53], v[58:59], v[52:53]
	v_pk_fma_f32 v[32:33], v[76:77], v[46:47], v[32:33] op_sel_hi:[1,0,1] neg_lo:[1,0,0] neg_hi:[1,0,0]
	v_pk_mul_f32 v[58:59], v[54:55], v[52:53]
	v_pk_fma_f32 v[52:53], v[54:55], v[52:53], v[54:55] neg_lo:[1,0,0] neg_hi:[1,0,0]
	v_pk_fma_f32 v[32:33], v[46:47], v[32:33], v[72:73] op_sel:[1,0,0]
	v_cndmask_b32_e32 v54, v52, v58, vcc
	v_cmp_gt_f32_e32 vcc, 0, v55
	v_cvt_pk_f16_f32 v52, v70, v71
	v_cvt_pk_f16_f32 v56, v88, v89
	v_cndmask_b32_e32 v53, v53, v59, vcc
	v_cvt_pk_f16_f32 v53, v54, v53
	v_pk_fma_f32 v[54:55], v[76:77], v[60:61], v[48:49] op_sel_hi:[1,0,1] neg_lo:[1,0,0] neg_hi:[1,0,0]
	v_xor_b32_e32 v49, 0x80000000, v79
	v_pk_fma_f32 v[54:55], v[60:61], v[54:55], v[72:73] op_sel:[1,0,0]
	v_xor_b32_e32 v48, 0x80000000, v78
	v_and_b32_e32 v59, 0x7fffffff, v55
	v_and_b32_e32 v58, 0x7fffffff, v54
	v_pk_fma_f32 v[58:59], v[58:59], s[8:9], 1.0 op_sel_hi:[1,0,0]
	v_pk_mul_f32 v[70:71], v[54:55], v[54:55]
	v_rcp_f32_e32 v58, v58
	v_rcp_f32_e32 v59, v59
	v_pk_fma_f32 v[50:51], v[48:49], v[60:61], v[50:51] op_sel_hi:[1,0,1]
	v_pk_mul_f32 v[70:71], v[70:71], s[16:17] op_sel_hi:[1,0]
	v_pk_fma_f32 v[50:51], v[60:61], v[50:51], v[74:75] op_sel:[1,0,0]
	v_pk_fma_f32 v[66:67], v[58:59], s[0:1], v[122:123] op_sel_hi:[1,0,0]
	v_exp_f32_e32 v70, v70
	v_pk_fma_f32 v[66:67], v[58:59], v[66:67], s[14:15] op_sel_hi:[1,1,0]
	v_exp_f32_e32 v71, v71
	v_pk_fma_f32 v[66:67], v[58:59], v[66:67], s[6:7] op_sel_hi:[1,1,0]
	v_and_b32_e32 v79, 0x7fffffff, v51
	v_and_b32_e32 v78, 0x7fffffff, v50
	v_pk_fma_f32 v[66:67], v[58:59], v[66:67], s[10:11] op_sel_hi:[1,1,0]
	v_pk_fma_f32 v[78:79], v[78:79], s[8:9], 1.0 op_sel_hi:[1,0,0]
	v_pk_mul_f32 v[58:59], v[58:59], v[66:67]
	v_rcp_f32_e32 v78, v78
	v_rcp_f32_e32 v79, v79
	v_pk_mul_f32 v[58:59], v[70:71], v[58:59]
	v_cmp_gt_f32_e32 vcc, 0, v54
	v_pk_mul_f32 v[70:71], v[54:55], v[58:59]
	v_pk_fma_f32 v[58:59], v[54:55], v[58:59], v[54:55] neg_lo:[1,0,0] neg_hi:[1,0,0]
	v_pk_mul_f32 v[66:67], v[50:51], v[50:51]
	v_cndmask_b32_e32 v70, v58, v70, vcc
	v_cmp_gt_f32_e32 vcc, 0, v55
	v_pk_fma_f32 v[54:55], v[78:79], s[0:1], v[122:123] op_sel_hi:[1,0,0]
	v_pk_fma_f32 v[42:43], v[48:49], v[62:63], v[42:43] op_sel_hi:[1,0,1]
	v_cndmask_b32_e32 v71, v59, v71, vcc
	v_pk_mul_f32 v[58:59], v[66:67], s[16:17] op_sel_hi:[1,0]
	v_pk_fma_f32 v[54:55], v[78:79], v[54:55], s[14:15] op_sel_hi:[1,1,0]
	v_exp_f32_e32 v58, v58
	v_exp_f32_e32 v59, v59
	v_pk_fma_f32 v[54:55], v[78:79], v[54:55], s[6:7] op_sel_hi:[1,1,0]
	v_cmp_gt_f32_e32 vcc, 0, v50
	v_pk_fma_f32 v[54:55], v[78:79], v[54:55], s[10:11] op_sel_hi:[1,1,0]
	v_pk_fma_f32 v[42:43], v[62:63], v[42:43], v[74:75] op_sel:[1,0,0]
	v_pk_mul_f32 v[54:55], v[78:79], v[54:55]
	v_and_b32_e32 v67, 0x7fffffff, v43
	v_pk_mul_f32 v[54:55], v[58:59], v[54:55]
	v_and_b32_e32 v66, 0x7fffffff, v42
	v_pk_mul_f32 v[58:59], v[50:51], v[54:55]
	v_pk_fma_f32 v[54:55], v[50:51], v[54:55], v[50:51] neg_lo:[1,0,0] neg_hi:[1,0,0]
	v_cvt_pk_f16_f32 v50, v70, v71
	v_cndmask_b32_e32 v54, v54, v58, vcc
	v_cmp_gt_f32_e32 vcc, 0, v51
	v_pk_fma_f32 v[66:67], v[66:67], s[8:9], 1.0 op_sel_hi:[1,0,0]
	v_pk_fma_f32 v[38:39], v[48:49], v[44:45], v[38:39] op_sel_hi:[1,0,1]
	v_cndmask_b32_e32 v51, v55, v59, vcc
	v_cvt_pk_f16_f32 v51, v54, v51
	v_and_b32_e32 v55, 0x7fffffff, v41
	v_and_b32_e32 v54, 0x7fffffff, v40
	v_pk_fma_f32 v[54:55], v[54:55], s[8:9], 1.0 op_sel_hi:[1,0,0]
	v_pk_mul_f32 v[58:59], v[40:41], v[40:41]
	v_rcp_f32_e32 v54, v54
	v_rcp_f32_e32 v55, v55
	ds_write2_b64 v121, v[68:69], v[50:51] offset0:8 offset1:12
	v_pk_mul_f32 v[58:59], v[58:59], s[16:17] op_sel_hi:[1,0]
	v_rcp_f32_e32 v66, v66
	v_pk_fma_f32 v[50:51], v[54:55], s[0:1], v[122:123] op_sel_hi:[1,0,0]
	v_exp_f32_e32 v58, v58
	v_pk_fma_f32 v[50:51], v[54:55], v[50:51], s[14:15] op_sel_hi:[1,1,0]
	v_exp_f32_e32 v59, v59
	v_pk_fma_f32 v[50:51], v[54:55], v[50:51], s[6:7] op_sel_hi:[1,1,0]
	v_rcp_f32_e32 v67, v67
	v_pk_fma_f32 v[50:51], v[54:55], v[50:51], s[10:11] op_sel_hi:[1,1,0]
	v_cmp_gt_f32_e32 vcc, 0, v40
	v_pk_mul_f32 v[50:51], v[54:55], v[50:51]
	v_pk_mul_f32 v[54:55], v[42:43], v[42:43]
	v_pk_mul_f32 v[50:51], v[58:59], v[50:51]
	v_pk_fma_f32 v[34:35], v[48:49], v[46:47], v[34:35] op_sel_hi:[1,0,1]
	v_pk_mul_f32 v[58:59], v[40:41], v[50:51]
	v_pk_fma_f32 v[50:51], v[40:41], v[50:51], v[40:41] neg_lo:[1,0,0] neg_hi:[1,0,0]
	v_pk_fma_f32 v[34:35], v[46:47], v[34:35], v[74:75] op_sel:[1,0,0]
	v_cndmask_b32_e32 v58, v50, v58, vcc
	v_cmp_gt_f32_e32 vcc, 0, v41
	v_pk_fma_f32 v[40:41], v[66:67], s[0:1], v[122:123] op_sel_hi:[1,0,0]
	s_nop 0
	v_cndmask_b32_e32 v59, v51, v59, vcc
	v_pk_mul_f32 v[50:51], v[54:55], s[16:17] op_sel_hi:[1,0]
	v_pk_fma_f32 v[40:41], v[66:67], v[40:41], s[14:15] op_sel_hi:[1,1,0]
	v_exp_f32_e32 v50, v50
	v_exp_f32_e32 v51, v51
	v_pk_fma_f32 v[40:41], v[66:67], v[40:41], s[6:7] op_sel_hi:[1,1,0]
	v_cmp_gt_f32_e32 vcc, 0, v42
	v_pk_fma_f32 v[40:41], v[66:67], v[40:41], s[10:11] op_sel_hi:[1,1,0]
	v_pk_fma_f32 v[54:55], v[44:45], v[38:39], v[74:75] op_sel:[1,0,0]
	v_pk_mul_f32 v[40:41], v[66:67], v[40:41]
	v_and_b32_e32 v69, 0x7fffffff, v55
	v_pk_mul_f32 v[40:41], v[50:51], v[40:41]
	v_and_b32_e32 v68, 0x7fffffff, v54
	v_pk_mul_f32 v[50:51], v[42:43], v[40:41]
	v_pk_fma_f32 v[40:41], v[42:43], v[40:41], v[42:43] neg_lo:[1,0,0] neg_hi:[1,0,0]
	v_pk_fma_f32 v[68:69], v[68:69], s[8:9], 1.0 op_sel_hi:[1,0,0]
	v_cndmask_b32_e32 v42, v40, v50, vcc
	v_cmp_gt_f32_e32 vcc, 0, v43
	v_cvt_pk_f16_f32 v40, v58, v59
	v_rcp_f32_e32 v68, v68
	v_cndmask_b32_e32 v41, v41, v51, vcc
	v_pk_fma_f32 v[50:51], v[44:45], v[36:37], v[72:73] op_sel:[1,0,0]
	v_cvt_pk_f16_f32 v41, v42, v41
	v_and_b32_e32 v37, 0x7fffffff, v51
	v_and_b32_e32 v36, 0x7fffffff, v50
	v_pk_fma_f32 v[36:37], v[36:37], s[8:9], 1.0 op_sel_hi:[1,0,0]
	ds_write2_b64 v94, v[64:65], v[40:41] offset0:40 offset1:44
	v_rcp_f32_e32 v36, v36
	v_rcp_f32_e32 v37, v37
	v_pk_mul_f32 v[40:41], v[50:51], v[50:51]
	v_rcp_f32_e32 v69, v69
	v_pk_mul_f32 v[40:41], v[40:41], s[16:17] op_sel_hi:[1,0]
	v_pk_fma_f32 v[38:39], v[36:37], s[0:1], v[122:123] op_sel_hi:[1,0,0]
	v_exp_f32_e32 v40, v40
	v_pk_fma_f32 v[38:39], v[36:37], v[38:39], s[14:15] op_sel_hi:[1,1,0]
	v_exp_f32_e32 v41, v41
	v_pk_fma_f32 v[38:39], v[36:37], v[38:39], s[6:7] op_sel_hi:[1,1,0]
	v_pk_mul_f32 v[58:59], v[54:55], v[54:55]
	v_pk_fma_f32 v[38:39], v[36:37], v[38:39], s[10:11] op_sel_hi:[1,1,0]
	v_cmp_gt_f32_e32 vcc, 0, v50
	v_pk_mul_f32 v[36:37], v[36:37], v[38:39]
	v_pk_mul_f32 v[58:59], v[58:59], s[16:17] op_sel_hi:[1,0]
	v_pk_mul_f32 v[36:37], v[40:41], v[36:37]
	global_load_dwordx4 v[40:43], v124, s[18:19] offset:256
	v_pk_mul_f32 v[64:65], v[50:51], v[36:37]
	v_pk_fma_f32 v[66:67], v[50:51], v[36:37], v[50:51] neg_lo:[1,0,0] neg_hi:[1,0,0]
	global_load_dwordx4 v[36:39], v124, s[20:21] offset:256
	v_cndmask_b32_e32 v64, v66, v64, vcc
	v_cmp_gt_f32_e32 vcc, 0, v51
	v_pk_fma_f32 v[50:51], v[68:69], s[0:1], v[122:123] op_sel_hi:[1,0,0]
	v_exp_f32_e32 v58, v58
	v_pk_fma_f32 v[50:51], v[68:69], v[50:51], s[14:15] op_sel_hi:[1,1,0]
	v_exp_f32_e32 v59, v59
	v_pk_fma_f32 v[50:51], v[68:69], v[50:51], s[6:7] op_sel_hi:[1,1,0]
	v_cndmask_b32_e32 v65, v67, v65, vcc
	v_pk_fma_f32 v[50:51], v[68:69], v[50:51], s[10:11] op_sel_hi:[1,1,0]
	v_cmp_gt_f32_e32 vcc, 0, v54
	v_pk_mul_f32 v[50:51], v[68:69], v[50:51]
	s_nop 0
	v_pk_mul_f32 v[50:51], v[58:59], v[50:51]
	s_nop 0
	v_pk_mul_f32 v[58:59], v[54:55], v[50:51]
	v_pk_fma_f32 v[50:51], v[54:55], v[50:51], v[54:55] neg_lo:[1,0,0] neg_hi:[1,0,0]
	s_nop 0
	v_cndmask_b32_e32 v54, v50, v58, vcc
	v_cmp_gt_f32_e32 vcc, 0, v55
	v_and_b32_e32 v55, 0x7fffffff, v33
	v_cvt_pk_f16_f32 v50, v64, v65
	v_cndmask_b32_e32 v51, v51, v59, vcc
	v_cvt_pk_f16_f32 v51, v54, v51
	v_and_b32_e32 v54, 0x7fffffff, v32
	v_pk_fma_f32 v[54:55], v[54:55], s[8:9], 1.0 op_sel_hi:[1,0,0]
	ds_write2_b64 v95, v[56:57], v[50:51] offset0:72 offset1:76
	v_rcp_f32_e32 v54, v54
	v_rcp_f32_e32 v55, v55
	v_pk_mul_f32 v[50:51], v[32:33], v[32:33]
	v_and_b32_e32 v57, 0x7fffffff, v35
	v_pk_mul_f32 v[50:51], v[50:51], s[16:17] op_sel_hi:[1,0]
	v_pk_fma_f32 v[48:49], v[54:55], s[0:1], v[122:123] op_sel_hi:[1,0,0]
	v_exp_f32_e32 v50, v50
	v_pk_fma_f32 v[48:49], v[54:55], v[48:49], s[14:15] op_sel_hi:[1,1,0]
	v_exp_f32_e32 v51, v51
	v_pk_fma_f32 v[48:49], v[54:55], v[48:49], s[6:7] op_sel_hi:[1,1,0]
	v_and_b32_e32 v56, 0x7fffffff, v34
	v_pk_fma_f32 v[48:49], v[54:55], v[48:49], s[10:11] op_sel_hi:[1,1,0]
	v_pk_fma_f32 v[56:57], v[56:57], s[8:9], 1.0 op_sel_hi:[1,0,0]
	v_pk_mul_f32 v[48:49], v[54:55], v[48:49]
	v_rcp_f32_e32 v56, v56
	v_rcp_f32_e32 v57, v57
	v_pk_mul_f32 v[48:49], v[50:51], v[48:49]
	v_cmp_gt_f32_e32 vcc, 0, v32
	v_pk_mul_f32 v[50:51], v[32:33], v[48:49]
	v_pk_fma_f32 v[48:49], v[32:33], v[48:49], v[32:33] neg_lo:[1,0,0] neg_hi:[1,0,0]
	v_pk_mul_f32 v[54:55], v[34:35], v[34:35]
	v_cndmask_b32_e32 v50, v48, v50, vcc
	v_cmp_gt_f32_e32 vcc, 0, v33
	v_pk_fma_f32 v[32:33], v[56:57], s[0:1], v[122:123] op_sel_hi:[1,0,0]
	s_nop 0
	v_cndmask_b32_e32 v51, v49, v51, vcc
	v_pk_mul_f32 v[48:49], v[54:55], s[16:17] op_sel_hi:[1,0]
	v_pk_fma_f32 v[32:33], v[56:57], v[32:33], s[14:15] op_sel_hi:[1,1,0]
	v_exp_f32_e32 v48, v48
	v_exp_f32_e32 v49, v49
	v_pk_fma_f32 v[32:33], v[56:57], v[32:33], s[6:7] op_sel_hi:[1,1,0]
	v_cmp_gt_f32_e32 vcc, 0, v34
	v_pk_fma_f32 v[32:33], v[56:57], v[32:33], s[10:11] op_sel_hi:[1,1,0]
	s_nop 0
	v_pk_mul_f32 v[32:33], v[56:57], v[32:33]
	s_nop 0
	v_pk_mul_f32 v[32:33], v[48:49], v[32:33]
	s_nop 0
	v_pk_mul_f32 v[48:49], v[34:35], v[32:33]
	v_pk_fma_f32 v[32:33], v[34:35], v[32:33], v[34:35] neg_lo:[1,0,0] neg_hi:[1,0,0]
	s_nop 0
	v_cndmask_b32_e32 v34, v32, v48, vcc
	v_cmp_gt_f32_e32 vcc, 0, v35
	v_cvt_pk_f16_f32 v32, v50, v51
	s_nop 0
	v_cndmask_b32_e32 v33, v33, v49, vcc
	v_cvt_pk_f16_f32 v33, v34, v33
	global_load_dwordx4 v[48:51], v124, s[18:19] offset:320
	ds_write2_b64 v90, v[52:53], v[32:33] offset0:104 offset1:108
	global_load_dwordx4 v[32:35], v124, s[20:21] offset:320
	s_waitcnt vmcnt(3)
	v_pk_fma_f32 v[28:29], v[40:41], v[60:61], v[28:29] op_sel_hi:[1,0,1] neg_lo:[1,0,0] neg_hi:[1,0,0]
	v_xor_b32_e32 v43, 0x80000000, v43
	v_xor_b32_e32 v42, 0x80000000, v42
	s_waitcnt vmcnt(2)
	v_pk_fma_f32 v[28:29], v[60:61], v[28:29], v[36:37] op_sel:[1,0,0]
	v_pk_fma_f32 v[30:31], v[42:43], v[60:61], v[30:31] op_sel_hi:[1,0,1]
	v_and_b32_e32 v53, 0x7fffffff, v29
	v_and_b32_e32 v52, 0x7fffffff, v28
	v_pk_fma_f32 v[52:53], v[52:53], s[8:9], 1.0 op_sel_hi:[1,0,0]
	v_pk_mul_f32 v[56:57], v[28:29], v[28:29]
	v_rcp_f32_e32 v52, v52
	v_rcp_f32_e32 v53, v53
	v_pk_mul_f32 v[56:57], v[56:57], s[16:17] op_sel_hi:[1,0]
	v_pk_fma_f32 v[30:31], v[60:61], v[30:31], v[38:39] op_sel:[1,0,0]
	v_exp_f32_e32 v56, v56
	v_pk_fma_f32 v[54:55], v[52:53], s[0:1], v[122:123] op_sel_hi:[1,0,0]
	v_exp_f32_e32 v57, v57
	v_pk_fma_f32 v[54:55], v[52:53], v[54:55], s[14:15] op_sel_hi:[1,1,0]
	v_and_b32_e32 v59, 0x7fffffff, v31
	v_pk_fma_f32 v[54:55], v[52:53], v[54:55], s[6:7] op_sel_hi:[1,1,0]
	v_and_b32_e32 v58, 0x7fffffff, v30
	v_pk_fma_f32 v[54:55], v[52:53], v[54:55], s[10:11] op_sel_hi:[1,1,0]
	v_pk_fma_f32 v[58:59], v[58:59], s[8:9], 1.0 op_sel_hi:[1,0,0]
	v_pk_mul_f32 v[52:53], v[52:53], v[54:55]
	v_rcp_f32_e32 v58, v58
	v_rcp_f32_e32 v59, v59
	v_pk_mul_f32 v[52:53], v[56:57], v[52:53]
	v_cmp_gt_f32_e32 vcc, 0, v28
	v_pk_mul_f32 v[56:57], v[28:29], v[52:53]
	v_pk_fma_f32 v[52:53], v[28:29], v[52:53], v[28:29] neg_lo:[1,0,0] neg_hi:[1,0,0]
	v_pk_mul_f32 v[54:55], v[30:31], v[30:31]
	v_cndmask_b32_e32 v56, v52, v56, vcc
	v_cmp_gt_f32_e32 vcc, 0, v29
	v_pk_fma_f32 v[28:29], v[58:59], s[0:1], v[122:123] op_sel_hi:[1,0,0]
	v_pk_fma_f32 v[24:25], v[40:41], v[62:63], v[24:25] op_sel_hi:[1,0,1] neg_lo:[1,0,0] neg_hi:[1,0,0]
	v_cndmask_b32_e32 v57, v53, v57, vcc
	v_pk_mul_f32 v[52:53], v[54:55], s[16:17] op_sel_hi:[1,0]
	v_pk_fma_f32 v[28:29], v[58:59], v[28:29], s[14:15] op_sel_hi:[1,1,0]
	v_exp_f32_e32 v52, v52
	v_exp_f32_e32 v53, v53
	v_pk_fma_f32 v[28:29], v[58:59], v[28:29], s[6:7] op_sel_hi:[1,1,0]
	v_cmp_gt_f32_e32 vcc, 0, v30
	v_pk_fma_f32 v[28:29], v[58:59], v[28:29], s[10:11] op_sel_hi:[1,1,0]
	v_pk_fma_f32 v[24:25], v[62:63], v[24:25], v[36:37] op_sel:[1,0,0]
	v_pk_mul_f32 v[28:29], v[58:59], v[28:29]
	v_pk_mul_f32 v[54:55], v[24:25], v[24:25]
	v_pk_mul_f32 v[28:29], v[52:53], v[28:29]
	v_pk_fma_f32 v[26:27], v[42:43], v[62:63], v[26:27] op_sel_hi:[1,0,1]
	v_pk_mul_f32 v[52:53], v[30:31], v[28:29]
	v_pk_fma_f32 v[28:29], v[30:31], v[28:29], v[30:31] neg_lo:[1,0,0] neg_hi:[1,0,0]
	v_and_b32_e32 v30, 0x7fffffff, v24
	v_cndmask_b32_e32 v52, v28, v52, vcc
	v_cmp_gt_f32_e32 vcc, 0, v31
	v_and_b32_e32 v31, 0x7fffffff, v25
	v_pk_fma_f32 v[30:31], v[30:31], s[8:9], 1.0 op_sel_hi:[1,0,0]
	v_cndmask_b32_e32 v29, v29, v53, vcc
	v_rcp_f32_e32 v30, v30
	v_rcp_f32_e32 v31, v31
	v_cvt_pk_f16_f32 v29, v52, v29
	v_pk_mul_f32 v[54:55], v[54:55], s[16:17] op_sel_hi:[1,0]
	v_pk_fma_f32 v[26:27], v[62:63], v[26:27], v[38:39] op_sel:[1,0,0]
	v_pk_fma_f32 v[52:53], v[30:31], s[0:1], v[122:123] op_sel_hi:[1,0,0]
	v_exp_f32_e32 v54, v54
	v_pk_fma_f32 v[52:53], v[30:31], v[52:53], s[14:15] op_sel_hi:[1,1,0]
	v_exp_f32_e32 v55, v55
	v_cvt_pk_f16_f32 v28, v56, v57
	v_pk_fma_f32 v[52:53], v[30:31], v[52:53], s[6:7] op_sel_hi:[1,1,0]
	v_and_b32_e32 v57, 0x7fffffff, v27
	v_and_b32_e32 v56, 0x7fffffff, v26
	v_pk_fma_f32 v[52:53], v[30:31], v[52:53], s[10:11] op_sel_hi:[1,1,0]
	v_pk_fma_f32 v[56:57], v[56:57], s[8:9], 1.0 op_sel_hi:[1,0,0]
	v_pk_mul_f32 v[30:31], v[30:31], v[52:53]
	v_rcp_f32_e32 v56, v56
	v_rcp_f32_e32 v57, v57
	v_pk_mul_f32 v[30:31], v[54:55], v[30:31]
	v_cmp_gt_f32_e32 vcc, 0, v24
	v_pk_mul_f32 v[54:55], v[24:25], v[30:31]
	v_pk_fma_f32 v[30:31], v[24:25], v[30:31], v[24:25] neg_lo:[1,0,0] neg_hi:[1,0,0]
	v_pk_mul_f32 v[52:53], v[26:27], v[26:27]
	v_cndmask_b32_e32 v54, v30, v54, vcc
	v_cmp_gt_f32_e32 vcc, 0, v25
	v_pk_fma_f32 v[24:25], v[56:57], s[0:1], v[122:123] op_sel_hi:[1,0,0]
	v_pk_fma_f32 v[20:21], v[40:41], v[44:45], v[20:21] op_sel_hi:[1,0,1] neg_lo:[1,0,0] neg_hi:[1,0,0]
	v_cndmask_b32_e32 v55, v31, v55, vcc
	v_pk_mul_f32 v[30:31], v[52:53], s[16:17] op_sel_hi:[1,0]
	v_pk_fma_f32 v[24:25], v[56:57], v[24:25], s[14:15] op_sel_hi:[1,1,0]
	v_exp_f32_e32 v30, v30
	v_exp_f32_e32 v31, v31
	v_pk_fma_f32 v[24:25], v[56:57], v[24:25], s[6:7] op_sel_hi:[1,1,0]
	v_cmp_gt_f32_e32 vcc, 0, v26
	v_pk_fma_f32 v[24:25], v[56:57], v[24:25], s[10:11] op_sel_hi:[1,1,0]
	v_pk_fma_f32 v[20:21], v[44:45], v[20:21], v[36:37] op_sel:[1,0,0]
	v_pk_mul_f32 v[24:25], v[56:57], v[24:25]
	v_pk_mul_f32 v[52:53], v[20:21], v[20:21]
	v_pk_mul_f32 v[24:25], v[30:31], v[24:25]
	v_pk_fma_f32 v[22:23], v[42:43], v[44:45], v[22:23] op_sel_hi:[1,0,1]
	v_pk_mul_f32 v[30:31], v[26:27], v[24:25]
	v_pk_fma_f32 v[24:25], v[26:27], v[24:25], v[26:27] neg_lo:[1,0,0] neg_hi:[1,0,0]
	v_and_b32_e32 v26, 0x7fffffff, v20
	v_cndmask_b32_e32 v30, v24, v30, vcc
	v_cmp_gt_f32_e32 vcc, 0, v27
	v_and_b32_e32 v27, 0x7fffffff, v21
	v_pk_fma_f32 v[26:27], v[26:27], s[8:9], 1.0 op_sel_hi:[1,0,0]
	v_cndmask_b32_e32 v25, v25, v31, vcc
	v_rcp_f32_e32 v26, v26
	v_rcp_f32_e32 v27, v27
	v_cvt_pk_f16_f32 v25, v30, v25
	v_pk_mul_f32 v[52:53], v[52:53], s[16:17] op_sel_hi:[1,0]
	v_pk_fma_f32 v[22:23], v[44:45], v[22:23], v[38:39] op_sel:[1,0,0]
	v_pk_fma_f32 v[30:31], v[26:27], s[0:1], v[122:123] op_sel_hi:[1,0,0]
	v_exp_f32_e32 v52, v52
	v_pk_fma_f32 v[30:31], v[26:27], v[30:31], s[14:15] op_sel_hi:[1,1,0]
	v_exp_f32_e32 v53, v53
	v_cvt_pk_f16_f32 v24, v54, v55
	v_pk_fma_f32 v[30:31], v[26:27], v[30:31], s[6:7] op_sel_hi:[1,1,0]
	v_and_b32_e32 v55, 0x7fffffff, v23
	v_and_b32_e32 v54, 0x7fffffff, v22
	v_pk_fma_f32 v[30:31], v[26:27], v[30:31], s[10:11] op_sel_hi:[1,1,0]
	v_pk_fma_f32 v[54:55], v[54:55], s[8:9], 1.0 op_sel_hi:[1,0,0]
	v_pk_mul_f32 v[26:27], v[26:27], v[30:31]
	v_rcp_f32_e32 v54, v54
	v_rcp_f32_e32 v55, v55
	v_pk_mul_f32 v[26:27], v[52:53], v[26:27]
	v_cmp_gt_f32_e32 vcc, 0, v20
	v_pk_mul_f32 v[52:53], v[20:21], v[26:27]
	v_pk_fma_f32 v[26:27], v[20:21], v[26:27], v[20:21] neg_lo:[1,0,0] neg_hi:[1,0,0]
	v_pk_mul_f32 v[30:31], v[22:23], v[22:23]
	v_cndmask_b32_e32 v52, v26, v52, vcc
	v_cmp_gt_f32_e32 vcc, 0, v21
	v_pk_fma_f32 v[20:21], v[54:55], s[0:1], v[122:123] op_sel_hi:[1,0,0]
	v_pk_fma_f32 v[16:17], v[40:41], v[46:47], v[16:17] op_sel_hi:[1,0,1] neg_lo:[1,0,0] neg_hi:[1,0,0]
	v_cndmask_b32_e32 v53, v27, v53, vcc
	v_pk_mul_f32 v[26:27], v[30:31], s[16:17] op_sel_hi:[1,0]
	v_pk_fma_f32 v[20:21], v[54:55], v[20:21], s[14:15] op_sel_hi:[1,1,0]
	v_exp_f32_e32 v26, v26
	v_exp_f32_e32 v27, v27
	v_pk_fma_f32 v[20:21], v[54:55], v[20:21], s[6:7] op_sel_hi:[1,1,0]
	v_cmp_gt_f32_e32 vcc, 0, v22
	v_pk_fma_f32 v[20:21], v[54:55], v[20:21], s[10:11] op_sel_hi:[1,1,0]
	v_pk_fma_f32 v[16:17], v[46:47], v[16:17], v[36:37] op_sel:[1,0,0]
	v_pk_mul_f32 v[20:21], v[54:55], v[20:21]
	v_pk_mul_f32 v[30:31], v[16:17], v[16:17]
	v_pk_mul_f32 v[20:21], v[26:27], v[20:21]
	v_pk_fma_f32 v[18:19], v[42:43], v[46:47], v[18:19] op_sel_hi:[1,0,1]
	v_pk_mul_f32 v[26:27], v[22:23], v[20:21]
	v_pk_fma_f32 v[20:21], v[22:23], v[20:21], v[22:23] neg_lo:[1,0,0] neg_hi:[1,0,0]
	v_and_b32_e32 v22, 0x7fffffff, v16
	v_cndmask_b32_e32 v26, v20, v26, vcc
	v_cmp_gt_f32_e32 vcc, 0, v23
	v_and_b32_e32 v23, 0x7fffffff, v17
	v_pk_fma_f32 v[22:23], v[22:23], s[8:9], 1.0 op_sel_hi:[1,0,0]
	v_cndmask_b32_e32 v21, v21, v27, vcc
	v_rcp_f32_e32 v22, v22
	v_rcp_f32_e32 v23, v23
	v_cvt_pk_f16_f32 v21, v26, v21
	v_pk_mul_f32 v[30:31], v[30:31], s[16:17] op_sel_hi:[1,0]
	v_pk_fma_f32 v[18:19], v[46:47], v[18:19], v[38:39] op_sel:[1,0,0]
	v_pk_fma_f32 v[26:27], v[22:23], s[0:1], v[122:123] op_sel_hi:[1,0,0]
	v_exp_f32_e32 v30, v30
	v_pk_fma_f32 v[26:27], v[22:23], v[26:27], s[14:15] op_sel_hi:[1,1,0]
	v_exp_f32_e32 v31, v31
	v_pk_fma_f32 v[26:27], v[22:23], v[26:27], s[6:7] op_sel_hi:[1,1,0]
	v_and_b32_e32 v37, 0x7fffffff, v19
	v_and_b32_e32 v36, 0x7fffffff, v18
	v_pk_fma_f32 v[26:27], v[22:23], v[26:27], s[10:11] op_sel_hi:[1,1,0]
	v_pk_fma_f32 v[36:37], v[36:37], s[8:9], 1.0 op_sel_hi:[1,0,0]
	v_pk_mul_f32 v[22:23], v[22:23], v[26:27]
	v_rcp_f32_e32 v36, v36
	v_rcp_f32_e32 v37, v37
	v_pk_mul_f32 v[22:23], v[30:31], v[22:23]
	v_cmp_gt_f32_e32 vcc, 0, v16
	v_pk_mul_f32 v[30:31], v[16:17], v[22:23]
	v_pk_fma_f32 v[22:23], v[16:17], v[22:23], v[16:17] neg_lo:[1,0,0] neg_hi:[1,0,0]
	v_pk_mul_f32 v[26:27], v[18:19], v[18:19]
	v_cndmask_b32_e32 v30, v22, v30, vcc
	v_cmp_gt_f32_e32 vcc, 0, v17
	v_pk_fma_f32 v[16:17], v[36:37], s[0:1], v[122:123] op_sel_hi:[1,0,0]
	s_waitcnt vmcnt(1)
	v_pk_fma_f32 v[8:9], v[48:49], v[62:63], v[8:9] op_sel_hi:[1,0,1] neg_lo:[1,0,0] neg_hi:[1,0,0]
	v_cndmask_b32_e32 v31, v23, v31, vcc
	v_pk_mul_f32 v[22:23], v[26:27], s[16:17] op_sel_hi:[1,0]
	v_pk_fma_f32 v[16:17], v[36:37], v[16:17], s[14:15] op_sel_hi:[1,1,0]
	v_exp_f32_e32 v22, v22
	v_exp_f32_e32 v23, v23
	v_pk_fma_f32 v[16:17], v[36:37], v[16:17], s[6:7] op_sel_hi:[1,1,0]
	v_cmp_gt_f32_e32 vcc, 0, v18
	v_pk_fma_f32 v[16:17], v[36:37], v[16:17], s[10:11] op_sel_hi:[1,1,0]
	s_waitcnt vmcnt(0)
	v_pk_fma_f32 v[8:9], v[62:63], v[8:9], v[32:33] op_sel:[1,0,0]
	v_pk_mul_f32 v[16:17], v[36:37], v[16:17]
	v_pk_fma_f32 v[4:5], v[48:49], v[44:45], v[4:5] op_sel_hi:[1,0,1] neg_lo:[1,0,0] neg_hi:[1,0,0]
	v_pk_mul_f32 v[16:17], v[22:23], v[16:17]
	v_pk_fma_f32 v[4:5], v[44:45], v[4:5], v[32:33] op_sel:[1,0,0]
	v_pk_mul_f32 v[22:23], v[18:19], v[16:17]
	v_pk_fma_f32 v[16:17], v[18:19], v[16:17], v[18:19] neg_lo:[1,0,0] neg_hi:[1,0,0]
	v_pk_fma_f32 v[0:1], v[48:49], v[46:47], v[0:1] op_sel_hi:[1,0,1] neg_lo:[1,0,0] neg_hi:[1,0,0]
	v_cndmask_b32_e32 v18, v16, v22, vcc
	v_cmp_gt_f32_e32 vcc, 0, v19
	v_cvt_pk_f16_f32 v16, v30, v31
	v_pk_fma_f32 v[0:1], v[46:47], v[0:1], v[32:33] op_sel:[1,0,0]
	v_cndmask_b32_e32 v17, v17, v23, vcc
	v_cvt_pk_f16_f32 v17, v18, v17
	v_pk_fma_f32 v[18:19], v[48:49], v[60:61], v[12:13] op_sel_hi:[1,0,1] neg_lo:[1,0,0] neg_hi:[1,0,0]
	v_xor_b32_e32 v13, 0x80000000, v51
	v_pk_fma_f32 v[18:19], v[60:61], v[18:19], v[32:33] op_sel:[1,0,0]
	v_xor_b32_e32 v12, 0x80000000, v50
	v_and_b32_e32 v23, 0x7fffffff, v19
	v_and_b32_e32 v22, 0x7fffffff, v18
	v_pk_fma_f32 v[22:23], v[22:23], s[8:9], 1.0 op_sel_hi:[1,0,0]
	v_pk_mul_f32 v[30:31], v[18:19], v[18:19]
	v_rcp_f32_e32 v22, v22
	v_rcp_f32_e32 v23, v23
	v_pk_fma_f32 v[14:15], v[12:13], v[60:61], v[14:15] op_sel_hi:[1,0,1]
	v_pk_mul_f32 v[30:31], v[30:31], s[16:17] op_sel_hi:[1,0]
	v_pk_fma_f32 v[14:15], v[60:61], v[14:15], v[34:35] op_sel:[1,0,0]
	v_pk_fma_f32 v[26:27], v[22:23], s[0:1], v[122:123] op_sel_hi:[1,0,0]
	v_exp_f32_e32 v30, v30
	v_pk_fma_f32 v[26:27], v[22:23], v[26:27], s[14:15] op_sel_hi:[1,1,0]
	v_exp_f32_e32 v31, v31
	v_pk_fma_f32 v[26:27], v[22:23], v[26:27], s[6:7] op_sel_hi:[1,1,0]
	v_and_b32_e32 v37, 0x7fffffff, v15
	v_and_b32_e32 v36, 0x7fffffff, v14
	v_pk_fma_f32 v[26:27], v[22:23], v[26:27], s[10:11] op_sel_hi:[1,1,0]
	v_pk_fma_f32 v[36:37], v[36:37], s[8:9], 1.0 op_sel_hi:[1,0,0]
	v_pk_mul_f32 v[22:23], v[22:23], v[26:27]
	v_rcp_f32_e32 v36, v36
	v_rcp_f32_e32 v37, v37
	v_pk_mul_f32 v[22:23], v[30:31], v[22:23]
	v_cmp_gt_f32_e32 vcc, 0, v18
	v_pk_mul_f32 v[30:31], v[18:19], v[22:23]
	v_pk_fma_f32 v[22:23], v[18:19], v[22:23], v[18:19] neg_lo:[1,0,0] neg_hi:[1,0,0]
	v_pk_mul_f32 v[26:27], v[14:15], v[14:15]
	v_cndmask_b32_e32 v30, v22, v30, vcc
	v_cmp_gt_f32_e32 vcc, 0, v19
	v_pk_fma_f32 v[18:19], v[36:37], s[0:1], v[122:123] op_sel_hi:[1,0,0]
	v_pk_fma_f32 v[10:11], v[12:13], v[62:63], v[10:11] op_sel_hi:[1,0,1]
	v_cndmask_b32_e32 v31, v23, v31, vcc
	v_pk_mul_f32 v[22:23], v[26:27], s[16:17] op_sel_hi:[1,0]
	v_pk_fma_f32 v[18:19], v[36:37], v[18:19], s[14:15] op_sel_hi:[1,1,0]
	v_exp_f32_e32 v22, v22
	v_exp_f32_e32 v23, v23
	v_pk_fma_f32 v[18:19], v[36:37], v[18:19], s[6:7] op_sel_hi:[1,1,0]
	v_cmp_gt_f32_e32 vcc, 0, v14
	v_pk_fma_f32 v[18:19], v[36:37], v[18:19], s[10:11] op_sel_hi:[1,1,0]
	v_pk_fma_f32 v[10:11], v[62:63], v[10:11], v[34:35] op_sel:[1,0,0]
	v_pk_mul_f32 v[18:19], v[36:37], v[18:19]
	v_and_b32_e32 v27, 0x7fffffff, v11
	v_pk_mul_f32 v[18:19], v[22:23], v[18:19]
	v_and_b32_e32 v26, 0x7fffffff, v10
	v_pk_mul_f32 v[22:23], v[14:15], v[18:19]
	v_pk_fma_f32 v[18:19], v[14:15], v[18:19], v[14:15] neg_lo:[1,0,0] neg_hi:[1,0,0]
	v_cvt_pk_f16_f32 v14, v30, v31
	v_cndmask_b32_e32 v18, v18, v22, vcc
	v_cmp_gt_f32_e32 vcc, 0, v15
	v_pk_fma_f32 v[26:27], v[26:27], s[8:9], 1.0 op_sel_hi:[1,0,0]
	v_pk_fma_f32 v[6:7], v[12:13], v[44:45], v[6:7] op_sel_hi:[1,0,1]
	v_cndmask_b32_e32 v15, v19, v23, vcc
	v_cvt_pk_f16_f32 v15, v18, v15
	v_and_b32_e32 v19, 0x7fffffff, v9
	v_and_b32_e32 v18, 0x7fffffff, v8
	v_pk_fma_f32 v[18:19], v[18:19], s[8:9], 1.0 op_sel_hi:[1,0,0]
	v_pk_mul_f32 v[22:23], v[8:9], v[8:9]
	v_rcp_f32_e32 v18, v18
	v_rcp_f32_e32 v19, v19
	ds_write2_b64 v121, v[28:29], v[14:15] offset0:16 offset1:20
	v_pk_mul_f32 v[22:23], v[22:23], s[16:17] op_sel_hi:[1,0]
	v_rcp_f32_e32 v26, v26
	v_pk_fma_f32 v[14:15], v[18:19], s[0:1], v[122:123] op_sel_hi:[1,0,0]
	v_exp_f32_e32 v22, v22
	v_pk_fma_f32 v[14:15], v[18:19], v[14:15], s[14:15] op_sel_hi:[1,1,0]
	v_exp_f32_e32 v23, v23
	v_pk_fma_f32 v[14:15], v[18:19], v[14:15], s[6:7] op_sel_hi:[1,1,0]
	v_rcp_f32_e32 v27, v27
	v_pk_fma_f32 v[14:15], v[18:19], v[14:15], s[10:11] op_sel_hi:[1,1,0]
	v_cmp_gt_f32_e32 vcc, 0, v8
	v_pk_mul_f32 v[14:15], v[18:19], v[14:15]
	v_pk_mul_f32 v[18:19], v[10:11], v[10:11]
	v_pk_mul_f32 v[14:15], v[22:23], v[14:15]
	v_pk_fma_f32 v[6:7], v[44:45], v[6:7], v[34:35] op_sel:[1,0,0]
	v_pk_mul_f32 v[22:23], v[8:9], v[14:15]
	v_pk_fma_f32 v[14:15], v[8:9], v[14:15], v[8:9] neg_lo:[1,0,0] neg_hi:[1,0,0]
	v_cvt_pk_f16_f32 v20, v52, v53
	v_cndmask_b32_e32 v22, v14, v22, vcc
	v_cmp_gt_f32_e32 vcc, 0, v9
	v_pk_fma_f32 v[8:9], v[26:27], s[0:1], v[122:123] op_sel_hi:[1,0,0]
	v_pk_fma_f32 v[2:3], v[12:13], v[46:47], v[2:3] op_sel_hi:[1,0,1]
	v_cndmask_b32_e32 v23, v15, v23, vcc
	v_pk_mul_f32 v[14:15], v[18:19], s[16:17] op_sel_hi:[1,0]
	v_pk_fma_f32 v[8:9], v[26:27], v[8:9], s[14:15] op_sel_hi:[1,1,0]
	v_exp_f32_e32 v14, v14
	v_exp_f32_e32 v15, v15
	v_pk_fma_f32 v[8:9], v[26:27], v[8:9], s[6:7] op_sel_hi:[1,1,0]
	v_cmp_gt_f32_e32 vcc, 0, v10
	v_pk_fma_f32 v[8:9], v[26:27], v[8:9], s[10:11] op_sel_hi:[1,1,0]
	v_and_b32_e32 v19, 0x7fffffff, v7
	v_pk_mul_f32 v[8:9], v[26:27], v[8:9]
	v_and_b32_e32 v18, 0x7fffffff, v6
	v_pk_mul_f32 v[8:9], v[14:15], v[8:9]
	v_pk_fma_f32 v[18:19], v[18:19], s[8:9], 1.0 op_sel_hi:[1,0,0]
	v_pk_mul_f32 v[14:15], v[10:11], v[8:9]
	v_pk_fma_f32 v[8:9], v[10:11], v[8:9], v[10:11] neg_lo:[1,0,0] neg_hi:[1,0,0]
	v_rcp_f32_e32 v18, v18
	v_cndmask_b32_e32 v10, v8, v14, vcc
	v_cmp_gt_f32_e32 vcc, 0, v11
	v_and_b32_e32 v11, 0x7fffffff, v5
	v_cvt_pk_f16_f32 v8, v22, v23
	v_cndmask_b32_e32 v9, v9, v15, vcc
	v_cvt_pk_f16_f32 v9, v10, v9
	v_and_b32_e32 v10, 0x7fffffff, v4
	v_pk_fma_f32 v[10:11], v[10:11], s[8:9], 1.0 op_sel_hi:[1,0,0]
	v_pk_mul_f32 v[14:15], v[4:5], v[4:5]
	v_rcp_f32_e32 v10, v10
	v_rcp_f32_e32 v11, v11
	ds_write2_b64 v94, v[24:25], v[8:9] offset0:48 offset1:52
	v_pk_mul_f32 v[14:15], v[14:15], s[16:17] op_sel_hi:[1,0]
	v_rcp_f32_e32 v19, v19
	v_pk_fma_f32 v[8:9], v[10:11], s[0:1], v[122:123] op_sel_hi:[1,0,0]
	v_exp_f32_e32 v14, v14
	v_pk_fma_f32 v[8:9], v[10:11], v[8:9], s[14:15] op_sel_hi:[1,1,0]
	v_exp_f32_e32 v15, v15
	v_pk_fma_f32 v[8:9], v[10:11], v[8:9], s[6:7] op_sel_hi:[1,1,0]
	v_cmp_gt_f32_e32 vcc, 0, v4
	v_pk_fma_f32 v[8:9], v[10:11], v[8:9], s[10:11] op_sel_hi:[1,1,0]
	v_pk_fma_f32 v[2:3], v[46:47], v[2:3], v[34:35] op_sel:[1,0,0]
	v_pk_mul_f32 v[8:9], v[10:11], v[8:9]
	v_pk_mul_f32 v[10:11], v[6:7], v[6:7]
	v_pk_mul_f32 v[8:9], v[14:15], v[8:9]
	s_nop 0
	v_pk_mul_f32 v[14:15], v[4:5], v[8:9]
	v_pk_fma_f32 v[8:9], v[4:5], v[8:9], v[4:5] neg_lo:[1,0,0] neg_hi:[1,0,0]
	s_nop 0
	v_cndmask_b32_e32 v14, v8, v14, vcc
	v_cmp_gt_f32_e32 vcc, 0, v5
	v_pk_fma_f32 v[4:5], v[18:19], s[0:1], v[122:123] op_sel_hi:[1,0,0]
	s_nop 0
	v_cndmask_b32_e32 v15, v9, v15, vcc
	v_pk_mul_f32 v[8:9], v[10:11], s[16:17] op_sel_hi:[1,0]
	v_pk_fma_f32 v[4:5], v[18:19], v[4:5], s[14:15] op_sel_hi:[1,1,0]
	v_exp_f32_e32 v8, v8
	v_exp_f32_e32 v9, v9
	v_pk_fma_f32 v[4:5], v[18:19], v[4:5], s[6:7] op_sel_hi:[1,1,0]
	v_cmp_gt_f32_e32 vcc, 0, v6
	v_pk_fma_f32 v[4:5], v[18:19], v[4:5], s[10:11] op_sel_hi:[1,1,0]
	v_and_b32_e32 v11, 0x7fffffff, v3
	v_pk_mul_f32 v[4:5], v[18:19], v[4:5]
	v_and_b32_e32 v10, 0x7fffffff, v2
	v_pk_mul_f32 v[4:5], v[8:9], v[4:5]
	v_pk_fma_f32 v[10:11], v[10:11], s[8:9], 1.0 op_sel_hi:[1,0,0]
	v_pk_mul_f32 v[8:9], v[6:7], v[4:5]
	v_pk_fma_f32 v[4:5], v[6:7], v[4:5], v[6:7] neg_lo:[1,0,0] neg_hi:[1,0,0]
	v_rcp_f32_e32 v10, v10
	v_cndmask_b32_e32 v6, v4, v8, vcc
	v_cmp_gt_f32_e32 vcc, 0, v7
	v_and_b32_e32 v7, 0x7fffffff, v1
	v_cvt_pk_f16_f32 v4, v14, v15
	v_cndmask_b32_e32 v5, v5, v9, vcc
	v_cvt_pk_f16_f32 v5, v6, v5
	v_and_b32_e32 v6, 0x7fffffff, v0
	v_pk_fma_f32 v[6:7], v[6:7], s[8:9], 1.0 op_sel_hi:[1,0,0]
	v_pk_mul_f32 v[8:9], v[0:1], v[0:1]
	v_rcp_f32_e32 v6, v6
	v_rcp_f32_e32 v7, v7
	ds_write2_b64 v95, v[20:21], v[4:5] offset0:80 offset1:84
	v_pk_mul_f32 v[8:9], v[8:9], s[16:17] op_sel_hi:[1,0]
	v_rcp_f32_e32 v11, v11
	v_pk_fma_f32 v[4:5], v[6:7], s[0:1], v[122:123] op_sel_hi:[1,0,0]
	v_exp_f32_e32 v8, v8
	v_pk_fma_f32 v[4:5], v[6:7], v[4:5], s[14:15] op_sel_hi:[1,1,0]
	v_exp_f32_e32 v9, v9
	v_pk_fma_f32 v[4:5], v[6:7], v[4:5], s[6:7] op_sel_hi:[1,1,0]
	v_cmp_gt_f32_e32 vcc, 0, v0
	v_pk_fma_f32 v[4:5], v[6:7], v[4:5], s[10:11] op_sel_hi:[1,1,0]
	s_nop 0
	v_pk_mul_f32 v[4:5], v[6:7], v[4:5]
	v_pk_mul_f32 v[6:7], v[2:3], v[2:3]
	v_pk_mul_f32 v[4:5], v[8:9], v[4:5]
	s_nop 0
	v_pk_mul_f32 v[8:9], v[0:1], v[4:5]
	v_pk_fma_f32 v[4:5], v[0:1], v[4:5], v[0:1] neg_lo:[1,0,0] neg_hi:[1,0,0]
	s_nop 0
	v_cndmask_b32_e32 v8, v4, v8, vcc
	v_cmp_gt_f32_e32 vcc, 0, v1
	v_pk_fma_f32 v[0:1], v[10:11], s[0:1], v[122:123] op_sel_hi:[1,0,0]
	s_lshl_b64 s[0:1], s[2:3], 1
	v_cndmask_b32_e32 v9, v5, v9, vcc
	v_pk_mul_f32 v[4:5], v[6:7], s[16:17] op_sel_hi:[1,0]
	v_pk_fma_f32 v[0:1], v[10:11], v[0:1], s[14:15] op_sel_hi:[1,1,0]
	v_exp_f32_e32 v4, v4
	v_exp_f32_e32 v5, v5
	v_pk_fma_f32 v[0:1], v[10:11], v[0:1], s[6:7] op_sel_hi:[1,1,0]
	v_cmp_gt_f32_e32 vcc, 0, v2
	v_pk_fma_f32 v[0:1], v[10:11], v[0:1], s[10:11] op_sel_hi:[1,1,0]
	s_mov_b32 s2, 0x2aaaaaab
	v_pk_mul_f32 v[0:1], v[10:11], v[0:1]
	s_add_u32 s0, s4, s0
	v_pk_mul_f32 v[0:1], v[4:5], v[0:1]
	s_movk_i32 s3, 0xffe8
	v_pk_mul_f32 v[4:5], v[2:3], v[0:1]
	v_pk_fma_f32 v[0:1], v[2:3], v[0:1], v[2:3] neg_lo:[1,0,0] neg_hi:[1,0,0]
	s_addc_u32 s1, s5, s1
	v_cndmask_b32_e32 v2, v0, v4, vcc
	v_cmp_gt_f32_e32 vcc, 0, v3
	v_cvt_pk_f16_f32 v0, v8, v9
	s_nop 0
	v_cndmask_b32_e32 v1, v1, v5, vcc
	v_cvt_pk_f16_f32 v1, v2, v1
	ds_write2_b64 v90, v[16:17], v[0:1] offset0:112 offset1:116
	v_mul_hi_i32 v0, v120, s2
	v_lshrrev_b32_e32 v1, 31, v0
	v_ashrrev_i32_e32 v0, 2, v0
	v_add_u32_e32 v6, v0, v1
	v_mad_u64_u32 v[4:5], s[4:5], v6, s3, v[120:121]
	v_add_u32_e32 v5, s17, v6
	v_mul_lo_u32 v0, v6, s7
	v_lshlrev_b32_e32 v1, 4, v4
	v_mad_i64_i32 v[6:7], s[4:5], v5, s12, 0
	v_lshlrev_b32_e32 v4, 3, v4
	v_lshl_add_u64 v[6:7], v[6:7], 1, s[0:1]
	v_ashrrev_i32_e32 v5, 31, v4
	v_lshl_add_u64 v[8:9], v[4:5], 1, v[6:7]
	v_add_u32_e32 v4, 0x100, v120
	v_mul_hi_i32 v5, v4, s2
	s_waitcnt lgkmcnt(0)
	s_barrier
	v_add3_u32 v0, 0, v0, v1
	v_lshrrev_b32_e32 v6, 31, v5
	v_ashrrev_i32_e32 v5, 2, v5
	ds_read_b128 v[0:3], v0
	v_add_u32_e32 v12, v5, v6
	v_mad_u64_u32 v[10:11], s[4:5], v12, s3, v[4:5]
	v_mul_lo_u32 v4, v12, s7
	v_lshlrev_b32_e32 v5, 4, v10
	v_add3_u32 v4, 0, v4, v5
	ds_read_b128 v[4:7], v4
	s_waitcnt lgkmcnt(1)
	global_store_dwordx4 v[8:9], v[0:3], off sc1
	s_nop 1
	v_add_u32_e32 v0, s17, v12
	v_mad_i64_i32 v[0:1], s[4:5], v0, s12, 0
	v_lshlrev_b32_e32 v2, 3, v10
	v_lshl_add_u64 v[0:1], v[0:1], 1, s[0:1]
	v_ashrrev_i32_e32 v3, 31, v2
	v_lshl_add_u64 v[0:1], v[2:3], 1, v[0:1]
	s_waitcnt lgkmcnt(0)
	global_store_dwordx4 v[0:1], v[4:7], off sc1
	v_add_u32_e32 v0, 0x200, v120
	v_mul_hi_i32 v1, v0, s2
	v_lshrrev_b32_e32 v2, 31, v1
	v_ashrrev_i32_e32 v1, 2, v1
	v_add_u32_e32 v6, v1, v2
	v_mad_u64_u32 v[4:5], s[4:5], v6, s3, v[0:1]
	v_add_u32_e32 v5, s17, v6
	v_mul_lo_u32 v0, v6, s7
	v_lshlrev_b32_e32 v1, 4, v4
	v_mad_i64_i32 v[6:7], s[4:5], v5, s12, 0
	v_lshlrev_b32_e32 v4, 3, v4
	v_lshl_add_u64 v[6:7], v[6:7], 1, s[0:1]
	v_ashrrev_i32_e32 v5, 31, v4
	v_lshl_add_u64 v[8:9], v[4:5], 1, v[6:7]
	v_add_u32_e32 v4, 0x300, v120
	v_mul_hi_i32 v5, v4, s2
	v_add3_u32 v0, 0, v0, v1
	v_lshrrev_b32_e32 v6, 31, v5
	v_ashrrev_i32_e32 v5, 2, v5
	ds_read_b128 v[0:3], v0
	v_add_u32_e32 v12, v5, v6
	v_mad_u64_u32 v[10:11], s[4:5], v12, s3, v[4:5]
	v_mul_lo_u32 v4, v12, s7
	v_lshlrev_b32_e32 v5, 4, v10
	v_add3_u32 v4, 0, v4, v5
	ds_read_b128 v[4:7], v4
	s_waitcnt lgkmcnt(1)
	global_store_dwordx4 v[8:9], v[0:3], off sc1
	s_nop 1
	v_add_u32_e32 v0, s17, v12
	v_mad_i64_i32 v[0:1], s[4:5], v0, s12, 0
	v_lshlrev_b32_e32 v2, 3, v10
	v_lshl_add_u64 v[0:1], v[0:1], 1, s[0:1]
	v_ashrrev_i32_e32 v3, 31, v2
	v_lshl_add_u64 v[0:1], v[2:3], 1, v[0:1]
	s_waitcnt lgkmcnt(0)
	global_store_dwordx4 v[0:1], v[4:7], off sc1
	v_add_u32_e32 v0, 0x400, v120
	v_mul_hi_i32 v1, v0, s2
	v_lshrrev_b32_e32 v2, 31, v1
	v_ashrrev_i32_e32 v1, 2, v1
	v_add_u32_e32 v6, v1, v2
	v_mad_u64_u32 v[4:5], s[4:5], v6, s3, v[0:1]
	v_add_u32_e32 v5, s17, v6
	v_mul_lo_u32 v0, v6, s7
	v_lshlrev_b32_e32 v1, 4, v4
	v_mad_i64_i32 v[6:7], s[4:5], v5, s12, 0
	v_lshlrev_b32_e32 v4, 3, v4
	v_lshl_add_u64 v[6:7], v[6:7], 1, s[0:1]
	v_ashrrev_i32_e32 v5, 31, v4
	v_lshl_add_u64 v[8:9], v[4:5], 1, v[6:7]
	v_add_u32_e32 v4, 0x500, v120
	v_mul_hi_i32 v5, v4, s2
	v_add3_u32 v0, 0, v0, v1
	v_lshrrev_b32_e32 v6, 31, v5
	v_ashrrev_i32_e32 v5, 2, v5
	ds_read_b128 v[0:3], v0
	v_add_u32_e32 v12, v5, v6
	v_mad_u64_u32 v[10:11], s[4:5], v12, s3, v[4:5]
	v_mul_lo_u32 v4, v12, s7
	v_lshlrev_b32_e32 v5, 4, v10
	v_add3_u32 v4, 0, v4, v5
	ds_read_b128 v[4:7], v4
	s_waitcnt lgkmcnt(1)
	global_store_dwordx4 v[8:9], v[0:3], off sc1
	s_nop 1
	v_add_u32_e32 v0, s17, v12
	v_mad_i64_i32 v[0:1], s[4:5], v0, s12, 0
	v_lshlrev_b32_e32 v2, 3, v10
	v_lshl_add_u64 v[0:1], v[0:1], 1, s[0:1]
	v_ashrrev_i32_e32 v3, 31, v2
	v_lshl_add_u64 v[0:1], v[2:3], 1, v[0:1]
	s_waitcnt lgkmcnt(0)
	global_store_dwordx4 v[0:1], v[4:7], off sc1
	v_add_u32_e32 v0, 0x600, v120
	v_mul_hi_i32 v1, v0, s2
	v_lshrrev_b32_e32 v2, 31, v1
	v_ashrrev_i32_e32 v1, 2, v1
	v_add_u32_e32 v6, v1, v2
	v_mad_u64_u32 v[4:5], s[4:5], v6, s3, v[0:1]
	v_add_u32_e32 v5, s17, v6
	v_mul_lo_u32 v0, v6, s7
	v_lshlrev_b32_e32 v1, 4, v4
	v_mad_i64_i32 v[6:7], s[4:5], v5, s12, 0
	v_lshlrev_b32_e32 v4, 3, v4
	v_lshl_add_u64 v[6:7], v[6:7], 1, s[0:1]
	v_ashrrev_i32_e32 v5, 31, v4
	v_lshl_add_u64 v[8:9], v[4:5], 1, v[6:7]
	v_add_u32_e32 v4, 0x700, v120
	v_mul_hi_i32 v5, v4, s2
	v_add3_u32 v0, 0, v0, v1
	v_lshrrev_b32_e32 v6, 31, v5
	v_ashrrev_i32_e32 v5, 2, v5
	ds_read_b128 v[0:3], v0
	v_add_u32_e32 v12, v5, v6
	v_mad_u64_u32 v[10:11], s[4:5], v12, s3, v[4:5]
	v_mul_lo_u32 v4, v12, s7
	v_lshlrev_b32_e32 v5, 4, v10
	v_add3_u32 v4, 0, v4, v5
	ds_read_b128 v[4:7], v4
	s_waitcnt lgkmcnt(1)
	global_store_dwordx4 v[8:9], v[0:3], off sc1
	s_nop 1
	v_add_u32_e32 v0, s17, v12
	v_mad_i64_i32 v[0:1], s[4:5], v0, s12, 0
	v_lshlrev_b32_e32 v2, 3, v10
	v_lshl_add_u64 v[0:1], v[0:1], 1, s[0:1]
	v_ashrrev_i32_e32 v3, 31, v2
	v_lshl_add_u64 v[0:1], v[2:3], 1, v[0:1]
	s_waitcnt lgkmcnt(0)
	global_store_dwordx4 v[0:1], v[4:7], off sc1
	v_add_u32_e32 v0, 0x800, v120
	v_mul_hi_i32 v1, v0, s2
	v_lshrrev_b32_e32 v2, 31, v1
	v_ashrrev_i32_e32 v1, 2, v1
	v_add_u32_e32 v6, v1, v2
	v_mad_u64_u32 v[4:5], s[4:5], v6, s3, v[0:1]
	v_add_u32_e32 v5, s17, v6
	v_mul_lo_u32 v0, v6, s7
	v_lshlrev_b32_e32 v1, 4, v4
	v_mad_i64_i32 v[6:7], s[4:5], v5, s12, 0
	v_lshlrev_b32_e32 v4, 3, v4
	v_lshl_add_u64 v[6:7], v[6:7], 1, s[0:1]
	v_ashrrev_i32_e32 v5, 31, v4
	v_lshl_add_u64 v[8:9], v[4:5], 1, v[6:7]
	v_add_u32_e32 v4, 0x900, v120
	v_mul_hi_i32 v5, v4, s2
	v_add3_u32 v0, 0, v0, v1
	v_lshrrev_b32_e32 v6, 31, v5
	v_ashrrev_i32_e32 v5, 2, v5
	ds_read_b128 v[0:3], v0
	v_add_u32_e32 v12, v5, v6
	v_mad_u64_u32 v[10:11], s[4:5], v12, s3, v[4:5]
	v_mul_lo_u32 v4, v12, s7
	v_lshlrev_b32_e32 v5, 4, v10
	v_add3_u32 v4, 0, v4, v5
	ds_read_b128 v[4:7], v4
	s_waitcnt lgkmcnt(1)
	global_store_dwordx4 v[8:9], v[0:3], off sc1
	s_nop 1
	v_add_u32_e32 v0, s17, v12
	v_mad_i64_i32 v[0:1], s[4:5], v0, s12, 0
	v_lshlrev_b32_e32 v2, 3, v10
	v_lshl_add_u64 v[0:1], v[0:1], 1, s[0:1]
	v_ashrrev_i32_e32 v3, 31, v2
	v_lshl_add_u64 v[0:1], v[2:3], 1, v[0:1]
	s_waitcnt lgkmcnt(0)
	global_store_dwordx4 v[0:1], v[4:7], off sc1
	v_add_u32_e32 v0, 0xa00, v120
	v_mul_hi_i32 v1, v0, s2
	v_lshrrev_b32_e32 v2, 31, v1
	v_ashrrev_i32_e32 v1, 2, v1
	v_add_u32_e32 v6, v1, v2
	v_mad_u64_u32 v[4:5], s[4:5], v6, s3, v[0:1]
	v_add_u32_e32 v5, s17, v6
	v_mul_lo_u32 v0, v6, s7
	v_lshlrev_b32_e32 v1, 4, v4
	v_mad_i64_i32 v[6:7], s[4:5], v5, s12, 0
	v_lshlrev_b32_e32 v4, 3, v4
	v_lshl_add_u64 v[6:7], v[6:7], 1, s[0:1]
	v_ashrrev_i32_e32 v5, 31, v4
	v_lshl_add_u64 v[8:9], v[4:5], 1, v[6:7]
	v_add_u32_e32 v4, 0xb00, v120
	v_mul_hi_i32 v5, v4, s2
	v_add3_u32 v0, 0, v0, v1
	v_lshrrev_b32_e32 v6, 31, v5
	v_ashrrev_i32_e32 v5, 2, v5
	ds_read_b128 v[0:3], v0
	v_add_u32_e32 v12, v5, v6
	v_mad_u64_u32 v[10:11], s[2:3], v12, s3, v[4:5]
	v_mul_lo_u32 v4, v12, s7
	v_lshlrev_b32_e32 v5, 4, v10
	v_add3_u32 v4, 0, v4, v5
	ds_read_b128 v[4:7], v4
	s_waitcnt lgkmcnt(1)
	global_store_dwordx4 v[8:9], v[0:3], off sc1
	s_nop 1
	v_add_u32_e32 v0, s17, v12
	v_mad_i64_i32 v[0:1], s[2:3], v0, s12, 0
	v_lshlrev_b32_e32 v2, 3, v10
	v_lshl_add_u64 v[0:1], v[0:1], 1, s[0:1]
	v_ashrrev_i32_e32 v3, 31, v2
	v_lshl_add_u64 v[0:1], v[2:3], 1, v[0:1]
	s_waitcnt lgkmcnt(0)
	global_store_dwordx4 v[0:1], v[4:7], off sc1
	s_endpgm
	.p2align	8

.LBB3_8:
	s_lshr_b32 s0, s3, 30
	s_add_i32 s0, s3, s0
	s_lshr_b32 s0, s0, 2
	s_mulk_i32 s0, 0xfd00
	s_add_i32 s0, s0, s27
	s_add_i32 s3, s3, 3
	s_cmp_lt_u32 s3, 7
	s_cselect_b64 vcc, -1, 0
	s_and_b32 s1, s2, 0xffffff00
	s_cmpk_eq_i32 s1, 0x100
	s_cselect_b32 s1, s6, s8
	s_cselect_b32 s6, s7, s9
	s_cselect_b32 s7, s12, s14
	s_cselect_b32 s8, s13, s15
	s_and_b64 s[2:3], vcc, exec
	s_cselect_b32 s5, s5, s6
	s_cselect_b32 s6, s4, s1
	s_cselect_b32 s4, s11, s8
	s_cselect_b32 s7, s10, s7
	s_ashr_i32 s1, s0, 31
	s_lshl_b64 s[2:3], s[0:1], 2
	v_mbcnt_lo_u32_b32 v109, -1, 0
	v_mbcnt_hi_u32_b32 v109, -1, v109
	s_add_u32 s2, s7, s2
	v_lshrrev_b32_e32 v96, 2, v109
	v_and_or_b32 v110, v96, 12, s28
	s_addc_u32 s3, s4, s3
	s_movk_i32 s4, 0x190
	v_and_or_b32 v111, v109, 15, s26
	s_barrier
	v_mov_b32_e32 v96, 0x3d553b94
	v_lshlrev_b32_e32 v122, 2, v110
	v_mul_lo_u32 v111, v111, s4
	v_lshlrev_b32_e32 v110, 1, v110
	v_cndmask_b32_e32 v108, 1.0, v96, vcc
	global_load_dwordx4 v[96:99], v122, s[2:3]
	global_load_dwordx4 v[100:103], v122, s[2:3] offset:64
	global_load_dwordx4 v[104:107], v122, s[2:3] offset:128
	v_add3_u32 v123, 0, v110, v111
	global_load_dwordx4 v[110:113], v122, s[2:3] offset:192
	global_load_dwordx4 v[114:117], v122, s[2:3] offset:256
	global_load_dwordx4 v[118:121], v122, s[2:3] offset:320
	v_add_u32_e32 v124, 0x1800, v123
	s_lshl_b64 s[0:1], s[0:1], 1
	v_add_u32_e32 v125, 0x3000, v123
	v_add_u32_e32 v126, 0x4800, v123
	s_add_u32 s6, s6, s0
	s_mov_b32 s0, 0x2aaaaaab
	s_addc_u32 s7, s5, s1
	s_movk_i32 s1, 0xffe8
	s_waitcnt vmcnt(5)
	v_pk_add_f32 v[94:95], v[98:99], v[94:95]
	v_pk_add_f32 v[92:93], v[96:97], v[92:93]
	s_waitcnt vmcnt(4)
	v_pk_add_f32 v[78:79], v[102:103], v[78:79]
	v_pk_add_f32 v[76:77], v[100:101], v[76:77]
	s_waitcnt vmcnt(1)
	v_pk_add_f32 v[26:27], v[116:117], v[26:27]
	v_pk_add_f32 v[24:25], v[114:115], v[24:25]
	s_waitcnt vmcnt(0)
	v_pk_add_f32 v[10:11], v[120:121], v[10:11]
	v_pk_add_f32 v[8:9], v[118:119], v[8:9]
	v_pk_add_f32 v[90:91], v[98:99], v[90:91]
	v_pk_add_f32 v[88:89], v[96:97], v[88:89]
	v_pk_add_f32 v[86:87], v[98:99], v[86:87]
	v_pk_add_f32 v[84:85], v[96:97], v[84:85]
	v_pk_add_f32 v[82:83], v[98:99], v[82:83]
	v_pk_add_f32 v[80:81], v[96:97], v[80:81]
	v_pk_add_f32 v[74:75], v[102:103], v[74:75]
	v_pk_add_f32 v[72:73], v[100:101], v[72:73]
	v_pk_add_f32 v[70:71], v[102:103], v[70:71]
	v_pk_add_f32 v[68:69], v[100:101], v[68:69]
	v_pk_add_f32 v[66:67], v[102:103], v[66:67]
	v_pk_add_f32 v[64:65], v[100:101], v[64:65]
	v_pk_mul_f32 v[94:95], v[108:109], v[94:95] op_sel_hi:[0,1]
	v_pk_mul_f32 v[92:93], v[108:109], v[92:93] op_sel_hi:[0,1]
	v_pk_mul_f32 v[78:79], v[108:109], v[78:79] op_sel_hi:[0,1]
	v_pk_mul_f32 v[76:77], v[108:109], v[76:77] op_sel_hi:[0,1]
	v_pk_mul_f32 v[26:27], v[108:109], v[26:27] op_sel_hi:[0,1]
	v_pk_mul_f32 v[24:25], v[108:109], v[24:25] op_sel_hi:[0,1]
	v_pk_add_f32 v[18:19], v[116:117], v[18:19]
	v_pk_add_f32 v[16:17], v[114:115], v[16:17]
	v_pk_mul_f32 v[10:11], v[108:109], v[10:11] op_sel_hi:[0,1]
	v_pk_mul_f32 v[8:9], v[108:109], v[8:9] op_sel_hi:[0,1]
	v_pk_add_f32 v[2:3], v[120:121], v[2:3]
	v_pk_add_f32 v[0:1], v[118:119], v[0:1]
	v_pk_mul_f32 v[90:91], v[108:109], v[90:91] op_sel_hi:[0,1]
	v_pk_mul_f32 v[88:89], v[108:109], v[88:89] op_sel_hi:[0,1]
	v_pk_mul_f32 v[86:87], v[108:109], v[86:87] op_sel_hi:[0,1]
	v_pk_mul_f32 v[84:85], v[108:109], v[84:85] op_sel_hi:[0,1]
	v_pk_mul_f32 v[82:83], v[108:109], v[82:83] op_sel_hi:[0,1]
	v_pk_mul_f32 v[80:81], v[108:109], v[80:81] op_sel_hi:[0,1]
	v_pk_mul_f32 v[74:75], v[108:109], v[74:75] op_sel_hi:[0,1]
	v_pk_mul_f32 v[72:73], v[108:109], v[72:73] op_sel_hi:[0,1]
	v_pk_mul_f32 v[70:71], v[108:109], v[70:71] op_sel_hi:[0,1]
	v_pk_mul_f32 v[68:69], v[108:109], v[68:69] op_sel_hi:[0,1]
	v_pk_mul_f32 v[66:67], v[108:109], v[66:67] op_sel_hi:[0,1]
	v_pk_mul_f32 v[64:65], v[108:109], v[64:65] op_sel_hi:[0,1]
	v_cvt_pk_f16_f32 v92, v92, v93
	v_cvt_pk_f16_f32 v93, v94, v95
	v_cvt_pk_f16_f32 v76, v76, v77
	v_cvt_pk_f16_f32 v77, v78, v79
	v_cvt_pk_f16_f32 v24, v24, v25
	v_cvt_pk_f16_f32 v25, v26, v27
	v_pk_mul_f32 v[18:19], v[108:109], v[18:19] op_sel_hi:[0,1]
	v_pk_mul_f32 v[16:17], v[108:109], v[16:17] op_sel_hi:[0,1]
	v_cvt_pk_f16_f32 v8, v8, v9
	v_cvt_pk_f16_f32 v9, v10, v11
	v_pk_mul_f32 v[2:3], v[108:109], v[2:3] op_sel_hi:[0,1]
	v_pk_mul_f32 v[0:1], v[108:109], v[0:1] op_sel_hi:[0,1]
	v_cvt_pk_f16_f32 v88, v88, v89
	v_cvt_pk_f16_f32 v89, v90, v91
	v_cvt_pk_f16_f32 v84, v84, v85
	v_cvt_pk_f16_f32 v85, v86, v87
	v_cvt_pk_f16_f32 v80, v80, v81
	v_cvt_pk_f16_f32 v81, v82, v83
	v_cvt_pk_f16_f32 v72, v72, v73
	v_cvt_pk_f16_f32 v73, v74, v75
	v_cvt_pk_f16_f32 v68, v68, v69
	v_cvt_pk_f16_f32 v69, v70, v71
	v_cvt_pk_f16_f32 v64, v64, v65
	v_cvt_pk_f16_f32 v65, v66, v67
	ds_write2_b64 v123, v[92:93], v[76:77] offset1:4
	ds_write2_b64 v124, v[88:89], v[72:73] offset0:32 offset1:36
	ds_write2_b64 v125, v[84:85], v[68:69] offset0:64 offset1:68
	ds_write2_b64 v126, v[80:81], v[64:65] offset0:96 offset1:100
	v_cvt_pk_f16_f32 v16, v16, v17
	v_cvt_pk_f16_f32 v17, v18, v19
	ds_write2_b64 v124, v[24:25], v[8:9] offset0:48 offset1:52
	v_cvt_pk_f16_f32 v0, v0, v1
	v_cvt_pk_f16_f32 v1, v2, v3
	v_bfi_b32 v8, 63, v109, s25
	v_pk_add_f32 v[22:23], v[116:117], v[22:23]
	v_pk_add_f32 v[20:21], v[114:115], v[20:21]
	v_pk_add_f32 v[6:7], v[120:121], v[6:7]
	v_pk_add_f32 v[4:5], v[118:119], v[4:5]
	ds_write2_b64 v126, v[16:17], v[0:1] offset0:112 offset1:116
	v_mul_hi_i32 v0, v8, s0
	v_pk_mul_f32 v[22:23], v[108:109], v[22:23] op_sel_hi:[0,1]
	v_pk_mul_f32 v[20:21], v[108:109], v[20:21] op_sel_hi:[0,1]
	v_pk_mul_f32 v[6:7], v[108:109], v[6:7] op_sel_hi:[0,1]
	v_pk_mul_f32 v[4:5], v[108:109], v[4:5] op_sel_hi:[0,1]
	v_lshrrev_b32_e32 v1, 31, v0
	v_ashrrev_i32_e32 v0, 2, v0
	v_cvt_pk_f16_f32 v20, v20, v21
	v_cvt_pk_f16_f32 v21, v22, v23
	v_cvt_pk_f16_f32 v4, v4, v5
	v_cvt_pk_f16_f32 v5, v6, v7
	v_add_u32_e32 v6, v0, v1
	v_pk_add_f32 v[30:31], v[116:117], v[30:31]
	v_pk_add_f32 v[28:29], v[114:115], v[28:29]
	v_pk_add_f32 v[14:15], v[120:121], v[14:15]
	v_pk_add_f32 v[12:13], v[118:119], v[12:13]
	ds_write2_b64 v125, v[20:21], v[4:5] offset0:80 offset1:84
	v_mad_u64_u32 v[4:5], s[2:3], v6, s1, v[8:9]
	v_pk_mul_f32 v[30:31], v[108:109], v[30:31] op_sel_hi:[0,1]
	v_pk_mul_f32 v[28:29], v[108:109], v[28:29] op_sel_hi:[0,1]
	v_pk_mul_f32 v[14:15], v[108:109], v[14:15] op_sel_hi:[0,1]
	v_pk_mul_f32 v[12:13], v[108:109], v[12:13] op_sel_hi:[0,1]
	v_lshlrev_b32_e32 v1, 4, v4
	v_add_u32_e32 v5, s24, v6
	s_movk_i32 s2, 0x600
	v_mov_b64_e32 v[10:11], s[6:7]
	v_lshlrev_b32_e32 v4, 3, v4
	v_pk_add_f32 v[62:63], v[106:107], v[62:63]
	v_pk_add_f32 v[60:61], v[104:105], v[60:61]
	v_pk_add_f32 v[58:59], v[106:107], v[58:59]
	v_pk_add_f32 v[56:57], v[104:105], v[56:57]
	v_pk_add_f32 v[54:55], v[106:107], v[54:55]
	v_pk_add_f32 v[52:53], v[104:105], v[52:53]
	v_pk_add_f32 v[50:51], v[106:107], v[50:51]
	v_pk_add_f32 v[48:49], v[104:105], v[48:49]
	v_pk_add_f32 v[46:47], v[112:113], v[46:47]
	v_pk_add_f32 v[44:45], v[110:111], v[44:45]
	v_pk_add_f32 v[42:43], v[112:113], v[42:43]
	v_pk_add_f32 v[40:41], v[110:111], v[40:41]
	v_pk_add_f32 v[38:39], v[112:113], v[38:39]
	v_pk_add_f32 v[36:37], v[110:111], v[36:37]
	v_pk_add_f32 v[34:35], v[112:113], v[34:35]
	v_pk_add_f32 v[32:33], v[110:111], v[32:33]
	v_cvt_pk_f16_f32 v28, v28, v29
	v_cvt_pk_f16_f32 v29, v30, v31
	v_cvt_pk_f16_f32 v12, v12, v13
	v_cvt_pk_f16_f32 v13, v14, v15
	v_mul_lo_u32 v0, v6, s4
	v_mad_i64_i32 v[6:7], s[6:7], v5, s2, v[10:11]
	v_ashrrev_i32_e32 v5, 31, v4
	v_pk_mul_f32 v[62:63], v[108:109], v[62:63] op_sel_hi:[0,1]
	v_pk_mul_f32 v[60:61], v[108:109], v[60:61] op_sel_hi:[0,1]
	v_pk_mul_f32 v[58:59], v[108:109], v[58:59] op_sel_hi:[0,1]
	v_pk_mul_f32 v[56:57], v[108:109], v[56:57] op_sel_hi:[0,1]
	v_pk_mul_f32 v[54:55], v[108:109], v[54:55] op_sel_hi:[0,1]
	v_pk_mul_f32 v[52:53], v[108:109], v[52:53] op_sel_hi:[0,1]
	v_pk_mul_f32 v[50:51], v[108:109], v[50:51] op_sel_hi:[0,1]
	v_pk_mul_f32 v[48:49], v[108:109], v[48:49] op_sel_hi:[0,1]
	v_pk_mul_f32 v[46:47], v[108:109], v[46:47] op_sel_hi:[0,1]
	v_pk_mul_f32 v[44:45], v[108:109], v[44:45] op_sel_hi:[0,1]
	v_pk_mul_f32 v[42:43], v[108:109], v[42:43] op_sel_hi:[0,1]
	v_pk_mul_f32 v[40:41], v[108:109], v[40:41] op_sel_hi:[0,1]
	v_pk_mul_f32 v[38:39], v[108:109], v[38:39] op_sel_hi:[0,1]
	v_pk_mul_f32 v[36:37], v[108:109], v[36:37] op_sel_hi:[0,1]
	v_pk_mul_f32 v[34:35], v[108:109], v[34:35] op_sel_hi:[0,1]
	v_pk_mul_f32 v[32:33], v[108:109], v[32:33] op_sel_hi:[0,1]
	ds_write2_b64 v123, v[28:29], v[12:13] offset0:16 offset1:20
	v_lshl_add_u64 v[12:13], v[4:5], 1, v[6:7]
	v_add_u32_e32 v4, 0x100, v8
	v_cvt_pk_f16_f32 v60, v60, v61
	v_cvt_pk_f16_f32 v61, v62, v63
	v_cvt_pk_f16_f32 v56, v56, v57
	v_cvt_pk_f16_f32 v57, v58, v59
	v_cvt_pk_f16_f32 v52, v52, v53
	v_cvt_pk_f16_f32 v53, v54, v55
	v_cvt_pk_f16_f32 v48, v48, v49
	v_cvt_pk_f16_f32 v49, v50, v51
	v_cvt_pk_f16_f32 v44, v44, v45
	v_cvt_pk_f16_f32 v45, v46, v47
	v_cvt_pk_f16_f32 v40, v40, v41
	v_cvt_pk_f16_f32 v41, v42, v43
	v_cvt_pk_f16_f32 v36, v36, v37
	v_cvt_pk_f16_f32 v37, v38, v39
	v_cvt_pk_f16_f32 v32, v32, v33
	v_cvt_pk_f16_f32 v33, v34, v35
	v_mul_hi_i32 v5, v4, s0
	ds_write2_b64 v123, v[60:61], v[44:45] offset0:8 offset1:12
	ds_write2_b64 v124, v[56:57], v[40:41] offset0:40 offset1:44
	ds_write2_b64 v125, v[52:53], v[36:37] offset0:72 offset1:76
	ds_write2_b64 v126, v[48:49], v[32:33] offset0:104 offset1:108
	v_lshrrev_b32_e32 v6, 31, v5
	v_ashrrev_i32_e32 v5, 2, v5
	s_waitcnt lgkmcnt(0)
	s_barrier
	v_add3_u32 v0, 0, v0, v1
	v_add_u32_e32 v9, v5, v6
	ds_read_b128 v[0:3], v0
	v_mad_u64_u32 v[14:15], s[6:7], v9, s1, v[4:5]
	v_mul_lo_u32 v4, v9, s4
	v_lshlrev_b32_e32 v5, 4, v14
	v_add3_u32 v4, 0, v4, v5
	ds_read_b128 v[4:7], v4
	s_waitcnt lgkmcnt(1)
	global_store_dwordx4 v[12:13], v[0:3], off
	s_nop 1
	v_add_u32_e32 v0, s24, v9
	v_lshlrev_b32_e32 v2, 3, v14
	v_mad_i64_i32 v[0:1], s[6:7], v0, s2, v[10:11]
	v_ashrrev_i32_e32 v3, 31, v2
	v_lshl_add_u64 v[0:1], v[2:3], 1, v[0:1]
	s_waitcnt lgkmcnt(0)
	global_store_dwordx4 v[0:1], v[4:7], off
	v_add_u32_e32 v0, 0x200, v8
	v_mul_hi_i32 v1, v0, s0
	v_lshrrev_b32_e32 v2, 31, v1
	v_ashrrev_i32_e32 v1, 2, v1
	v_add_u32_e32 v6, v1, v2
	v_mad_u64_u32 v[4:5], s[6:7], v6, s1, v[0:1]
	v_lshlrev_b32_e32 v1, 4, v4
	v_add_u32_e32 v5, s24, v6
	v_lshlrev_b32_e32 v4, 3, v4
	v_mul_lo_u32 v0, v6, s4
	v_mad_i64_i32 v[6:7], s[6:7], v5, s2, v[10:11]
	v_ashrrev_i32_e32 v5, 31, v4
	v_lshl_add_u64 v[12:13], v[4:5], 1, v[6:7]
	v_add_u32_e32 v4, 0x300, v8
	v_mul_hi_i32 v5, v4, s0
	v_lshrrev_b32_e32 v6, 31, v5
	v_ashrrev_i32_e32 v5, 2, v5
	v_add3_u32 v0, 0, v0, v1
	v_add_u32_e32 v9, v5, v6
	ds_read_b128 v[0:3], v0
	v_mad_u64_u32 v[14:15], s[6:7], v9, s1, v[4:5]
	v_mul_lo_u32 v4, v9, s4
	v_lshlrev_b32_e32 v5, 4, v14
	v_add3_u32 v4, 0, v4, v5
	ds_read_b128 v[4:7], v4
	s_waitcnt lgkmcnt(1)
	global_store_dwordx4 v[12:13], v[0:3], off
	s_nop 1
	v_add_u32_e32 v0, s24, v9
	v_lshlrev_b32_e32 v2, 3, v14
	v_mad_i64_i32 v[0:1], s[6:7], v0, s2, v[10:11]
	v_ashrrev_i32_e32 v3, 31, v2
	v_lshl_add_u64 v[0:1], v[2:3], 1, v[0:1]
	s_waitcnt lgkmcnt(0)
	global_store_dwordx4 v[0:1], v[4:7], off
	v_add_u32_e32 v0, 0x400, v8
	v_mul_hi_i32 v1, v0, s0
	v_lshrrev_b32_e32 v2, 31, v1
	v_ashrrev_i32_e32 v1, 2, v1
	v_add_u32_e32 v6, v1, v2
	v_mad_u64_u32 v[4:5], s[6:7], v6, s1, v[0:1]
	v_lshlrev_b32_e32 v1, 4, v4
	v_add_u32_e32 v5, s24, v6
	v_lshlrev_b32_e32 v4, 3, v4
	v_mul_lo_u32 v0, v6, s4
	v_mad_i64_i32 v[6:7], s[6:7], v5, s2, v[10:11]
	v_ashrrev_i32_e32 v5, 31, v4
	v_lshl_add_u64 v[12:13], v[4:5], 1, v[6:7]
	v_add_u32_e32 v4, 0x500, v8
	v_mul_hi_i32 v5, v4, s0
	v_lshrrev_b32_e32 v6, 31, v5
	v_ashrrev_i32_e32 v5, 2, v5
	v_add3_u32 v0, 0, v0, v1
	v_add_u32_e32 v9, v5, v6
	ds_read_b128 v[0:3], v0
	v_mad_u64_u32 v[14:15], s[6:7], v9, s1, v[4:5]
	v_mul_lo_u32 v4, v9, s4
	v_lshlrev_b32_e32 v5, 4, v14
	v_add3_u32 v4, 0, v4, v5
	ds_read_b128 v[4:7], v4
	s_waitcnt lgkmcnt(1)
	global_store_dwordx4 v[12:13], v[0:3], off
	s_nop 1
	v_add_u32_e32 v0, s24, v9
	v_lshlrev_b32_e32 v2, 3, v14
	v_mad_i64_i32 v[0:1], s[6:7], v0, s2, v[10:11]
	v_ashrrev_i32_e32 v3, 31, v2
	v_lshl_add_u64 v[0:1], v[2:3], 1, v[0:1]
	s_waitcnt lgkmcnt(0)
	global_store_dwordx4 v[0:1], v[4:7], off
	v_add_u32_e32 v0, 0x600, v8
	v_mul_hi_i32 v1, v0, s0
	v_lshrrev_b32_e32 v2, 31, v1
	v_ashrrev_i32_e32 v1, 2, v1
	v_add_u32_e32 v6, v1, v2
	v_mad_u64_u32 v[4:5], s[6:7], v6, s1, v[0:1]
	v_lshlrev_b32_e32 v1, 4, v4
	v_add_u32_e32 v5, s24, v6
	v_lshlrev_b32_e32 v4, 3, v4
	v_mul_lo_u32 v0, v6, s4
	v_mad_i64_i32 v[6:7], s[6:7], v5, s2, v[10:11]
	v_ashrrev_i32_e32 v5, 31, v4
	v_lshl_add_u64 v[12:13], v[4:5], 1, v[6:7]
	v_add_u32_e32 v4, 0x700, v8
	v_mul_hi_i32 v5, v4, s0
	v_lshrrev_b32_e32 v6, 31, v5
	v_ashrrev_i32_e32 v5, 2, v5
	v_add3_u32 v0, 0, v0, v1
	v_add_u32_e32 v9, v5, v6
	ds_read_b128 v[0:3], v0
	v_mad_u64_u32 v[14:15], s[6:7], v9, s1, v[4:5]
	v_mul_lo_u32 v4, v9, s4
	v_lshlrev_b32_e32 v5, 4, v14
	v_add3_u32 v4, 0, v4, v5
	ds_read_b128 v[4:7], v4
	s_waitcnt lgkmcnt(1)
	global_store_dwordx4 v[12:13], v[0:3], off
	s_nop 1
	v_add_u32_e32 v0, s24, v9
	v_lshlrev_b32_e32 v2, 3, v14
	v_mad_i64_i32 v[0:1], s[6:7], v0, s2, v[10:11]
	v_ashrrev_i32_e32 v3, 31, v2
	v_lshl_add_u64 v[0:1], v[2:3], 1, v[0:1]
	s_waitcnt lgkmcnt(0)
	global_store_dwordx4 v[0:1], v[4:7], off
	v_add_u32_e32 v0, 0x800, v8
	v_mul_hi_i32 v1, v0, s0
	v_lshrrev_b32_e32 v2, 31, v1
	v_ashrrev_i32_e32 v1, 2, v1
	v_add_u32_e32 v6, v1, v2
	v_mad_u64_u32 v[4:5], s[6:7], v6, s1, v[0:1]
	v_lshlrev_b32_e32 v1, 4, v4
	v_add_u32_e32 v5, s24, v6
	v_lshlrev_b32_e32 v4, 3, v4
	v_mul_lo_u32 v0, v6, s4
	v_mad_i64_i32 v[6:7], s[6:7], v5, s2, v[10:11]
	v_ashrrev_i32_e32 v5, 31, v4
	v_lshl_add_u64 v[12:13], v[4:5], 1, v[6:7]
	v_add_u32_e32 v4, 0x900, v8
	v_mul_hi_i32 v5, v4, s0
	v_lshrrev_b32_e32 v6, 31, v5
	v_ashrrev_i32_e32 v5, 2, v5
	v_add3_u32 v0, 0, v0, v1
	v_add_u32_e32 v9, v5, v6
	ds_read_b128 v[0:3], v0
	v_mad_u64_u32 v[14:15], s[6:7], v9, s1, v[4:5]
	v_mul_lo_u32 v4, v9, s4
	v_lshlrev_b32_e32 v5, 4, v14
	v_add3_u32 v4, 0, v4, v5
	ds_read_b128 v[4:7], v4
	s_waitcnt lgkmcnt(1)
	global_store_dwordx4 v[12:13], v[0:3], off
	s_nop 1
	v_add_u32_e32 v0, s24, v9
	v_lshlrev_b32_e32 v2, 3, v14
	v_mad_i64_i32 v[0:1], s[6:7], v0, s2, v[10:11]
	v_ashrrev_i32_e32 v3, 31, v2
	v_lshl_add_u64 v[0:1], v[2:3], 1, v[0:1]
	s_waitcnt lgkmcnt(0)
	global_store_dwordx4 v[0:1], v[4:7], off
	v_add_u32_e32 v0, 0xa00, v8
	v_mul_hi_i32 v1, v0, s0
	v_lshrrev_b32_e32 v2, 31, v1
	v_ashrrev_i32_e32 v1, 2, v1
	v_add_u32_e32 v6, v1, v2
	v_mad_u64_u32 v[4:5], s[6:7], v6, s1, v[0:1]
	v_lshlrev_b32_e32 v1, 4, v4
	v_add_u32_e32 v5, s24, v6
	v_lshlrev_b32_e32 v4, 3, v4
	v_mul_lo_u32 v0, v6, s4
	v_mad_i64_i32 v[6:7], s[6:7], v5, s2, v[10:11]
	v_ashrrev_i32_e32 v5, 31, v4
	v_lshl_add_u64 v[12:13], v[4:5], 1, v[6:7]
	v_add_u32_e32 v4, 0xb00, v8
	v_mul_hi_i32 v5, v4, s0
	v_lshrrev_b32_e32 v6, 31, v5
	v_ashrrev_i32_e32 v5, 2, v5
	v_add3_u32 v0, 0, v0, v1
	v_add_u32_e32 v14, v5, v6
	ds_read_b128 v[0:3], v0
	v_mad_u64_u32 v[8:9], s[0:1], v14, s1, v[4:5]
	v_mul_lo_u32 v4, v14, s4
	v_lshlrev_b32_e32 v5, 4, v8
	v_add3_u32 v4, 0, v4, v5
	ds_read_b128 v[4:7], v4
	s_waitcnt lgkmcnt(1)
	global_store_dwordx4 v[12:13], v[0:3], off
	s_nop 1
	v_add_u32_e32 v0, s24, v14
	v_lshlrev_b32_e32 v2, 3, v8
	v_mad_i64_i32 v[0:1], s[0:1], v0, s2, v[10:11]
	v_ashrrev_i32_e32 v3, 31, v2
	v_lshl_add_u64 v[0:1], v[2:3], 1, v[0:1]
	s_waitcnt lgkmcnt(0)
	global_store_dwordx4 v[0:1], v[4:7], off
	s_endpgm
	.p2align	8

.LBB4_8:
	s_endpgm
	.p2align	8

_Z6gemm_kILi1ELb1ELb1ELb0ELb0ELb1EEvPKtS1_ii7EpiArgs:
	s_load_dwordx8 s[4:11], s[0:1], 0x0
	s_load_dwordx2 s[14:15], s[0:1], 0x30
	s_load_dwordx2 s[12:13], s[0:1], 0x48
	s_lshl_b32 s0, s2, 3
	s_and_b32 s0, s0, 56
	s_bfe_u32 s1, s2, 0x30003
	s_or_b32 s0, s0, s1
	s_lshl_b32 s22, s0, 7
	v_readfirstlane_b32 s18, v0
	s_lshr_b32 s1, s2, 6
	s_waitcnt lgkmcnt(0)
	s_mul_hi_i32 s3, s9, s22
	s_mul_i32 s2, s9, s22
	s_lshr_b32 s19, s18, 6
	s_bfe_u32 s23, s18, 0x20006
	s_ashr_i32 s17, s9, 31
	s_lshl_b64 s[2:3], s[2:3], 1
	s_mul_i32 s0, s1, 0xc0
	s_add_u32 s2, s4, s2
	s_addc_u32 s3, s5, s3
	s_mul_hi_i32 s5, s9, s0
	s_mul_i32 s4, s9, s0
	s_ashr_i32 s1, s0, 31
	s_lshl_b64 s[4:5], s[4:5], 1
	s_add_u32 s4, s6, s4
	v_lshrrev_b32_e32 v1, 4, v0
	s_addc_u32 s5, s7, s5
	s_lshr_b32 s6, s18, 2
	v_xor_b32_e32 v4, v1, v0
	s_lshl_b32 s25, s19, 10
	s_and_b32 s6, s6, 0x3fffffc0
	v_and_b32_e32 v2, 15, v0
	v_lshrrev_b32_e32 v3, 3, v0
	v_lshlrev_b32_e32 v4, 3, v4
	v_bfe_u32 v5, v0, 1, 3
	s_cmp_lg_u32 0, -1
	v_mul_lo_u32 v3, s9, v3
	v_and_b32_e32 v4, 56, v4
	s_mov_b32 s16, s9
	v_bitop3_b32 v5, v1, v5, 3 bitop3:0x6c
	v_or_b32_e32 v1, s6, v2
	s_cselect_b32 s6, 0, 0
	v_add_lshl_u32 v84, v3, v4, 1
	s_add_i32 s25, s25, s6
	s_nop 4
	s_mov_b32 s6, m0
	s_mov_b32 m0, s25
	s_nop 0
	global_load_lds_dwordx4 v84, s[2:3] nt
	s_mov_b32 m0, s6
	s_lshl_b64 s[18:19], s[16:17], 7
	s_add_u32 s6, s2, s18
	s_addc_u32 s7, s3, s19
	s_add_i32 s26, s25, 0x2000
	s_nop 4
	s_mov_b32 s16, m0
	s_mov_b32 m0, s26
	s_nop 0
	global_load_lds_dwordx4 v84, s[6:7] nt
	s_mov_b32 m0, s16
	s_add_i32 s27, s25, 0x4000
	s_nop 4
	s_mov_b32 s16, m0
	s_mov_b32 m0, s27
	s_nop 0
	global_load_lds_dwordx4 v84, s[4:5]
	s_mov_b32 m0, s16
	s_add_u32 s16, s4, s18
	s_addc_u32 s17, s5, s19
	s_add_i32 s28, s25, 0x6000
	s_nop 4
	s_mov_b32 s20, m0
	s_mov_b32 m0, s28
	s_nop 0
	global_load_lds_dwordx4 v84, s[16:17]
	s_mov_b32 m0, s20
	s_add_u32 s18, s16, s18
	s_addc_u32 s19, s17, s19
	s_add_i32 s29, s25, 0x8000
	s_nop 4
	s_mov_b32 s20, m0
	s_mov_b32 m0, s29
	s_nop 0
	global_load_lds_dwordx4 v84, s[18:19]
	s_mov_b32 m0, s20
	s_add_u32 s20, s2, 0x80
	s_addc_u32 s21, s3, 0
	s_add_i32 s30, s25, 0xa000
	s_nop 4
	s_mov_b32 s31, m0
	s_mov_b32 m0, s30
	s_nop 0
	global_load_lds_dwordx4 v84, s[20:21] nt
	s_mov_b32 m0, s31
	s_add_u32 s20, s6, 0x80
	s_addc_u32 s21, s7, 0
	s_add_i32 s31, s25, 0xc000
	s_nop 4
	s_mov_b32 s33, m0
	s_mov_b32 m0, s31
	s_nop 0
	global_load_lds_dwordx4 v84, s[20:21] nt
	s_mov_b32 m0, s33
	s_add_u32 s20, s4, 0x80
	s_addc_u32 s21, s5, 0
	s_add_i32 s33, s25, 0xe000
	s_nop 4
	s_mov_b32 s34, m0
	s_mov_b32 m0, s33
	s_nop 0
	global_load_lds_dwordx4 v84, s[20:21]
	s_mov_b32 m0, s34
	s_add_u32 s20, s16, 0x80
	s_addc_u32 s21, s17, 0
	s_add_i32 s34, s25, 0x10000
	s_nop 4
	s_mov_b32 s35, m0
	s_mov_b32 m0, s34
	s_nop 0
	global_load_lds_dwordx4 v84, s[20:21]
	s_mov_b32 m0, s35
	s_add_u32 s20, s18, 0x80
	s_addc_u32 s21, s19, 0
	s_add_i32 s35, s25, 0x12000
	s_nop 4
	s_mov_b32 s36, m0
	s_mov_b32 m0, s35
	s_nop 0
	global_load_lds_dwordx4 v84, s[20:21]
	s_mov_b32 m0, s36
	s_add_u32 s20, s2, 0x100
	s_addc_u32 s21, s3, 0
	s_add_i32 s36, s25, 0x14000
	s_nop 4
	s_mov_b32 s37, m0
	s_mov_b32 m0, s36
	s_nop 0
	global_load_lds_dwordx4 v84, s[20:21] nt
	s_mov_b32 m0, s37
	s_add_u32 s20, s6, 0x100
	s_addc_u32 s21, s7, 0
	s_add_i32 s37, s25, 0x16000
	s_nop 4
	s_mov_b32 s38, m0
	s_mov_b32 m0, s37
	s_nop 0
	global_load_lds_dwordx4 v84, s[20:21] nt
	s_mov_b32 m0, s38
	s_add_u32 s20, s4, 0x100
	s_addc_u32 s21, s5, 0
	s_add_i32 s38, s25, 0x18000
	s_nop 4
	s_mov_b32 s39, m0
	s_mov_b32 m0, s38
	s_nop 0
	global_load_lds_dwordx4 v84, s[20:21]
	s_mov_b32 m0, s39
	s_add_u32 s20, s16, 0x100
	s_addc_u32 s21, s17, 0
	s_add_i32 s39, s25, 0x1a000
	s_mul_i32 s23, s23, 48
	s_nop 4
	s_mov_b32 s40, m0
	s_mov_b32 m0, s39
	s_nop 0
	global_load_lds_dwordx4 v84, s[20:21]
	s_mov_b32 m0, s40
	s_add_u32 s20, s18, 0x100
	v_lshlrev_b32_e32 v5, 4, v5
	v_or_b32_e32 v2, s23, v2
	v_lshl_add_u32 v31, v1, 7, 0
	s_addc_u32 s21, s19, 0
	s_add_i32 s40, s25, 0x1c000
	s_nop 4
	s_mov_b32 s41, m0
	s_mov_b32 m0, s40
	s_nop 0
	global_load_lds_dwordx4 v84, s[20:21]
	s_mov_b32 m0, s41
	v_xor_b32_e32 v30, 64, v5
	v_lshl_add_u32 v2, v2, 7, 0
	v_add_u32_e32 v79, v31, v5
	s_waitcnt vmcnt(10) lgkmcnt(0)
	s_barrier
	v_add_u32_e32 v82, v2, v5
	v_add_u32_e32 v81, v2, v30
	s_ashr_i32 s9, s9, 6
	v_add_u32_e32 v83, v31, v30
	v_add_u32_e32 v100, 0x14000, v79
	v_add_u32_e32 v101, 0x14000, v83
	v_add_u32_e32 v102, 0x14000, v82
	v_add_u32_e32 v103, 0x14000, v81
	s_add_u32 s54, s2, 0x100
	s_addc_u32 s55, s3, 0
	s_add_u32 s56, s6, 0x100
	s_addc_u32 s57, s7, 0
	s_add_u32 s58, s4, 0x100
	s_addc_u32 s59, s5, 0
	s_add_u32 s60, s16, 0x100
	s_addc_u32 s61, s17, 0
	s_add_u32 s62, s18, 0x100
	s_addc_u32 s63, s19, 0
	s_mul_hi_u32 s64, s9, 0x55555556
	s_add_i32 s64, s64, -1
	ds_read_b128 v[168:171], v79 offset:0
	ds_read_b128 v[184:187], v82 offset:16384
	ds_read_b128 v[188:191], v82 offset:18432
	ds_read_b128 v[192:195], v82 offset:20480
	ds_read_b128 v[172:175], v79 offset:2048
	ds_read_b128 v[176:179], v79 offset:4096
	ds_read_b128 v[180:183], v79 offset:6144
	v_mov_b32_e32 v120, 0
	v_mov_b32_e32 v121, 0
	v_mov_b32_e32 v122, 0
	v_mov_b32_e32 v123, 0
	v_mov_b32_e32 v124, 0
	v_mov_b32_e32 v125, 0
	v_mov_b32_e32 v126, 0
	v_mov_b32_e32 v127, 0
	v_mov_b32_e32 v128, 0
	v_mov_b32_e32 v129, 0
	v_mov_b32_e32 v130, 0
	v_mov_b32_e32 v131, 0
	v_mov_b32_e32 v132, 0
	v_mov_b32_e32 v133, 0
	v_mov_b32_e32 v134, 0
	v_mov_b32_e32 v135, 0
	v_mov_b32_e32 v136, 0
	v_mov_b32_e32 v137, 0
	v_mov_b32_e32 v138, 0
	v_mov_b32_e32 v139, 0
	v_mov_b32_e32 v140, 0
	v_mov_b32_e32 v141, 0
	v_mov_b32_e32 v142, 0
	v_mov_b32_e32 v143, 0
	v_mov_b32_e32 v144, 0
	v_mov_b32_e32 v145, 0
	v_mov_b32_e32 v146, 0
	v_mov_b32_e32 v147, 0
	v_mov_b32_e32 v148, 0
	v_mov_b32_e32 v149, 0
	v_mov_b32_e32 v150, 0
	v_mov_b32_e32 v151, 0
	v_mov_b32_e32 v152, 0
	v_mov_b32_e32 v153, 0
	v_mov_b32_e32 v154, 0
	v_mov_b32_e32 v155, 0
	v_mov_b32_e32 v156, 0
	v_mov_b32_e32 v157, 0
	v_mov_b32_e32 v158, 0
	v_mov_b32_e32 v159, 0
	v_mov_b32_e32 v160, 0
	v_mov_b32_e32 v161, 0
	v_mov_b32_e32 v162, 0
	v_mov_b32_e32 v163, 0
	v_mov_b32_e32 v164, 0
	v_mov_b32_e32 v165, 0
	v_mov_b32_e32 v166, 0
	v_mov_b32_e32 v167, 0
	s_waitcnt lgkmcnt(0)
	v_mfma_f32_16x16x32_f16 v[120:123], v[184:187], v[168:171], v[120:123]
	ds_read_b128 v[196:199], v83 offset:0
	v_mfma_f32_16x16x32_f16 v[124:127], v[188:191], v[168:171], v[124:127]
	ds_read_b128 v[212:215], v81 offset:16384
	v_mfma_f32_16x16x32_f16 v[128:131], v[192:195], v[168:171], v[128:131]
	ds_read_b128 v[216:219], v81 offset:18432
	v_mfma_f32_16x16x32_f16 v[132:135], v[184:187], v[172:175], v[132:135]
	ds_read_b128 v[220:223], v81 offset:20480
	v_mfma_f32_16x16x32_f16 v[136:139], v[188:191], v[172:175], v[136:139]
	ds_read_b128 v[200:203], v83 offset:2048
	v_mfma_f32_16x16x32_f16 v[140:143], v[192:195], v[172:175], v[140:143]
	ds_read_b128 v[204:207], v83 offset:4096
	v_mfma_f32_16x16x32_f16 v[144:147], v[184:187], v[176:179], v[144:147]
	ds_read_b128 v[208:211], v83 offset:6144
	v_mfma_f32_16x16x32_f16 v[148:151], v[188:191], v[176:179], v[148:151]
	v_mfma_f32_16x16x32_f16 v[152:155], v[192:195], v[176:179], v[152:155]
	v_mfma_f32_16x16x32_f16 v[156:159], v[184:187], v[180:183], v[156:159]
	v_mfma_f32_16x16x32_f16 v[160:163], v[188:191], v[180:183], v[160:163]
	v_mfma_f32_16x16x32_f16 v[164:167], v[192:195], v[180:183], v[164:167]
	s_cmp_ge_u32 s25, 0x1000
	s_cbranch_scc1 .Lgk_loop_dnB
.Lgk_loop_dnA:
	s_waitcnt vmcnt(5) lgkmcnt(0)
	s_barrier
	s_mov_b32 m0, s25
	s_add_u32 s54, s54, 0x80
	s_addc_u32 s55, s55, 0
	global_load_lds_dwordx4 v84, s[54:55]
	s_mov_b32 m0, s26
	s_add_u32 s56, s56, 0x80
	s_addc_u32 s57, s57, 0
	global_load_lds_dwordx4 v84, s[56:57]
	s_mov_b32 m0, s27
	s_add_u32 s58, s58, 0x80
	s_addc_u32 s59, s59, 0
	global_load_lds_dwordx4 v84, s[58:59]
	s_mov_b32 m0, s28
	s_add_u32 s60, s60, 0x80
	s_addc_u32 s61, s61, 0
	global_load_lds_dwordx4 v84, s[60:61]
	s_mov_b32 m0, s29
	s_add_u32 s62, s62, 0x80
	s_addc_u32 s63, s63, 0
	global_load_lds_dwordx4 v84, s[62:63]
	v_mfma_f32_16x16x32_f16 v[120:123], v[212:215], v[196:199], v[120:123]
	ds_read_b128 v[168:171], v79 offset:40960
	v_mfma_f32_16x16x32_f16 v[124:127], v[216:219], v[196:199], v[124:127]
	ds_read_b128 v[184:187], v82 offset:57344
	v_mfma_f32_16x16x32_f16 v[128:131], v[220:223], v[196:199], v[128:131]
	ds_read_b128 v[188:191], v82 offset:59392
	v_mfma_f32_16x16x32_f16 v[132:135], v[212:215], v[200:203], v[132:135]
	ds_read_b128 v[192:195], v82 offset:61440
	v_mfma_f32_16x16x32_f16 v[136:139], v[216:219], v[200:203], v[136:139]
	ds_read_b128 v[172:175], v79 offset:43008
	v_mfma_f32_16x16x32_f16 v[140:143], v[220:223], v[200:203], v[140:143]
	ds_read_b128 v[176:179], v79 offset:45056
	v_mfma_f32_16x16x32_f16 v[144:147], v[212:215], v[204:207], v[144:147]
	ds_read_b128 v[180:183], v79 offset:47104
	v_mfma_f32_16x16x32_f16 v[148:151], v[216:219], v[204:207], v[148:151]
	v_mfma_f32_16x16x32_f16 v[152:155], v[220:223], v[204:207], v[152:155]
	v_mfma_f32_16x16x32_f16 v[156:159], v[212:215], v[208:211], v[156:159]
	v_mfma_f32_16x16x32_f16 v[160:163], v[216:219], v[208:211], v[160:163]
	v_mfma_f32_16x16x32_f16 v[164:167], v[220:223], v[208:211], v[164:167]
	s_waitcnt lgkmcnt(0)
	v_mfma_f32_16x16x32_f16 v[120:123], v[184:187], v[168:171], v[120:123]
	ds_read_b128 v[196:199], v83 offset:40960
	v_mfma_f32_16x16x32_f16 v[124:127], v[188:191], v[168:171], v[124:127]
	ds_read_b128 v[212:215], v81 offset:57344
	v_mfma_f32_16x16x32_f16 v[128:131], v[192:195], v[168:171], v[128:131]
	ds_read_b128 v[216:219], v81 offset:59392
	v_mfma_f32_16x16x32_f16 v[132:135], v[184:187], v[172:175], v[132:135]
	ds_read_b128 v[220:223], v81 offset:61440
	v_mfma_f32_16x16x32_f16 v[136:139], v[188:191], v[172:175], v[136:139]
	ds_read_b128 v[200:203], v83 offset:43008
	v_mfma_f32_16x16x32_f16 v[140:143], v[192:195], v[172:175], v[140:143]
	ds_read_b128 v[204:207], v83 offset:45056
	v_mfma_f32_16x16x32_f16 v[144:147], v[184:187], v[176:179], v[144:147]
	ds_read_b128 v[208:211], v83 offset:47104
	v_mfma_f32_16x16x32_f16 v[148:151], v[188:191], v[176:179], v[148:151]
	v_mfma_f32_16x16x32_f16 v[152:155], v[192:195], v[176:179], v[152:155]
	v_mfma_f32_16x16x32_f16 v[156:159], v[184:187], v[180:183], v[156:159]
	v_mfma_f32_16x16x32_f16 v[160:163], v[188:191], v[180:183], v[160:163]
	v_mfma_f32_16x16x32_f16 v[164:167], v[192:195], v[180:183], v[164:167]
	s_waitcnt vmcnt(5) lgkmcnt(0)
	s_barrier
	s_mov_b32 m0, s30
	s_add_u32 s54, s54, 0x80
	s_addc_u32 s55, s55, 0
	global_load_lds_dwordx4 v84, s[54:55]
	s_mov_b32 m0, s31
	s_add_u32 s56, s56, 0x80
	s_addc_u32 s57, s57, 0
	global_load_lds_dwordx4 v84, s[56:57]
	s_mov_b32 m0, s33
	s_add_u32 s58, s58, 0x80
	s_addc_u32 s59, s59, 0
	global_load_lds_dwordx4 v84, s[58:59]
	s_mov_b32 m0, s34
	s_add_u32 s60, s60, 0x80
	s_addc_u32 s61, s61, 0
	global_load_lds_dwordx4 v84, s[60:61]
	s_mov_b32 m0, s35
	s_add_u32 s62, s62, 0x80
	s_addc_u32 s63, s63, 0
	global_load_lds_dwordx4 v84, s[62:63]
	v_mfma_f32_16x16x32_f16 v[120:123], v[212:215], v[196:199], v[120:123]
	ds_read_b128 v[168:171], v100 offset:0
	v_mfma_f32_16x16x32_f16 v[124:127], v[216:219], v[196:199], v[124:127]
	ds_read_b128 v[184:187], v102 offset:16384
	v_mfma_f32_16x16x32_f16 v[128:131], v[220:223], v[196:199], v[128:131]
	ds_read_b128 v[188:191], v102 offset:18432
	v_mfma_f32_16x16x32_f16 v[132:135], v[212:215], v[200:203], v[132:135]
	ds_read_b128 v[192:195], v102 offset:20480
	v_mfma_f32_16x16x32_f16 v[136:139], v[216:219], v[200:203], v[136:139]
	ds_read_b128 v[172:175], v100 offset:2048
	v_mfma_f32_16x16x32_f16 v[140:143], v[220:223], v[200:203], v[140:143]
	ds_read_b128 v[176:179], v100 offset:4096
	v_mfma_f32_16x16x32_f16 v[144:147], v[212:215], v[204:207], v[144:147]
	ds_read_b128 v[180:183], v100 offset:6144
	v_mfma_f32_16x16x32_f16 v[148:151], v[216:219], v[204:207], v[148:151]
	v_mfma_f32_16x16x32_f16 v[152:155], v[220:223], v[204:207], v[152:155]
	v_mfma_f32_16x16x32_f16 v[156:159], v[212:215], v[208:211], v[156:159]
	v_mfma_f32_16x16x32_f16 v[160:163], v[216:219], v[208:211], v[160:163]
	v_mfma_f32_16x16x32_f16 v[164:167], v[220:223], v[208:211], v[164:167]
	s_waitcnt lgkmcnt(0)
	v_mfma_f32_16x16x32_f16 v[120:123], v[184:187], v[168:171], v[120:123]
	ds_read_b128 v[196:199], v101 offset:0
	v_mfma_f32_16x16x32_f16 v[124:127], v[188:191], v[168:171], v[124:127]
	ds_read_b128 v[212:215], v103 offset:16384
	v_mfma_f32_16x16x32_f16 v[128:131], v[192:195], v[168:171], v[128:131]
	ds_read_b128 v[216:219], v103 offset:18432
	v_mfma_f32_16x16x32_f16 v[132:135], v[184:187], v[172:175], v[132:135]
	ds_read_b128 v[220:223], v103 offset:20480
	v_mfma_f32_16x16x32_f16 v[136:139], v[188:191], v[172:175], v[136:139]
	ds_read_b128 v[200:203], v101 offset:2048
	v_mfma_f32_16x16x32_f16 v[140:143], v[192:195], v[172:175], v[140:143]
	ds_read_b128 v[204:207], v101 offset:4096
	v_mfma_f32_16x16x32_f16 v[144:147], v[184:187], v[176:179], v[144:147]
	ds_read_b128 v[208:211], v101 offset:6144
	v_mfma_f32_16x16x32_f16 v[148:151], v[188:191], v[176:179], v[148:151]
	v_mfma_f32_16x16x32_f16 v[152:155], v[192:195], v[176:179], v[152:155]
	v_mfma_f32_16x16x32_f16 v[156:159], v[184:187], v[180:183], v[156:159]
	v_mfma_f32_16x16x32_f16 v[160:163], v[188:191], v[180:183], v[160:163]
	v_mfma_f32_16x16x32_f16 v[164:167], v[192:195], v[180:183], v[164:167]
	s_waitcnt vmcnt(5) lgkmcnt(0)
	s_barrier
	s_mov_b32 m0, s36
	s_add_u32 s54, s54, 0x80
	s_addc_u32 s55, s55, 0
	global_load_lds_dwordx4 v84, s[54:55]
	s_mov_b32 m0, s37
	s_add_u32 s56, s56, 0x80
	s_addc_u32 s57, s57, 0
	global_load_lds_dwordx4 v84, s[56:57]
	s_mov_b32 m0, s38
	s_add_u32 s58, s58, 0x80
	s_addc_u32 s59, s59, 0
	global_load_lds_dwordx4 v84, s[58:59]
	s_mov_b32 m0, s39
	s_add_u32 s60, s60, 0x80
	s_addc_u32 s61, s61, 0
	global_load_lds_dwordx4 v84, s[60:61]
	s_mov_b32 m0, s40
	s_add_u32 s62, s62, 0x80
	s_addc_u32 s63, s63, 0
	global_load_lds_dwordx4 v84, s[62:63]
	v_mfma_f32_16x16x32_f16 v[120:123], v[212:215], v[196:199], v[120:123]
	ds_read_b128 v[168:171], v79 offset:0
	v_mfma_f32_16x16x32_f16 v[124:127], v[216:219], v[196:199], v[124:127]
	ds_read_b128 v[184:187], v82 offset:16384
	v_mfma_f32_16x16x32_f16 v[128:131], v[220:223], v[196:199], v[128:131]
	ds_read_b128 v[188:191], v82 offset:18432
	v_mfma_f32_16x16x32_f16 v[132:135], v[212:215], v[200:203], v[132:135]
	ds_read_b128 v[192:195], v82 offset:20480
	v_mfma_f32_16x16x32_f16 v[136:139], v[216:219], v[200:203], v[136:139]
	ds_read_b128 v[172:175], v79 offset:2048
	v_mfma_f32_16x16x32_f16 v[140:143], v[220:223], v[200:203], v[140:143]
	ds_read_b128 v[176:179], v79 offset:4096
	v_mfma_f32_16x16x32_f16 v[144:147], v[212:215], v[204:207], v[144:147]
	ds_read_b128 v[180:183], v79 offset:6144
	v_mfma_f32_16x16x32_f16 v[148:151], v[216:219], v[204:207], v[148:151]
	v_mfma_f32_16x16x32_f16 v[152:155], v[220:223], v[204:207], v[152:155]
	v_mfma_f32_16x16x32_f16 v[156:159], v[212:215], v[208:211], v[156:159]
	v_mfma_f32_16x16x32_f16 v[160:163], v[216:219], v[208:211], v[160:163]
	v_mfma_f32_16x16x32_f16 v[164:167], v[220:223], v[208:211], v[164:167]
	s_waitcnt lgkmcnt(0)
	v_mfma_f32_16x16x32_f16 v[120:123], v[184:187], v[168:171], v[120:123]
	ds_read_b128 v[196:199], v83 offset:0
	v_mfma_f32_16x16x32_f16 v[124:127], v[188:191], v[168:171], v[124:127]
	ds_read_b128 v[212:215], v81 offset:16384
	v_mfma_f32_16x16x32_f16 v[128:131], v[192:195], v[168:171], v[128:131]
	ds_read_b128 v[216:219], v81 offset:18432
	v_mfma_f32_16x16x32_f16 v[132:135], v[184:187], v[172:175], v[132:135]
	ds_read_b128 v[220:223], v81 offset:20480
	v_mfma_f32_16x16x32_f16 v[136:139], v[188:191], v[172:175], v[136:139]
	ds_read_b128 v[200:203], v83 offset:2048
	v_mfma_f32_16x16x32_f16 v[140:143], v[192:195], v[172:175], v[140:143]
	ds_read_b128 v[204:207], v83 offset:4096
	v_mfma_f32_16x16x32_f16 v[144:147], v[184:187], v[176:179], v[144:147]
	ds_read_b128 v[208:211], v83 offset:6144
	v_mfma_f32_16x16x32_f16 v[148:151], v[188:191], v[176:179], v[148:151]
	v_mfma_f32_16x16x32_f16 v[152:155], v[192:195], v[176:179], v[152:155]
	v_mfma_f32_16x16x32_f16 v[156:159], v[184:187], v[180:183], v[156:159]
	v_mfma_f32_16x16x32_f16 v[160:163], v[188:191], v[180:183], v[160:163]
	v_mfma_f32_16x16x32_f16 v[164:167], v[192:195], v[180:183], v[164:167]
	s_add_i32 s64, s64, -1
	s_cmp_lg_u32 s64, 0
	s_cbranch_scc1 .Lgk_loop_dnA
	s_waitcnt vmcnt(5) lgkmcnt(0)
	s_barrier
	v_mfma_f32_16x16x32_f16 v[120:123], v[212:215], v[196:199], v[120:123]
	ds_read_b128 v[168:171], v79 offset:40960
	v_mfma_f32_16x16x32_f16 v[124:127], v[216:219], v[196:199], v[124:127]
	ds_read_b128 v[184:187], v82 offset:57344
	v_mfma_f32_16x16x32_f16 v[128:131], v[220:223], v[196:199], v[128:131]
	ds_read_b128 v[188:191], v82 offset:59392
	v_mfma_f32_16x16x32_f16 v[132:135], v[212:215], v[200:203], v[132:135]
	ds_read_b128 v[192:195], v82 offset:61440
	v_mfma_f32_16x16x32_f16 v[136:139], v[216:219], v[200:203], v[136:139]
	ds_read_b128 v[172:175], v79 offset:43008
	v_mfma_f32_16x16x32_f16 v[140:143], v[220:223], v[200:203], v[140:143]
	ds_read_b128 v[176:179], v79 offset:45056
	v_mfma_f32_16x16x32_f16 v[144:147], v[212:215], v[204:207], v[144:147]
	ds_read_b128 v[180:183], v79 offset:47104
	v_mfma_f32_16x16x32_f16 v[148:151], v[216:219], v[204:207], v[148:151]
	v_mfma_f32_16x16x32_f16 v[152:155], v[220:223], v[204:207], v[152:155]
	v_mfma_f32_16x16x32_f16 v[156:159], v[212:215], v[208:211], v[156:159]
	v_mfma_f32_16x16x32_f16 v[160:163], v[216:219], v[208:211], v[160:163]
	v_mfma_f32_16x16x32_f16 v[164:167], v[220:223], v[208:211], v[164:167]
	s_waitcnt lgkmcnt(0)
	v_mfma_f32_16x16x32_f16 v[120:123], v[184:187], v[168:171], v[120:123]
	ds_read_b128 v[196:199], v83 offset:40960
	v_mfma_f32_16x16x32_f16 v[124:127], v[188:191], v[168:171], v[124:127]
	ds_read_b128 v[212:215], v81 offset:57344
	v_mfma_f32_16x16x32_f16 v[128:131], v[192:195], v[168:171], v[128:131]
	ds_read_b128 v[216:219], v81 offset:59392
	v_mfma_f32_16x16x32_f16 v[132:135], v[184:187], v[172:175], v[132:135]
	ds_read_b128 v[220:223], v81 offset:61440
	v_mfma_f32_16x16x32_f16 v[136:139], v[188:191], v[172:175], v[136:139]
	ds_read_b128 v[200:203], v83 offset:43008
	v_mfma_f32_16x16x32_f16 v[140:143], v[192:195], v[172:175], v[140:143]
	ds_read_b128 v[204:207], v83 offset:45056
	v_mfma_f32_16x16x32_f16 v[144:147], v[184:187], v[176:179], v[144:147]
	ds_read_b128 v[208:211], v83 offset:47104
	v_mfma_f32_16x16x32_f16 v[148:151], v[188:191], v[176:179], v[148:151]
	v_mfma_f32_16x16x32_f16 v[152:155], v[192:195], v[176:179], v[152:155]
	v_mfma_f32_16x16x32_f16 v[156:159], v[184:187], v[180:183], v[156:159]
	v_mfma_f32_16x16x32_f16 v[160:163], v[188:191], v[180:183], v[160:163]
	v_mfma_f32_16x16x32_f16 v[164:167], v[192:195], v[180:183], v[164:167]
	s_waitcnt vmcnt(0) lgkmcnt(0)
	s_barrier
	v_mfma_f32_16x16x32_f16 v[120:123], v[212:215], v[196:199], v[120:123]
	ds_read_b128 v[168:171], v100 offset:0
	v_mfma_f32_16x16x32_f16 v[124:127], v[216:219], v[196:199], v[124:127]
	ds_read_b128 v[184:187], v102 offset:16384
	v_mfma_f32_16x16x32_f16 v[128:131], v[220:223], v[196:199], v[128:131]
	ds_read_b128 v[188:191], v102 offset:18432
	v_mfma_f32_16x16x32_f16 v[132:135], v[212:215], v[200:203], v[132:135]
	ds_read_b128 v[192:195], v102 offset:20480
	v_mfma_f32_16x16x32_f16 v[136:139], v[216:219], v[200:203], v[136:139]
	ds_read_b128 v[172:175], v100 offset:2048
	v_mfma_f32_16x16x32_f16 v[140:143], v[220:223], v[200:203], v[140:143]
	ds_read_b128 v[176:179], v100 offset:4096
	v_mfma_f32_16x16x32_f16 v[144:147], v[212:215], v[204:207], v[144:147]
	ds_read_b128 v[180:183], v100 offset:6144
	v_mfma_f32_16x16x32_f16 v[148:151], v[216:219], v[204:207], v[148:151]
	v_mfma_f32_16x16x32_f16 v[152:155], v[220:223], v[204:207], v[152:155]
	v_mfma_f32_16x16x32_f16 v[156:159], v[212:215], v[208:211], v[156:159]
	v_mfma_f32_16x16x32_f16 v[160:163], v[216:219], v[208:211], v[160:163]
	v_mfma_f32_16x16x32_f16 v[164:167], v[220:223], v[208:211], v[164:167]
	s_waitcnt lgkmcnt(0)
	v_mfma_f32_16x16x32_f16 v[120:123], v[184:187], v[168:171], v[120:123]
	ds_read_b128 v[196:199], v101 offset:0
	v_mfma_f32_16x16x32_f16 v[124:127], v[188:191], v[168:171], v[124:127]
	ds_read_b128 v[212:215], v103 offset:16384
	v_mfma_f32_16x16x32_f16 v[128:131], v[192:195], v[168:171], v[128:131]
	ds_read_b128 v[216:219], v103 offset:18432
	v_mfma_f32_16x16x32_f16 v[132:135], v[184:187], v[172:175], v[132:135]
	ds_read_b128 v[220:223], v103 offset:20480
	v_mfma_f32_16x16x32_f16 v[136:139], v[188:191], v[172:175], v[136:139]
	ds_read_b128 v[200:203], v101 offset:2048
	v_mfma_f32_16x16x32_f16 v[140:143], v[192:195], v[172:175], v[140:143]
	ds_read_b128 v[204:207], v101 offset:4096
	v_mfma_f32_16x16x32_f16 v[144:147], v[184:187], v[176:179], v[144:147]
	ds_read_b128 v[208:211], v101 offset:6144
	v_mfma_f32_16x16x32_f16 v[148:151], v[188:191], v[176:179], v[148:151]
	v_mfma_f32_16x16x32_f16 v[152:155], v[192:195], v[176:179], v[152:155]
	v_mfma_f32_16x16x32_f16 v[156:159], v[184:187], v[180:183], v[156:159]
	v_mfma_f32_16x16x32_f16 v[160:163], v[188:191], v[180:183], v[160:163]
	v_mfma_f32_16x16x32_f16 v[164:167], v[192:195], v[180:183], v[164:167]
	s_waitcnt lgkmcnt(0)
	v_mfma_f32_16x16x32_f16 v[120:123], v[212:215], v[196:199], v[120:123]
	v_mfma_f32_16x16x32_f16 v[124:127], v[216:219], v[196:199], v[124:127]
	v_mfma_f32_16x16x32_f16 v[128:131], v[220:223], v[196:199], v[128:131]
	v_mfma_f32_16x16x32_f16 v[132:135], v[212:215], v[200:203], v[132:135]
	v_mfma_f32_16x16x32_f16 v[136:139], v[216:219], v[200:203], v[136:139]
	v_mfma_f32_16x16x32_f16 v[140:143], v[220:223], v[200:203], v[140:143]
	v_mfma_f32_16x16x32_f16 v[144:147], v[212:215], v[204:207], v[144:147]
	v_mfma_f32_16x16x32_f16 v[148:151], v[216:219], v[204:207], v[148:151]
	v_mfma_f32_16x16x32_f16 v[152:155], v[220:223], v[204:207], v[152:155]
	v_mfma_f32_16x16x32_f16 v[156:159], v[212:215], v[208:211], v[156:159]
	v_mfma_f32_16x16x32_f16 v[160:163], v[216:219], v[208:211], v[160:163]
	v_mfma_f32_16x16x32_f16 v[164:167], v[220:223], v[208:211], v[164:167]
	s_branch .Lgk_loop_dn_done
.Lgk_loop_dnB:
	s_waitcnt vmcnt(5) lgkmcnt(0)
	s_barrier
	v_mfma_f32_16x16x32_f16 v[120:123], v[212:215], v[196:199], v[120:123]
	ds_read_b128 v[168:171], v79 offset:40960
	v_mfma_f32_16x16x32_f16 v[124:127], v[216:219], v[196:199], v[124:127]
	ds_read_b128 v[184:187], v82 offset:57344
	v_mfma_f32_16x16x32_f16 v[128:131], v[220:223], v[196:199], v[128:131]
	ds_read_b128 v[188:191], v82 offset:59392
	v_mfma_f32_16x16x32_f16 v[132:135], v[212:215], v[200:203], v[132:135]
	ds_read_b128 v[192:195], v82 offset:61440
	v_mfma_f32_16x16x32_f16 v[136:139], v[216:219], v[200:203], v[136:139]
	ds_read_b128 v[172:175], v79 offset:43008
	v_mfma_f32_16x16x32_f16 v[140:143], v[220:223], v[200:203], v[140:143]
	ds_read_b128 v[176:179], v79 offset:45056
	v_mfma_f32_16x16x32_f16 v[144:147], v[212:215], v[204:207], v[144:147]
	ds_read_b128 v[180:183], v79 offset:47104
	v_mfma_f32_16x16x32_f16 v[148:151], v[216:219], v[204:207], v[148:151]
	v_mfma_f32_16x16x32_f16 v[152:155], v[220:223], v[204:207], v[152:155]
	v_mfma_f32_16x16x32_f16 v[156:159], v[212:215], v[208:211], v[156:159]
	v_mfma_f32_16x16x32_f16 v[160:163], v[216:219], v[208:211], v[160:163]
	v_mfma_f32_16x16x32_f16 v[164:167], v[220:223], v[208:211], v[164:167]
	s_waitcnt lgkmcnt(0)
	v_mfma_f32_16x16x32_f16 v[120:123], v[184:187], v[168:171], v[120:123]
	ds_read_b128 v[196:199], v83 offset:40960
	v_mfma_f32_16x16x32_f16 v[124:127], v[188:191], v[168:171], v[124:127]
	ds_read_b128 v[212:215], v81 offset:57344
	v_mfma_f32_16x16x32_f16 v[128:131], v[192:195], v[168:171], v[128:131]
	ds_read_b128 v[216:219], v81 offset:59392
	v_mfma_f32_16x16x32_f16 v[132:135], v[184:187], v[172:175], v[132:135]
	ds_read_b128 v[220:223], v81 offset:61440
	v_mfma_f32_16x16x32_f16 v[136:139], v[188:191], v[172:175], v[136:139]
	ds_read_b128 v[200:203], v83 offset:43008
	v_mfma_f32_16x16x32_f16 v[140:143], v[192:195], v[172:175], v[140:143]
	ds_read_b128 v[204:207], v83 offset:45056
	v_mfma_f32_16x16x32_f16 v[144:147], v[184:187], v[176:179], v[144:147]
	ds_read_b128 v[208:211], v83 offset:47104
	v_mfma_f32_16x16x32_f16 v[148:151], v[188:191], v[176:179], v[148:151]
	v_mfma_f32_16x16x32_f16 v[152:155], v[192:195], v[176:179], v[152:155]
	v_mfma_f32_16x16x32_f16 v[156:159], v[184:187], v[180:183], v[156:159]
	v_mfma_f32_16x16x32_f16 v[160:163], v[188:191], v[180:183], v[160:163]
	v_mfma_f32_16x16x32_f16 v[164:167], v[192:195], v[180:183], v[164:167]
	s_mov_b32 m0, s25
	s_add_u32 s54, s54, 0x80
	s_addc_u32 s55, s55, 0
	global_load_lds_dwordx4 v84, s[54:55]
	s_mov_b32 m0, s26
	s_add_u32 s56, s56, 0x80
	s_addc_u32 s57, s57, 0
	global_load_lds_dwordx4 v84, s[56:57]
	s_mov_b32 m0, s27
	s_add_u32 s58, s58, 0x80
	s_addc_u32 s59, s59, 0
	global_load_lds_dwordx4 v84, s[58:59]
	s_mov_b32 m0, s28
	s_add_u32 s60, s60, 0x80
	s_addc_u32 s61, s61, 0
	global_load_lds_dwordx4 v84, s[60:61]
	s_mov_b32 m0, s29
	s_add_u32 s62, s62, 0x80
	s_addc_u32 s63, s63, 0
	global_load_lds_dwordx4 v84, s[62:63]
	s_waitcnt vmcnt(5) lgkmcnt(0)
	s_barrier
	v_mfma_f32_16x16x32_f16 v[120:123], v[212:215], v[196:199], v[120:123]
	ds_read_b128 v[168:171], v100 offset:0
	v_mfma_f32_16x16x32_f16 v[124:127], v[216:219], v[196:199], v[124:127]
	ds_read_b128 v[184:187], v102 offset:16384
	v_mfma_f32_16x16x32_f16 v[128:131], v[220:223], v[196:199], v[128:131]
	ds_read_b128 v[188:191], v102 offset:18432
	v_mfma_f32_16x16x32_f16 v[132:135], v[212:215], v[200:203], v[132:135]
	ds_read_b128 v[192:195], v102 offset:20480
	v_mfma_f32_16x16x32_f16 v[136:139], v[216:219], v[200:203], v[136:139]
	ds_read_b128 v[172:175], v100 offset:2048
	v_mfma_f32_16x16x32_f16 v[140:143], v[220:223], v[200:203], v[140:143]
	ds_read_b128 v[176:179], v100 offset:4096
	v_mfma_f32_16x16x32_f16 v[144:147], v[212:215], v[204:207], v[144:147]
	ds_read_b128 v[180:183], v100 offset:6144
	v_mfma_f32_16x16x32_f16 v[148:151], v[216:219], v[204:207], v[148:151]
	v_mfma_f32_16x16x32_f16 v[152:155], v[220:223], v[204:207], v[152:155]
	v_mfma_f32_16x16x32_f16 v[156:159], v[212:215], v[208:211], v[156:159]
	v_mfma_f32_16x16x32_f16 v[160:163], v[216:219], v[208:211], v[160:163]
	v_mfma_f32_16x16x32_f16 v[164:167], v[220:223], v[208:211], v[164:167]
	s_waitcnt lgkmcnt(0)
	v_mfma_f32_16x16x32_f16 v[120:123], v[184:187], v[168:171], v[120:123]
	ds_read_b128 v[196:199], v101 offset:0
	v_mfma_f32_16x16x32_f16 v[124:127], v[188:191], v[168:171], v[124:127]
	ds_read_b128 v[212:215], v103 offset:16384
	v_mfma_f32_16x16x32_f16 v[128:131], v[192:195], v[168:171], v[128:131]
	ds_read_b128 v[216:219], v103 offset:18432
	v_mfma_f32_16x16x32_f16 v[132:135], v[184:187], v[172:175], v[132:135]
	ds_read_b128 v[220:223], v103 offset:20480
	v_mfma_f32_16x16x32_f16 v[136:139], v[188:191], v[172:175], v[136:139]
	ds_read_b128 v[200:203], v101 offset:2048
	v_mfma_f32_16x16x32_f16 v[140:143], v[192:195], v[172:175], v[140:143]
	ds_read_b128 v[204:207], v101 offset:4096
	v_mfma_f32_16x16x32_f16 v[144:147], v[184:187], v[176:179], v[144:147]
	ds_read_b128 v[208:211], v101 offset:6144
	v_mfma_f32_16x16x32_f16 v[148:151], v[188:191], v[176:179], v[148:151]
	v_mfma_f32_16x16x32_f16 v[152:155], v[192:195], v[176:179], v[152:155]
	v_mfma_f32_16x16x32_f16 v[156:159], v[184:187], v[180:183], v[156:159]
	v_mfma_f32_16x16x32_f16 v[160:163], v[188:191], v[180:183], v[160:163]
	v_mfma_f32_16x16x32_f16 v[164:167], v[192:195], v[180:183], v[164:167]
	s_mov_b32 m0, s30
	s_add_u32 s54, s54, 0x80
	s_addc_u32 s55, s55, 0
	global_load_lds_dwordx4 v84, s[54:55]
	s_mov_b32 m0, s31
	s_add_u32 s56, s56, 0x80
	s_addc_u32 s57, s57, 0
	global_load_lds_dwordx4 v84, s[56:57]
	s_mov_b32 m0, s33
	s_add_u32 s58, s58, 0x80
	s_addc_u32 s59, s59, 0
	global_load_lds_dwordx4 v84, s[58:59]
	s_mov_b32 m0, s34
	s_add_u32 s60, s60, 0x80
	s_addc_u32 s61, s61, 0
	global_load_lds_dwordx4 v84, s[60:61]
	s_mov_b32 m0, s35
	s_add_u32 s62, s62, 0x80
	s_addc_u32 s63, s63, 0
	global_load_lds_dwordx4 v84, s[62:63]
	s_waitcnt vmcnt(5) lgkmcnt(0)
	s_barrier
	v_mfma_f32_16x16x32_f16 v[120:123], v[212:215], v[196:199], v[120:123]
	ds_read_b128 v[168:171], v79 offset:0
	v_mfma_f32_16x16x32_f16 v[124:127], v[216:219], v[196:199], v[124:127]
	ds_read_b128 v[184:187], v82 offset:16384
	v_mfma_f32_16x16x32_f16 v[128:131], v[220:223], v[196:199], v[128:131]
	ds_read_b128 v[188:191], v82 offset:18432
	v_mfma_f32_16x16x32_f16 v[132:135], v[212:215], v[200:203], v[132:135]
	ds_read_b128 v[192:195], v82 offset:20480
	v_mfma_f32_16x16x32_f16 v[136:139], v[216:219], v[200:203], v[136:139]
	ds_read_b128 v[172:175], v79 offset:2048
	v_mfma_f32_16x16x32_f16 v[140:143], v[220:223], v[200:203], v[140:143]
	ds_read_b128 v[176:179], v79 offset:4096
	v_mfma_f32_16x16x32_f16 v[144:147], v[212:215], v[204:207], v[144:147]
	ds_read_b128 v[180:183], v79 offset:6144
	v_mfma_f32_16x16x32_f16 v[148:151], v[216:219], v[204:207], v[148:151]
	v_mfma_f32_16x16x32_f16 v[152:155], v[220:223], v[204:207], v[152:155]
	v_mfma_f32_16x16x32_f16 v[156:159], v[212:215], v[208:211], v[156:159]
	v_mfma_f32_16x16x32_f16 v[160:163], v[216:219], v[208:211], v[160:163]
	v_mfma_f32_16x16x32_f16 v[164:167], v[220:223], v[208:211], v[164:167]
	s_waitcnt lgkmcnt(0)
	v_mfma_f32_16x16x32_f16 v[120:123], v[184:187], v[168:171], v[120:123]
	ds_read_b128 v[196:199], v83 offset:0
	v_mfma_f32_16x16x32_f16 v[124:127], v[188:191], v[168:171], v[124:127]
	ds_read_b128 v[212:215], v81 offset:16384
	v_mfma_f32_16x16x32_f16 v[128:131], v[192:195], v[168:171], v[128:131]
	ds_read_b128 v[216:219], v81 offset:18432
	v_mfma_f32_16x16x32_f16 v[132:135], v[184:187], v[172:175], v[132:135]
	ds_read_b128 v[220:223], v81 offset:20480
	v_mfma_f32_16x16x32_f16 v[136:139], v[188:191], v[172:175], v[136:139]
	ds_read_b128 v[200:203], v83 offset:2048
	v_mfma_f32_16x16x32_f16 v[140:143], v[192:195], v[172:175], v[140:143]
	ds_read_b128 v[204:207], v83 offset:4096
	v_mfma_f32_16x16x32_f16 v[144:147], v[184:187], v[176:179], v[144:147]
	ds_read_b128 v[208:211], v83 offset:6144
	v_mfma_f32_16x16x32_f16 v[148:151], v[188:191], v[176:179], v[148:151]
	v_mfma_f32_16x16x32_f16 v[152:155], v[192:195], v[176:179], v[152:155]
	v_mfma_f32_16x16x32_f16 v[156:159], v[184:187], v[180:183], v[156:159]
	v_mfma_f32_16x16x32_f16 v[160:163], v[188:191], v[180:183], v[160:163]
	v_mfma_f32_16x16x32_f16 v[164:167], v[192:195], v[180:183], v[164:167]
	s_mov_b32 m0, s36
	s_add_u32 s54, s54, 0x80
	s_addc_u32 s55, s55, 0
	global_load_lds_dwordx4 v84, s[54:55]
	s_mov_b32 m0, s37
	s_add_u32 s56, s56, 0x80
	s_addc_u32 s57, s57, 0
	global_load_lds_dwordx4 v84, s[56:57]
	s_mov_b32 m0, s38
	s_add_u32 s58, s58, 0x80
	s_addc_u32 s59, s59, 0
	global_load_lds_dwordx4 v84, s[58:59]
	s_mov_b32 m0, s39
	s_add_u32 s60, s60, 0x80
	s_addc_u32 s61, s61, 0
	global_load_lds_dwordx4 v84, s[60:61]
	s_mov_b32 m0, s40
	s_add_u32 s62, s62, 0x80
	s_addc_u32 s63, s63, 0
	global_load_lds_dwordx4 v84, s[62:63]
	s_add_i32 s64, s64, -1
	s_cmp_lg_u32 s64, 0
	s_cbranch_scc1 .Lgk_loop_dnB
	s_waitcnt vmcnt(5) lgkmcnt(0)
	s_barrier
	v_mfma_f32_16x16x32_f16 v[120:123], v[212:215], v[196:199], v[120:123]
	ds_read_b128 v[168:171], v79 offset:40960
	v_mfma_f32_16x16x32_f16 v[124:127], v[216:219], v[196:199], v[124:127]
	ds_read_b128 v[184:187], v82 offset:57344
	v_mfma_f32_16x16x32_f16 v[128:131], v[220:223], v[196:199], v[128:131]
	ds_read_b128 v[188:191], v82 offset:59392
	v_mfma_f32_16x16x32_f16 v[132:135], v[212:215], v[200:203], v[132:135]
	ds_read_b128 v[192:195], v82 offset:61440
	v_mfma_f32_16x16x32_f16 v[136:139], v[216:219], v[200:203], v[136:139]
	ds_read_b128 v[172:175], v79 offset:43008
	v_mfma_f32_16x16x32_f16 v[140:143], v[220:223], v[200:203], v[140:143]
	ds_read_b128 v[176:179], v79 offset:45056
	v_mfma_f32_16x16x32_f16 v[144:147], v[212:215], v[204:207], v[144:147]
	ds_read_b128 v[180:183], v79 offset:47104
	v_mfma_f32_16x16x32_f16 v[148:151], v[216:219], v[204:207], v[148:151]
	v_mfma_f32_16x16x32_f16 v[152:155], v[220:223], v[204:207], v[152:155]
	v_mfma_f32_16x16x32_f16 v[156:159], v[212:215], v[208:211], v[156:159]
	v_mfma_f32_16x16x32_f16 v[160:163], v[216:219], v[208:211], v[160:163]
	v_mfma_f32_16x16x32_f16 v[164:167], v[220:223], v[208:211], v[164:167]
	s_waitcnt lgkmcnt(0)
	v_mfma_f32_16x16x32_f16 v[120:123], v[184:187], v[168:171], v[120:123]
	ds_read_b128 v[196:199], v83 offset:40960
	v_mfma_f32_16x16x32_f16 v[124:127], v[188:191], v[168:171], v[124:127]
	ds_read_b128 v[212:215], v81 offset:57344
	v_mfma_f32_16x16x32_f16 v[128:131], v[192:195], v[168:171], v[128:131]
	ds_read_b128 v[216:219], v81 offset:59392
	v_mfma_f32_16x16x32_f16 v[132:135], v[184:187], v[172:175], v[132:135]
	ds_read_b128 v[220:223], v81 offset:61440
	v_mfma_f32_16x16x32_f16 v[136:139], v[188:191], v[172:175], v[136:139]
	ds_read_b128 v[200:203], v83 offset:43008
	v_mfma_f32_16x16x32_f16 v[140:143], v[192:195], v[172:175], v[140:143]
	ds_read_b128 v[204:207], v83 offset:45056
	v_mfma_f32_16x16x32_f16 v[144:147], v[184:187], v[176:179], v[144:147]
	ds_read_b128 v[208:211], v83 offset:47104
	v_mfma_f32_16x16x32_f16 v[148:151], v[188:191], v[176:179], v[148:151]
	v_mfma_f32_16x16x32_f16 v[152:155], v[192:195], v[176:179], v[152:155]
	v_mfma_f32_16x16x32_f16 v[156:159], v[184:187], v[180:183], v[156:159]
	v_mfma_f32_16x16x32_f16 v[160:163], v[188:191], v[180:183], v[160:163]
	v_mfma_f32_16x16x32_f16 v[164:167], v[192:195], v[180:183], v[164:167]
	s_waitcnt vmcnt(0) lgkmcnt(0)
	s_barrier
	v_mfma_f32_16x16x32_f16 v[120:123], v[212:215], v[196:199], v[120:123]
	ds_read_b128 v[168:171], v100 offset:0
	v_mfma_f32_16x16x32_f16 v[124:127], v[216:219], v[196:199], v[124:127]
	ds_read_b128 v[184:187], v102 offset:16384
	v_mfma_f32_16x16x32_f16 v[128:131], v[220:223], v[196:199], v[128:131]
	ds_read_b128 v[188:191], v102 offset:18432
	v_mfma_f32_16x16x32_f16 v[132:135], v[212:215], v[200:203], v[132:135]
	ds_read_b128 v[192:195], v102 offset:20480
	v_mfma_f32_16x16x32_f16 v[136:139], v[216:219], v[200:203], v[136:139]
	ds_read_b128 v[172:175], v100 offset:2048
	v_mfma_f32_16x16x32_f16 v[140:143], v[220:223], v[200:203], v[140:143]
	ds_read_b128 v[176:179], v100 offset:4096
	v_mfma_f32_16x16x32_f16 v[144:147], v[212:215], v[204:207], v[144:147]
	ds_read_b128 v[180:183], v100 offset:6144
	v_mfma_f32_16x16x32_f16 v[148:151], v[216:219], v[204:207], v[148:151]
	v_mfma_f32_16x16x32_f16 v[152:155], v[220:223], v[204:207], v[152:155]
	v_mfma_f32_16x16x32_f16 v[156:159], v[212:215], v[208:211], v[156:159]
	v_mfma_f32_16x16x32_f16 v[160:163], v[216:219], v[208:211], v[160:163]
	v_mfma_f32_16x16x32_f16 v[164:167], v[220:223], v[208:211], v[164:167]
	s_waitcnt lgkmcnt(0)
	v_mfma_f32_16x16x32_f16 v[120:123], v[184:187], v[168:171], v[120:123]
	ds_read_b128 v[196:199], v101 offset:0
	v_mfma_f32_16x16x32_f16 v[124:127], v[188:191], v[168:171], v[124:127]
	ds_read_b128 v[212:215], v103 offset:16384
	v_mfma_f32_16x16x32_f16 v[128:131], v[192:195], v[168:171], v[128:131]
	ds_read_b128 v[216:219], v103 offset:18432
	v_mfma_f32_16x16x32_f16 v[132:135], v[184:187], v[172:175], v[132:135]
	ds_read_b128 v[220:223], v103 offset:20480
	v_mfma_f32_16x16x32_f16 v[136:139], v[188:191], v[172:175], v[136:139]
	ds_read_b128 v[200:203], v101 offset:2048
	v_mfma_f32_16x16x32_f16 v[140:143], v[192:195], v[172:175], v[140:143]
	ds_read_b128 v[204:207], v101 offset:4096
	v_mfma_f32_16x16x32_f16 v[144:147], v[184:187], v[176:179], v[144:147]
	ds_read_b128 v[208:211], v101 offset:6144
	v_mfma_f32_16x16x32_f16 v[148:151], v[188:191], v[176:179], v[148:151]
	v_mfma_f32_16x16x32_f16 v[152:155], v[192:195], v[176:179], v[152:155]
	v_mfma_f32_16x16x32_f16 v[156:159], v[184:187], v[180:183], v[156:159]
	v_mfma_f32_16x16x32_f16 v[160:163], v[188:191], v[180:183], v[160:163]
	v_mfma_f32_16x16x32_f16 v[164:167], v[192:195], v[180:183], v[164:167]
	s_waitcnt lgkmcnt(0)
	v_mfma_f32_16x16x32_f16 v[120:123], v[212:215], v[196:199], v[120:123]
	v_mfma_f32_16x16x32_f16 v[124:127], v[216:219], v[196:199], v[124:127]
	v_mfma_f32_16x16x32_f16 v[128:131], v[220:223], v[196:199], v[128:131]
	v_mfma_f32_16x16x32_f16 v[132:135], v[212:215], v[200:203], v[132:135]
	v_mfma_f32_16x16x32_f16 v[136:139], v[216:219], v[200:203], v[136:139]
	v_mfma_f32_16x16x32_f16 v[140:143], v[220:223], v[200:203], v[140:143]
	v_mfma_f32_16x16x32_f16 v[144:147], v[212:215], v[204:207], v[144:147]
	v_mfma_f32_16x16x32_f16 v[148:151], v[216:219], v[204:207], v[148:151]
	v_mfma_f32_16x16x32_f16 v[152:155], v[220:223], v[204:207], v[152:155]
	v_mfma_f32_16x16x32_f16 v[156:159], v[212:215], v[208:211], v[156:159]
	v_mfma_f32_16x16x32_f16 v[160:163], v[216:219], v[208:211], v[160:163]
	v_mfma_f32_16x16x32_f16 v[164:167], v[220:223], v[208:211], v[164:167]
.Lgk_loop_dn_done:
	s_nop 7
	s_nop 3
	v_bfe_u32 v96, v0, 4, 2
	v_lshlrev_b32_e32 v96, 2, v96
	s_add_i32 s2, s23, s0
	v_or_b32_e32 v98, s2, v96
	v_ashrrev_i32_e32 v99, 31, v98
	v_lshl_add_u64 v[98:99], v[98:99], 2, s[14:15]
	global_load_dwordx4 v[104:107], v[98:99], off
	global_load_dwordx4 v[108:111], v[98:99], off offset:64
	global_load_dwordx4 v[112:115], v[98:99], off offset:128
	s_movk_i32 s4, 0x310
	v_mul_lo_u32 v1, v1, s4
	s_movk_i32 s5, 0xffd0
	v_or_b32_e32 v97, s23, v96
	v_lshlrev_b32_e32 v97, 2, v97
	v_add3_u32 v1, 0, v97, v1
	s_lshl_b64 s[2:3], s[0:1], 1
	s_add_u32 s2, s12, s2
	s_addc_u32 s3, s13, s3
	s_lshl_b64 s[0:1], s[0:1], 2
	s_add_u32 s0, s10, s0
	s_addc_u32 s1, s11, s1
	v_mul_u32_u24_e32 v67, 0x556, v0
	s_waitcnt lgkmcnt(0)
	s_barrier
	s_waitcnt vmcnt(0)
	v_pk_add_f32 v[120:121], v[104:105], v[120:121]
	v_pk_add_f32 v[122:123], v[106:107], v[122:123]
	ds_write_b128 v1, v[120:123] offset:0
	v_pk_add_f32 v[124:125], v[108:109], v[124:125]
	v_pk_add_f32 v[126:127], v[110:111], v[126:127]
	ds_write_b128 v1, v[124:127] offset:64
	v_pk_add_f32 v[128:129], v[112:113], v[128:129]
	v_pk_add_f32 v[130:131], v[114:115], v[130:131]
	ds_write_b128 v1, v[128:131] offset:128
	v_pk_add_f32 v[132:133], v[104:105], v[132:133]
	v_pk_add_f32 v[134:135], v[106:107], v[134:135]
	ds_write_b128 v1, v[132:135] offset:12544
	v_pk_add_f32 v[136:137], v[108:109], v[136:137]
	v_pk_add_f32 v[138:139], v[110:111], v[138:139]
	ds_write_b128 v1, v[136:139] offset:12608
	v_pk_add_f32 v[140:141], v[112:113], v[140:141]
	v_pk_add_f32 v[142:143], v[114:115], v[142:143]
	ds_write_b128 v1, v[140:143] offset:12672
	v_pk_add_f32 v[144:145], v[104:105], v[144:145]
	v_pk_add_f32 v[146:147], v[106:107], v[146:147]
	ds_write_b128 v1, v[144:147] offset:25088
	v_pk_add_f32 v[148:149], v[108:109], v[148:149]
	v_pk_add_f32 v[150:151], v[110:111], v[150:151]
	ds_write_b128 v1, v[148:151] offset:25152
	v_pk_add_f32 v[152:153], v[112:113], v[152:153]
	v_pk_add_f32 v[154:155], v[114:115], v[154:155]
	ds_write_b128 v1, v[152:155] offset:25216
	v_pk_add_f32 v[156:157], v[104:105], v[156:157]
	v_pk_add_f32 v[158:159], v[106:107], v[158:159]
	ds_write_b128 v1, v[156:159] offset:37632
	v_pk_add_f32 v[160:161], v[108:109], v[160:161]
	v_pk_add_f32 v[162:163], v[110:111], v[162:163]
	ds_write_b128 v1, v[160:163] offset:37696
	v_pk_add_f32 v[164:165], v[112:113], v[164:165]
	v_pk_add_f32 v[166:167], v[114:115], v[166:167]
	ds_write_b128 v1, v[164:167] offset:37760
	v_or_b32_e32 v1, 0x200, v0
	v_mul_u32_u24_e32 v2, 0x556, v1
	v_lshrrev_b32_e32 v58, 16, v2
	v_or_b32_e32 v2, 0x400, v0
	v_mul_u32_u24_e32 v3, 0x556, v2
	v_lshrrev_b32_e32 v59, 16, v3
	v_mad_i32_i24 v60, v59, s5, v2
	v_or_b32_e32 v2, 0x600, v0
	v_mul_u32_u24_e32 v3, 0x556, v2
	v_lshrrev_b32_e32 v61, 16, v3
	v_mad_i32_i24 v62, v61, s5, v2
	v_or_b32_e32 v2, 0x800, v0
	v_mul_u32_u24_e32 v3, 0xaab, v2
	v_lshrrev_b32_e32 v63, 17, v3
	v_mad_i32_i24 v64, v63, s5, v2
	v_or_b32_e32 v2, 0xa00, v0
	v_mul_u32_u24_e32 v3, 0xaab, v2
	v_lshrrev_b32_e32 v65, 17, v3
	v_mad_i32_i24 v66, v65, s5, v2
	v_mul_i32_i24_sdwa v2, v67, s5 dst_sel:DWORD dst_unused:UNUSED_PAD src0_sel:WORD_1 src1_sel:DWORD
	v_or_b32_sdwa v3, s22, v67 dst_sel:DWORD dst_unused:UNUSED_PAD src0_sel:DWORD src1_sel:WORD_1
	v_mad_i64_i32 v[12:13], s[6:7], v3, s8, 0
	v_add_lshl_u32 v2, v2, v0, 2
	v_ashrrev_i32_e32 v3, 31, v2
	v_lshl_add_u64 v[4:5], v[12:13], 1, s[2:3]
	v_mad_i32_i24 v1, v58, s5, v1
	v_lshl_add_u64 v[2:3], v[2:3], 1, v[4:5]
	v_or_b32_e32 v4, s22, v58
	v_or_b32_e32 v6, s22, v59
	v_mad_i64_i32 v[14:15], s[6:7], v4, s8, 0
	v_lshlrev_b32_e32 v16, 2, v1
	v_mad_i64_i32 v[18:19], s[6:7], v6, s8, 0
	v_lshlrev_b32_e32 v20, 2, v60
	v_or_b32_e32 v8, s22, v61
	v_ashrrev_i32_e32 v17, 31, v16
	v_lshl_add_u64 v[4:5], v[14:15], 1, s[2:3]
	v_ashrrev_i32_e32 v21, 31, v20
	v_lshl_add_u64 v[6:7], v[18:19], 1, s[2:3]
	v_mad_i64_i32 v[22:23], s[6:7], v8, s8, 0
	v_lshlrev_b32_e32 v24, 2, v62
	s_waitcnt lgkmcnt(0)
	s_barrier
	v_lshl_add_u64 v[4:5], v[16:17], 1, v[4:5]
	v_lshl_add_u64 v[6:7], v[20:21], 1, v[6:7]
	v_ashrrev_i32_e32 v25, 31, v24
	v_lshl_add_u64 v[8:9], v[22:23], 1, s[2:3]
	global_load_dwordx2 v[2:3], v[2:3], off nt
	v_lshl_add_u64 v[8:9], v[24:25], 1, v[8:9]
	global_load_dwordx2 v[10:11], v[4:5], off nt
	global_load_dwordx2 v[26:27], v[6:7], off nt
	global_load_dwordx2 v[28:29], v[8:9], off nt
	v_or_b32_e32 v4, s22, v63
	v_or_b32_e32 v6, s22, v65
	v_mad_i64_i32 v[30:31], s[6:7], v4, s8, 0
	v_lshlrev_b32_e32 v32, 2, v64
	v_mad_i64_i32 v[34:35], s[6:7], v6, s8, 0
	v_lshlrev_b32_e32 v36, 2, v66
	v_ashrrev_i32_e32 v33, 31, v32
	v_lshl_add_u64 v[4:5], v[30:31], 1, s[2:3]
	v_ashrrev_i32_e32 v37, 31, v36
	v_lshl_add_u64 v[6:7], v[34:35], 1, s[2:3]
	v_lshl_add_u64 v[4:5], v[32:33], 1, v[4:5]
	v_lshl_add_u64 v[6:7], v[36:37], 1, v[6:7]
	global_load_dwordx2 v[4:5], v[4:5], off nt
	v_mov_b32_e32 v8, 48
	global_load_dwordx2 v[6:7], v[6:7], off nt
	v_mul_lo_u16_sdwa v8, v67, v8 dst_sel:DWORD dst_unused:UNUSED_PAD src0_sel:WORD_1 src1_sel:DWORD
	v_sub_u16_e32 v8, v0, v8
	v_lshl_add_u64 v[12:13], v[12:13], 2, s[0:1]
	s_waitcnt vmcnt(5)
	v_cvt_f32_f16_e32 v38, v2
	v_cvt_f32_f16_sdwa v39, v2 dst_sel:DWORD dst_unused:UNUSED_PAD src0_sel:WORD_1
	v_cvt_f32_f16_e32 v40, v3
	v_cvt_f32_f16_sdwa v41, v3 dst_sel:DWORD dst_unused:UNUSED_PAD src0_sel:WORD_1
	v_mul_u32_u24_sdwa v3, v67, s4 dst_sel:DWORD dst_unused:UNUSED_PAD src0_sel:WORD_1 src1_sel:DWORD
	v_lshlrev_b32_e32 v2, 4, v8
	v_add3_u32 v3, 0, v3, v2
	s_waitcnt vmcnt(4)
	v_cvt_f32_f16_e32 v42, v10
	v_cvt_f32_f16_sdwa v43, v10 dst_sel:DWORD dst_unused:UNUSED_PAD src0_sel:WORD_1
	v_cvt_f32_f16_e32 v44, v11
	v_cvt_f32_f16_sdwa v45, v11 dst_sel:DWORD dst_unused:UNUSED_PAD src0_sel:WORD_1
	s_waitcnt vmcnt(3)
	v_cvt_f32_f16_e32 v46, v26
	v_cvt_f32_f16_sdwa v47, v26 dst_sel:DWORD dst_unused:UNUSED_PAD src0_sel:WORD_1
	v_cvt_f32_f16_e32 v26, v27
	v_cvt_f32_f16_sdwa v27, v27 dst_sel:DWORD dst_unused:UNUSED_PAD src0_sel:WORD_1
	s_waitcnt vmcnt(2)
	v_cvt_f32_f16_e32 v48, v28
	v_cvt_f32_f16_sdwa v49, v28 dst_sel:DWORD dst_unused:UNUSED_PAD src0_sel:WORD_1
	s_waitcnt vmcnt(1)
	v_cvt_f32_f16_e32 v50, v4
	v_cvt_f32_f16_sdwa v51, v4 dst_sel:DWORD dst_unused:UNUSED_PAD src0_sel:WORD_1
	v_cvt_f32_f16_e32 v52, v5
	v_cvt_f32_f16_sdwa v53, v5 dst_sel:DWORD dst_unused:UNUSED_PAD src0_sel:WORD_1
	s_waitcnt vmcnt(0)
	v_cvt_f32_f16_e32 v54, v6
	v_cvt_f32_f16_sdwa v55, v6 dst_sel:DWORD dst_unused:UNUSED_PAD src0_sel:WORD_1
	v_cvt_f32_f16_e32 v56, v7
	v_cvt_f32_f16_sdwa v57, v7 dst_sel:DWORD dst_unused:UNUSED_PAD src0_sel:WORD_1
	ds_read_b128 v[4:7], v3
	v_mul_u32_u24_e32 v3, 0x310, v58
	v_lshlrev_b32_e32 v58, 4, v1
	v_add3_u32 v1, 0, v3, v58
	ds_read_b128 v[8:11], v1
	v_mov_b32_e32 v3, 0
	s_waitcnt lgkmcnt(1)
	v_pk_add_f32 v[6:7], v[6:7], v[40:41]
	v_pk_add_f32 v[4:5], v[4:5], v[38:39]
	v_lshl_add_u64 v[12:13], v[12:13], 0, v[2:3]
	global_store_dwordx4 v[12:13], v[4:7], off nt
	v_mul_u32_u24_e32 v1, 0x310, v59
	v_lshlrev_b32_e32 v59, 4, v60
	v_lshl_add_u64 v[6:7], v[14:15], 2, s[0:1]
	v_lshlrev_b64 v[4:5], 2, v[16:17]
	s_waitcnt lgkmcnt(0)
	v_pk_add_f32 v[10:11], v[10:11], v[44:45]
	v_pk_add_f32 v[8:9], v[8:9], v[42:43]
	v_lshl_add_u64 v[6:7], v[6:7], 0, v[4:5]
	v_add3_u32 v1, 0, v1, v59
	global_store_dwordx4 v[6:7], v[8:11], off nt
	ds_read_b128 v[6:9], v1
	v_mul_u32_u24_e32 v1, 0x310, v61
	v_lshlrev_b32_e32 v60, 4, v62
	v_add3_u32 v1, 0, v1, v60
	ds_read_b128 v[10:13], v1
	v_cvt_f32_f16_e32 v28, v29
	v_cvt_f32_f16_sdwa v29, v29 dst_sel:DWORD dst_unused:UNUSED_PAD src0_sel:WORD_1
	s_waitcnt lgkmcnt(1)
	v_pk_add_f32 v[16:17], v[8:9], v[26:27]
	v_pk_add_f32 v[14:15], v[6:7], v[46:47]
	v_lshl_add_u64 v[8:9], v[18:19], 2, s[0:1]
	v_lshlrev_b64 v[6:7], 2, v[20:21]
	v_lshl_add_u64 v[8:9], v[8:9], 0, v[6:7]
	global_store_dwordx4 v[8:9], v[14:17], off nt
	v_lshlrev_b64 v[8:9], 2, v[24:25]
	v_mul_u32_u24_e32 v1, 0x310, v63
	v_lshl_add_u64 v[14:15], v[22:23], 2, s[0:1]
	v_lshlrev_b32_e32 v61, 4, v64
	s_waitcnt lgkmcnt(0)
	v_pk_add_f32 v[12:13], v[12:13], v[28:29]
	v_pk_add_f32 v[10:11], v[10:11], v[48:49]
	v_lshl_add_u64 v[14:15], v[14:15], 0, v[8:9]
	v_add3_u32 v1, 0, v1, v61
	global_store_dwordx4 v[14:15], v[10:13], off nt
	ds_read_b128 v[10:13], v1
	v_mul_u32_u24_e32 v1, 0x310, v65
	v_lshlrev_b32_e32 v62, 4, v66
	v_add3_u32 v1, 0, v1, v62
	ds_read_b128 v[14:17], v1
	s_waitcnt lgkmcnt(1)
	v_pk_add_f32 v[20:21], v[12:13], v[52:53]
	v_pk_add_f32 v[18:19], v[10:11], v[50:51]
	v_lshl_add_u64 v[12:13], v[30:31], 2, s[0:1]
	v_lshlrev_b64 v[10:11], 2, v[32:33]
	v_lshl_add_u64 v[12:13], v[12:13], 0, v[10:11]
	global_store_dwordx4 v[12:13], v[18:21], off nt
	v_lshlrev_b64 v[12:13], 2, v[36:37]
	s_waitcnt lgkmcnt(0)
	v_pk_add_f32 v[16:17], v[16:17], v[56:57]
	v_lshl_add_u64 v[18:19], v[34:35], 2, s[0:1]
	v_pk_add_f32 v[14:15], v[14:15], v[54:55]
	v_lshl_add_u64 v[18:19], v[18:19], 0, v[12:13]
	v_or_b32_e32 v1, 0xc00, v0
	global_store_dwordx4 v[18:19], v[14:17], off nt
	s_nop 1
	v_mul_u32_u24_e32 v14, 0xaab, v1
	v_lshrrev_b32_e32 v57, 17, v14
	v_mul_i32_i24_e32 v14, 0xffffffd0, v57
	v_or_b32_e32 v15, s22, v57
	v_mad_i64_i32 v[22:23], s[4:5], v15, s8, 0
	v_add_lshl_u32 v14, v14, v1, 2
	v_ashrrev_i32_e32 v15, 31, v14
	v_lshl_add_u64 v[16:17], v[22:23], 1, s[2:3]
	v_or_b32_e32 v1, 0xe00, v0
	v_lshl_add_u64 v[14:15], v[14:15], 1, v[16:17]
	v_mul_u32_u24_e32 v16, 0xaab, v1
	v_lshrrev_b32_e32 v63, 17, v16
	v_mul_i32_i24_e32 v16, 0xffffffd0, v63
	v_add_u32_e32 v17, s22, v63
	v_mad_i64_i32 v[24:25], s[4:5], v17, s8, 0
	v_add_lshl_u32 v16, v16, v1, 2
	v_ashrrev_i32_e32 v17, 31, v16
	v_lshl_add_u64 v[18:19], v[24:25], 1, s[2:3]
	v_or_b32_e32 v1, 0x1000, v0
	v_lshl_add_u64 v[16:17], v[16:17], 1, v[18:19]
	v_mul_u32_u24_e32 v18, 0xaab, v1
	v_lshrrev_b32_e32 v64, 17, v18
	v_mul_i32_i24_e32 v18, 0xffffffd0, v64
	v_or_b32_e32 v19, s22, v64
	v_mad_i64_i32 v[26:27], s[4:5], v19, s8, 0
	v_add_lshl_u32 v18, v18, v1, 2
	v_ashrrev_i32_e32 v19, 31, v18
	v_lshl_add_u64 v[20:21], v[26:27], 1, s[2:3]
	v_or_b32_e32 v1, 0x1200, v0
	v_lshl_add_u64 v[18:19], v[18:19], 1, v[20:21]
	v_mul_u32_u24_e32 v20, 0xaab, v1
	v_lshrrev_b32_e32 v65, 17, v20
	v_mul_i32_i24_e32 v20, 0xffffffd0, v65
	v_or_b32_e32 v21, s22, v65
	v_mad_i64_i32 v[28:29], s[4:5], v21, s8, 0
	v_add_lshl_u32 v20, v20, v1, 2
	v_ashrrev_i32_e32 v21, 31, v20
	v_lshl_add_u64 v[30:31], v[28:29], 1, s[2:3]
	v_or_b32_e32 v1, 0x1400, v0
	v_lshl_add_u64 v[20:21], v[20:21], 1, v[30:31]
	global_load_dwordx2 v[30:31], v[14:15], off nt
	global_load_dwordx2 v[32:33], v[16:17], off nt
	global_load_dwordx2 v[34:35], v[18:19], off nt
	global_load_dwordx2 v[36:37], v[20:21], off nt
	v_mul_u32_u24_e32 v14, 0xaab, v1
	v_lshrrev_b32_e32 v66, 17, v14
	v_mul_i32_i24_e32 v14, 0xffffffd0, v66
	v_or_b32_e32 v15, s22, v66
	v_or_b32_e32 v0, 0x1600, v0
	v_mad_i64_i32 v[38:39], s[4:5], v15, s8, 0
	v_add_lshl_u32 v14, v14, v1, 2
	v_mul_u32_u24_e32 v1, 0xaab, v0
	v_ashrrev_i32_e32 v15, 31, v14
	v_lshl_add_u64 v[16:17], v[38:39], 1, s[2:3]
	v_lshrrev_b32_e32 v67, 17, v1
	v_lshl_add_u64 v[14:15], v[14:15], 1, v[16:17]
	v_mul_i32_i24_e32 v1, 0xffffffd0, v67
	v_add_u32_e32 v16, s22, v67
	v_mad_i64_i32 v[40:41], s[4:5], v16, s8, 0
	v_add_lshl_u32 v0, v1, v0, 2
	v_ashrrev_i32_e32 v1, 31, v0
	v_lshl_add_u64 v[16:17], v[40:41], 1, s[2:3]
	v_lshl_add_u64 v[0:1], v[0:1], 1, v[16:17]
	global_load_dwordx2 v[14:15], v[14:15], off nt
	s_waitcnt vmcnt(4)
	v_cvt_f32_f16_e32 v42, v30
	global_load_dwordx2 v[0:1], v[0:1], off nt
	v_cvt_f32_f16_sdwa v43, v30 dst_sel:DWORD dst_unused:UNUSED_PAD src0_sel:WORD_1
	v_cvt_f32_f16_e32 v30, v31
	v_cvt_f32_f16_sdwa v31, v31 dst_sel:DWORD dst_unused:UNUSED_PAD src0_sel:WORD_1
	s_waitcnt vmcnt(4)
	v_cvt_f32_f16_e32 v44, v32
	v_cvt_f32_f16_sdwa v45, v32 dst_sel:DWORD dst_unused:UNUSED_PAD src0_sel:WORD_1
	v_cvt_f32_f16_e32 v32, v33
	v_cvt_f32_f16_sdwa v33, v33 dst_sel:DWORD dst_unused:UNUSED_PAD src0_sel:WORD_1
	s_waitcnt vmcnt(3)
	v_cvt_f32_f16_e32 v46, v34
	v_cvt_f32_f16_sdwa v47, v34 dst_sel:DWORD dst_unused:UNUSED_PAD src0_sel:WORD_1
	v_cvt_f32_f16_e32 v34, v35
	v_cvt_f32_f16_sdwa v35, v35 dst_sel:DWORD dst_unused:UNUSED_PAD src0_sel:WORD_1
	s_waitcnt vmcnt(2)
	v_cvt_f32_f16_e32 v48, v36
	v_cvt_f32_f16_sdwa v49, v36 dst_sel:DWORD dst_unused:UNUSED_PAD src0_sel:WORD_1
	v_cvt_f32_f16_e32 v36, v37
	v_cvt_f32_f16_sdwa v37, v37 dst_sel:DWORD dst_unused:UNUSED_PAD src0_sel:WORD_1
	s_waitcnt vmcnt(1)
	v_cvt_f32_f16_e32 v50, v14
	v_cvt_f32_f16_sdwa v51, v14 dst_sel:DWORD dst_unused:UNUSED_PAD src0_sel:WORD_1
	v_cvt_f32_f16_e32 v52, v15
	v_cvt_f32_f16_sdwa v53, v15 dst_sel:DWORD dst_unused:UNUSED_PAD src0_sel:WORD_1
	s_waitcnt vmcnt(0)
	v_cvt_f32_f16_e32 v54, v0
	v_cvt_f32_f16_sdwa v55, v0 dst_sel:DWORD dst_unused:UNUSED_PAD src0_sel:WORD_1
	v_mul_u32_u24_e32 v0, 0x310, v57
	v_add3_u32 v0, 0, v0, v2
	ds_read_b128 v[14:17], v0
	v_mul_u32_u24_e32 v0, 0x310, v63
	v_add3_u32 v0, 0, v0, v58
	v_cvt_f32_f16_e32 v56, v1
	v_cvt_f32_f16_sdwa v57, v1 dst_sel:DWORD dst_unused:UNUSED_PAD src0_sel:WORD_1
	ds_read_b128 v[18:21], v0
	v_lshl_add_u64 v[0:1], v[22:23], 2, s[0:1]
	s_waitcnt lgkmcnt(1)
	v_pk_add_f32 v[16:17], v[16:17], v[30:31]
	v_pk_add_f32 v[14:15], v[14:15], v[42:43]
	v_lshl_add_u64 v[0:1], v[0:1], 0, v[2:3]
	global_store_dwordx4 v[0:1], v[14:17], off nt
	s_waitcnt lgkmcnt(0)
	v_pk_add_f32 v[0:1], v[18:19], v[44:45]
	v_pk_add_f32 v[2:3], v[20:21], v[32:33]
	v_lshl_add_u64 v[14:15], v[24:25], 2, s[0:1]
	v_lshl_add_u64 v[4:5], v[14:15], 0, v[4:5]
	v_mul_u32_u24_e32 v14, 0x310, v64
	v_add3_u32 v14, 0, v14, v59
	ds_read_b128 v[14:17], v14
	global_store_dwordx4 v[4:5], v[0:3], off nt
	v_lshl_add_u64 v[4:5], v[26:27], 2, s[0:1]
	v_lshl_add_u64 v[4:5], v[4:5], 0, v[6:7]
	v_mul_u32_u24_e32 v0, 0x310, v65
	v_add3_u32 v0, 0, v0, v60
	ds_read_b128 v[0:3], v0
	s_waitcnt lgkmcnt(1)
	v_pk_add_f32 v[14:15], v[14:15], v[46:47]
	v_pk_add_f32 v[16:17], v[16:17], v[34:35]
	global_store_dwordx4 v[4:5], v[14:17], off nt
	v_lshl_add_u64 v[4:5], v[28:29], 2, s[0:1]
	v_lshl_add_u64 v[8:9], v[4:5], 0, v[8:9]
	v_mul_u32_u24_e32 v4, 0x310, v66
	v_add3_u32 v4, 0, v4, v61
	ds_read_b128 v[4:7], v4
	s_waitcnt lgkmcnt(1)
	v_pk_add_f32 v[0:1], v[0:1], v[48:49]
	v_pk_add_f32 v[2:3], v[2:3], v[36:37]
	global_store_dwordx4 v[8:9], v[0:3], off nt
	v_lshl_add_u64 v[8:9], v[38:39], 2, s[0:1]
	s_waitcnt lgkmcnt(0)
	v_pk_add_f32 v[4:5], v[4:5], v[50:51]
	v_mul_u32_u24_e32 v0, 0x310, v67
	v_add3_u32 v0, 0, v0, v62
	ds_read_b128 v[0:3], v0
	v_pk_add_f32 v[6:7], v[6:7], v[52:53]
	v_lshl_add_u64 v[8:9], v[8:9], 0, v[10:11]
	global_store_dwordx4 v[8:9], v[4:7], off nt
	s_waitcnt lgkmcnt(0)
	v_pk_add_f32 v[0:1], v[0:1], v[54:55]
	v_lshl_add_u64 v[4:5], v[40:41], 2, s[0:1]
	v_pk_add_f32 v[2:3], v[2:3], v[56:57]
	v_lshl_add_u64 v[4:5], v[4:5], 0, v[12:13]
	global_store_dwordx4 v[4:5], v[0:3], off nt
	s_endpgm
	.p2align	8

	.amdhsa_kernel _Z6gemm_kILi1ELb1ELb1ELb0ELb0ELb1EEvPKtS1_ii7EpiArgs
		.amdhsa_group_segment_fixed_size 0
		.amdhsa_private_segment_fixed_size 0
		.amdhsa_kernarg_size 88
		.amdhsa_user_sgpr_count 2
		.amdhsa_user_sgpr_dispatch_ptr 0
		.amdhsa_user_sgpr_queue_ptr 0
		.amdhsa_user_sgpr_kernarg_segment_ptr 1
		.amdhsa_user_sgpr_dispatch_id 0
		.amdhsa_user_sgpr_kernarg_preload_length 0
		.amdhsa_user_sgpr_kernarg_preload_offset 0
		.amdhsa_user_sgpr_private_segment_size 0
		.amdhsa_uses_dynamic_stack 0
		.amdhsa_enable_private_segment 0
		.amdhsa_system_sgpr_workgroup_id_x 1
		.amdhsa_system_sgpr_workgroup_id_y 0
		.amdhsa_system_sgpr_workgroup_id_z 0
		.amdhsa_system_sgpr_workgroup_info 0
		.amdhsa_system_vgpr_workitem_id 0
		.amdhsa_next_free_vgpr 224
		.amdhsa_next_free_sgpr 70
		.amdhsa_accum_offset 224
		.amdhsa_reserve_vcc 0
		.amdhsa_float_round_mode_32 0
		.amdhsa_float_round_mode_16_64 0
		.amdhsa_float_denorm_mode_32 3
		.amdhsa_float_denorm_mode_16_64 3
		.amdhsa_dx10_clamp 1
		.amdhsa_ieee_mode 1
		.amdhsa_fp16_overflow 0
		.amdhsa_tg_split 0
		.amdhsa_exception_fp_ieee_invalid_op 0
		.amdhsa_exception_fp_denorm_src 0
		.amdhsa_exception_fp_ieee_div_zero 0
		.amdhsa_exception_fp_ieee_overflow 0
		.amdhsa_exception_fp_ieee_underflow 0
		.amdhsa_exception_fp_ieee_inexact 0
		.amdhsa_exception_int_div_zero 0
	.end_amdhsa_kernel

	.text
	.p2alignl 6, 3212836864
	.fill 256, 4, 3212836864
	.p2align	8

amdhsa.kernels:
  - .agpr_count:     0
    .args:
      - .offset:         0
        .size:           144
        .value_kind:     by_value
    .group_segment_fixed_size: 16640
    .kernarg_segment_align: 8
    .kernarg_segment_size: 144
    .language:       OpenCL C
    .language_version:
      - 2
      - 0
    .max_flat_workgroup_size: 256
    .name:           _Z8prep_ln18PrepArgs
    .private_segment_fixed_size: 0
    .sgpr_count:     18
    .sgpr_spill_count: 0
    .symbol:         _Z8prep_ln18PrepArgs.kd
    .uniform_work_group_size: 1
    .uses_dynamic_stack: false
    .vgpr_count:     61
    .vgpr_spill_count: 0
    .wavefront_size: 64
  - .agpr_count:     0
    .args:
      - .address_space:  global
        .offset:         0
        .size:           8
        .value_kind:     global_buffer
      - .address_space:  global
        .offset:         8
        .size:           8
        .value_kind:     global_buffer
      - .address_space:  global
        .offset:         16
        .size:           8
        .value_kind:     global_buffer
      - .address_space:  global
        .offset:         24
        .size:           8
        .value_kind:     global_buffer
      - .offset:         32
        .size:           144
        .value_kind:     by_value
    .group_segment_fixed_size: 0
    .kernarg_segment_align: 8
    .kernarg_segment_size: 176
    .language:       OpenCL C
    .language_version:
      - 2
      - 0
    .max_flat_workgroup_size: 256
    .name:           _Z10attn64_fwdPKtS0_S0_Pt8PrepArgs
    .private_segment_fixed_size: 0
    .sgpr_count:     42
    .sgpr_spill_count: 0
    .symbol:         _Z10attn64_fwdPKtS0_S0_Pt8PrepArgs.kd
    .uniform_work_group_size: 1
    .uses_dynamic_stack: false
    .vgpr_count:     221
    .vgpr_spill_count: 0
    .wavefront_size: 64
  - .agpr_count:     0
    .args:
      - .address_space:  global
        .offset:         0
        .size:           8
        .value_kind:     global_buffer
      - .address_space:  global
        .offset:         8
        .size:           8
        .value_kind:     global_buffer
      - .offset:         16
        .size:           4
        .value_kind:     by_value
      - .offset:         20
        .size:           4
        .value_kind:     by_value
      - .offset:         24
        .size:           64
        .value_kind:     by_value
    .group_segment_fixed_size: 0
    .kernarg_segment_align: 8
    .kernarg_segment_size: 88
    .language:       OpenCL C
    .language_version:
      - 2
      - 0
    .max_flat_workgroup_size: 256
    .name:           _Z8gemm2b_kILi2EEvPKtS1_ii7EpiArgs
    .private_segment_fixed_size: 0
    .sgpr_count:     75
    .sgpr_spill_count: 0
    .symbol:         _Z8gemm2b_kILi2EEvPKtS1_ii7EpiArgs.kd
    .uniform_work_group_size: 1
    .uses_dynamic_stack: false
    .vgpr_count:     182
    .vgpr_spill_count: 0
    .wavefront_size: 64
  - .agpr_count:     0
    .args:
      - .address_space:  global
        .offset:         0
        .size:           8
        .value_kind:     global_buffer
      - .address_space:  global
        .offset:         8
        .size:           8
        .value_kind:     global_buffer
      - .offset:         16
        .size:           4
        .value_kind:     by_value
      - .offset:         20
        .size:           4
        .value_kind:     by_value
      - .offset:         24
        .size:           64
        .value_kind:     by_value
    .group_segment_fixed_size: 0
    .kernarg_segment_align: 8
    .kernarg_segment_size: 88
    .language:       OpenCL C
    .language_version:
      - 2
      - 0
    .max_flat_workgroup_size: 256
    .name:           _Z8gemm2b_kILi0EEvPKtS1_ii7EpiArgs
    .private_segment_fixed_size: 0
    .sgpr_count:     85
    .sgpr_spill_count: 0
    .symbol:         _Z8gemm2b_kILi0EEvPKtS1_ii7EpiArgs.kd
    .uniform_work_group_size: 1
    .uses_dynamic_stack: false
    .vgpr_count:     186
    .vgpr_spill_count: 0
    .wavefront_size: 64
  - .agpr_count:     0
    .args:
      - .address_space:  global
        .offset:         0
        .size:           8
        .value_kind:     global_buffer
      - .address_space:  global
        .offset:         8
        .size:           8
        .value_kind:     global_buffer
      - .offset:         16
        .size:           4
        .value_kind:     by_value
      - .offset:         20
        .size:           4
        .value_kind:     by_value
      - .offset:         24
        .size:           64
        .value_kind:     by_value
    .group_segment_fixed_size: 0
    .kernarg_segment_align: 8
    .kernarg_segment_size: 88
    .language:       OpenCL C
    .language_version:
      - 2
      - 0
    .max_flat_workgroup_size: 512
    .name:           _Z6gemm_kILi1ELb1ELb0ELb1ELb1ELb0EEvPKtS1_ii7EpiArgs
    .private_segment_fixed_size: 0
    .sgpr_count:     61
    .sgpr_spill_count: 0
    .symbol:         _Z6gemm_kILi1ELb1ELb0ELb1ELb1ELb0EEvPKtS1_ii7EpiArgs.kd
    .uniform_work_group_size: 1
    .uses_dynamic_stack: false
    .vgpr_count:     116
    .vgpr_spill_count: 0
    .wavefront_size: 64
  - .agpr_count:     0
    .args:
      - .address_space:  global
        .offset:         0
        .size:           8
        .value_kind:     global_buffer
      - .address_space:  global
        .offset:         8
        .size:           8
        .value_kind:     global_buffer
      - .offset:         16
        .size:           4
        .value_kind:     by_value
      - .offset:         20
        .size:           4
        .value_kind:     by_value
      - .offset:         24
        .size:           64
        .value_kind:     by_value
    .group_segment_fixed_size: 0
    .kernarg_segment_align: 8
    .kernarg_segment_size: 88
    .language:       OpenCL C
    .language_version:
      - 2
      - 0
    .max_flat_workgroup_size: 512
    .name:           _Z6gemm_kILi1ELb1ELb1ELb0ELb0ELb1EEvPKtS1_ii7EpiArgs
    .private_segment_fixed_size: 0
    .sgpr_count:     76
    .sgpr_spill_count: 0
    .symbol:         _Z6gemm_kILi1ELb1ELb1ELb0ELb0ELb1EEvPKtS1_ii7EpiArgs.kd
    .uniform_work_group_size: 1
    .uses_dynamic_stack: false
    .vgpr_count:     224
    .vgpr_spill_count: 0
    .wavefront_size: 64
